# v82 + code placement: all nine GEMM K-loop tops aligned to 8 bytes (.p2align 3; the edits had left five of them at 4 mod 8)
# speedup vs baseline: 1.0035x; 1.0035x over previous
; #define PG8_STAGE_A(b, h, ptr, NX) do { if constexpr (Sched::GATHER) { unsigned gs_[2]; gs_[0] = ((NX) && last_) ? gN[h][0] : gA[h][0]; gs_[1] = ((NX) && last_) ? gN[h][1] : gA[h][1]; PG8_STAGE(PG8_SA(b, h), ptr, gs_); } \
;         else PG8_STAGE(PG8_SA(b, h), (ptr) + ((h) ? hstep : (size_t)0), voffA); } while (0)
; #define PG8_STAGE(bufoff, gbase, voff) do { _Pragma("unroll") for (int _i = 0; _i < 2; ++_i) \
;         __builtin_amdgcn_global_load_lds((const unsigned*)((const char*)(gbase) + (voff)[_i]), (PG8_LAS unsigned*)(lds + (bufoff) + ldsw + _i * 8192), 16, 0, 0); } while (0)
; #define PG8_LDA(dst, b, h) do { _Pragma("unroll") for (int m = 0; m < 4; ++m) _Pragma("unroll") for (int k = 0; k < 2; ++k) dst[m][k] = *(const PG8_LAS bf16x8*)(lds + PG8_SA(b, h) + aoff + m * 2048 + k * 1024); } while (0)
; #define PG8_WAIT_V(n) asm volatile("s_waitcnt vmcnt(" #n ")" ::: "memory")
; #define PG8_WAIT_L(n) asm volatile("s_waitcnt lgkmcnt(" #n ")" ::: "memory")
; #define PG8_BAR __builtin_amdgcn_s_barrier()
; template <class Epi, class Sched, bool ALIGN_EPI = false, bool SP2 = false>
; __device__ __forceinline__ void gemm_phase(PG8_LAS unsigned char* lds, const Gemm g, const Sched& S, const Epi& E, const bool skip_epi = false) {
;     ...
;         const char* nA = has_next ? (const char*)g.A + (size_t)nxt.pm * pmstepA + nxt.ko : cA; const char* nB = has_next ? (const char*)g.Bt + (size_t)nxt.pn * tstep + nxt.ko : cB;
;         for (int t = 0; t < nt; t += 2) {
;             const bool last = (t == nt - 2); last_ = last && has_next;
;             const char* a1 = cA + (size_t)(t + 1) * kstep;
;             const char* a2 = last ? nA : cA + (size_t)(t + 2) * kstep; const char* b2 = last ? nB : cB + (size_t)(t + 2) * kstep;
;             const char* a3 = a2 + kstep; const char* b3 = b2 + kstep;
;             if (last && has_next) S.a_ready(nxt);
;             if constexpr (SP2) {
;             PG8_LDB(B0, 0, 0); PG8_LDB(B1, 0, 1); PG8_SCHED; PG8_LDA(At, 0, 0); PG8_STAGE_A(1, 1, a1, false);
;             PG8_WAIT_V(8); PG8_WAIT_L(0); PG8_BAR; PG8_MMA(0, 0, At, B0); PG8_MMA(0, 1, At, B1); PG8_BAR; PG8_SCHED;
;             PG8_LDA(At, 0, 1); PG8_STAGE(PG8_SB(0, 0), b2, voffB); PG8_STAGE(PG8_SB(0, 1), b2 + hstep, voffB); PG8_STAGE_A(0, 0, a2, true);
;             PG8_WAIT_V(8); PG8_WAIT_L(0); PG8_BAR; PG8_MMA(1, 0, At, B0); PG8_MMA(1, 1, At, B1); PG8_BAR; PG8_SCHED;
.LBB0_252:
	s_ashr_i32 s17, s16, 31
	s_lshl_b64 s[18:19], s[16:17], 19
	s_add_u32 s18, s86, s18
	s_addc_u32 s19, s87, s19
	s_and_b64 s[20:21], s[4:5], exec
	s_cselect_b32 s17, s19, s25
	s_cselect_b32 s56, s18, s24
	s_ashr_i32 s15, s14, 31
	s_lshl_b64 s[20:21], s[14:15], 19
	v_readlane_b32 s28, v254, 36
	v_readlane_b32 s29, v254, 37
	s_add_u32 s20, s28, s20
	s_addc_u32 s21, s29, s21
	s_and_b64 s[28:29], s[4:5], exec
	s_cselect_b32 s15, s21, s27
	s_cselect_b32 s57, s20, s26
	s_add_u32 s24, s24, 0x40080
	s_addc_u32 s25, s25, 0
	s_add_u32 s58, s26, 0x100
	s_addc_u32 s59, s27, 0
	s_mov_b32 s60, -2
	s_waitcnt vmcnt(0)
	ds_read_b128 v[148:151], v170
	ds_read_b128 v[152:155], v170 offset:1024
	ds_read_b128 v[156:159], v170 offset:2048
	ds_read_b128 v[160:163], v170 offset:3072
	ds_read_b128 v[176:179], v171
	ds_read_b128 v[180:183], v171 offset:1024
	ds_read_b128 v[184:187], v171 offset:2048
	ds_read_b128 v[188:191], v171 offset:3072
	s_add_u32 s26, s24, 0xfffc0080
	s_addc_u32 s27, s25, -1
	s_cmp_eq_u32 s60, 12
	s_cselect_b32 s29, s17, s27
	s_cselect_b32 s28, s56, s26
	s_cselect_b32 s27, s15, s59
	s_cselect_b32 s26, s57, s58
	v_lshl_add_u64 v[164:165], s[24:25], 0, v[140:141]
	s_add_i32 m0, s23, 0xc000
	ds_read_b128 v[192:195], v172
	ds_read_b128 v[196:199], v172 offset:1024
	ds_read_b128 v[200:203], v172 offset:2048
	ds_read_b128 v[204:207], v172 offset:3072
	ds_read_b128 v[208:211], v172 offset:4096
	ds_read_b128 v[212:215], v172 offset:5120
	ds_read_b128 v[216:219], v172 offset:6144
	ds_read_b128 v[220:223], v172 offset:7168
	global_load_lds_dwordx4 v[164:165], off
	v_lshl_add_u64 v[164:165], s[24:25], 0, v[142:143]
	s_add_i32 m0, s23, 0xe000
	s_nop 0
	global_load_lds_dwordx4 v[164:165], off
	s_waitcnt vmcnt(8)
	s_waitcnt lgkmcnt(0)
	s_barrier
	s_setprio 3
	s_waitcnt lgkmcnt(0)
	v_mfma_f32_16x16x32_bf16 v[126:129], v[148:151], v[192:195], 0
	v_mfma_f32_16x16x32_bf16 v[122:125], v[156:159], v[192:195], 0
	v_mfma_f32_16x16x32_bf16 v[114:117], v[148:151], v[200:203], 0
	v_mfma_f32_16x16x32_bf16 v[106:109], v[156:159], v[200:203], 0
	v_mfma_f32_16x16x32_bf16 v[98:101], v[148:151], v[208:211], 0
	v_mfma_f32_16x16x32_bf16 v[90:93], v[156:159], v[208:211], 0
	v_mfma_f32_16x16x32_bf16 v[82:85], v[148:151], v[216:219], 0
	v_mfma_f32_16x16x32_bf16 v[74:77], v[156:159], v[216:219], 0
	v_mfma_f32_16x16x32_bf16 v[126:129], v[152:155], v[196:199], v[126:129]
	v_mfma_f32_16x16x32_bf16 v[122:125], v[160:163], v[196:199], v[122:125]
	v_mfma_f32_16x16x32_bf16 v[114:117], v[152:155], v[204:207], v[114:117]
	v_mfma_f32_16x16x32_bf16 v[106:109], v[160:163], v[204:207], v[106:109]
	v_mfma_f32_16x16x32_bf16 v[98:101], v[152:155], v[212:215], v[98:101]
	v_mfma_f32_16x16x32_bf16 v[90:93], v[160:163], v[212:215], v[90:93]
	v_mfma_f32_16x16x32_bf16 v[82:85], v[152:155], v[220:223], v[82:85]
	v_mfma_f32_16x16x32_bf16 v[74:77], v[160:163], v[220:223], v[74:77]
	s_setprio 0
	s_setprio 3
	v_mfma_f32_16x16x32_bf16 v[118:121], v[176:179], v[192:195], 0
	v_mfma_f32_16x16x32_bf16 v[110:113], v[184:187], v[192:195], 0
	v_mfma_f32_16x16x32_bf16 v[102:105], v[176:179], v[200:203], 0
	v_mfma_f32_16x16x32_bf16 v[94:97], v[184:187], v[200:203], 0
	v_mfma_f32_16x16x32_bf16 v[86:89], v[176:179], v[208:211], 0
	v_mfma_f32_16x16x32_bf16 v[78:81], v[184:187], v[208:211], 0
	v_mfma_f32_16x16x32_bf16 v[70:73], v[176:179], v[216:219], 0
	v_mfma_f32_16x16x32_bf16 v[66:69], v[184:187], v[216:219], 0
	v_mfma_f32_16x16x32_bf16 v[118:121], v[180:183], v[196:199], v[118:121]
	v_mfma_f32_16x16x32_bf16 v[110:113], v[188:191], v[196:199], v[110:113]
	v_mfma_f32_16x16x32_bf16 v[102:105], v[180:183], v[204:207], v[102:105]
	v_mfma_f32_16x16x32_bf16 v[94:97], v[188:191], v[204:207], v[94:97]
	v_mfma_f32_16x16x32_bf16 v[86:89], v[180:183], v[212:215], v[86:89]
	v_mfma_f32_16x16x32_bf16 v[78:81], v[188:191], v[212:215], v[78:81]
	v_mfma_f32_16x16x32_bf16 v[70:73], v[180:183], v[220:223], v[70:73]
	v_mfma_f32_16x16x32_bf16 v[66:69], v[188:191], v[220:223], v[66:69]
	s_setprio 0
	s_barrier
	s_add_i32 s61, s46, s2
	v_lshl_add_u64 v[164:165], s[26:27], 0, v[134:135]
	s_mov_b32 m0, s61
	ds_read_b128 v[192:195], v172 offset:16384
	ds_read_b128 v[196:199], v172 offset:17408
	ds_read_b128 v[200:203], v172 offset:18432
	ds_read_b128 v[204:207], v172 offset:19456
	ds_read_b128 v[208:211], v172 offset:20480
	ds_read_b128 v[212:215], v172 offset:21504
	ds_read_b128 v[216:219], v172 offset:22528
	ds_read_b128 v[220:223], v172 offset:23552
	global_load_lds_dwordx4 v[164:165], off
	s_add_i32 m0, s61, 0x2000
	s_add_u32 s62, s26, 0x40000
	v_lshl_add_u64 v[224:225], s[26:27], 0, v[130:131]
	s_addc_u32 s63, s27, 0
	s_add_i32 s61, s47, s2
	global_load_lds_dwordx4 v[224:225], off
	v_lshl_add_u64 v[226:227], s[62:63], 0, v[134:135]
	s_mov_b32 m0, s61
	v_lshl_add_u64 v[230:231], s[28:29], 0, v[132:133]
	global_load_lds_dwordx4 v[226:227], off
	v_lshl_add_u64 v[226:227], s[62:63], 0, v[130:131]
	s_add_i32 m0, s61, 0x2000
	s_nop 0
	global_load_lds_dwordx4 v[226:227], off
	v_lshl_add_u64 v[226:227], s[28:29], 0, v[136:137]
	s_mov_b32 m0, s23
	s_nop 0
	global_load_lds_dwordx4 v[226:227], off
	s_mov_b32 m0, s31
	s_nop 0
	global_load_lds_dwordx4 v[230:231], off
	s_waitcnt vmcnt(8)
	s_waitcnt lgkmcnt(0)
	s_barrier
; #define PG8_STAGE_A(b, h, ptr, NX) do { if constexpr (Sched::GATHER) { unsigned gs_[2]; gs_[0] = ((NX) && last_) ? gN[h][0] : gA[h][0]; gs_[1] = ((NX) && last_) ? gN[h][1] : gA[h][1]; PG8_STAGE(PG8_SA(b, h), ptr, gs_); } \
;         else PG8_STAGE(PG8_SA(b, h), (ptr) + ((h) ? hstep : (size_t)0), voffA); } while (0)
; #define PG8_STAGE(bufoff, gbase, voff) do { _Pragma("unroll") for (int _i = 0; _i < 2; ++_i) \
;         __builtin_amdgcn_global_load_lds((const unsigned*)((const char*)(gbase) + (voff)[_i]), (PG8_LAS unsigned*)(lds + (bufoff) + ldsw + _i * 8192), 16, 0, 0); } while (0)
; #define PG8_LDA(dst, b, h) do { _Pragma("unroll") for (int m = 0; m < 4; ++m) _Pragma("unroll") for (int k = 0; k < 2; ++k) dst[m][k] = *(const PG8_LAS bf16x8*)(lds + PG8_SA(b, h) + aoff + m * 2048 + k * 1024); } while (0)
; #define PG8_LDB(dst, b, h) do { _Pragma("unroll") for (int n = 0; n < 2; ++n) _Pragma("unroll") for (int k = 0; k < 2; ++k) dst[n][k] = *(const PG8_LAS bf16x8*)(lds + PG8_SB(b, h) + boff + n * 2048 + k * 1024); } while (0)
; #define PG8_MMA(ai, bj, At, Bt) do { __builtin_amdgcn_s_setprio(1); _Pragma("unroll") for (int m = 0; m < 4; ++m) _Pragma("unroll") for (int n = 0; n < 2; ++n) _Pragma("unroll") for (int k = 0; k < 2; ++k) \
;         acc[ai][bj][m][n] = __builtin_amdgcn_mfma_f32_16x16x32_bf16(Bt[n][k], At[m][k], acc[ai][bj][m][n], 0, 0, 0); __builtin_amdgcn_s_setprio(0); } while (0)
; #define PG8_WAIT_V(n) asm volatile("s_waitcnt vmcnt(" #n ")" ::: "memory")
; #define PG8_WAIT_L(n) asm volatile("s_waitcnt lgkmcnt(" #n ")" ::: "memory")
; #define PG8_BAR __builtin_amdgcn_s_barrier()
; #define PG8_SCHED __builtin_amdgcn_sched_barrier(0)
; template <class Epi, class Sched, bool ALIGN_EPI = false, bool SP2 = false>
; __device__ __forceinline__ void gemm_phase(PG8_LAS unsigned char* lds, const Gemm g, const Sched& S, const Epi& E, const bool skip_epi = false) {
;     ...
;             PG8_WAIT_V(8); PG8_WAIT_L(0); PG8_BAR; PG8_MMA(1, 0, At, B0); PG8_MMA(1, 1, At, B1); PG8_BAR; PG8_SCHED;
;             PG8_LDB(B0, 1, 0); PG8_LDB(B1, 1, 1); PG8_SCHED; PG8_LDA(At, 1, 0); PG8_STAGE_A(0, 1, a2, true);
;             PG8_WAIT_V(8); PG8_WAIT_L(0); PG8_BAR; PG8_MMA(0, 0, At, B0); PG8_MMA(0, 1, At, B1); PG8_BAR; PG8_SCHED;
;             PG8_LDA(At, 1, 1); PG8_STAGE(PG8_SB(1, 0), b3, voffB); PG8_STAGE(PG8_SB(1, 1), b3 + hstep, voffB); PG8_STAGE_A(1, 0, a3, true);
	s_setprio 3
	s_waitcnt lgkmcnt(0)
	v_mfma_f32_16x16x32_bf16 v[62:65], v[148:151], v[192:195], 0
	v_mfma_f32_16x16x32_bf16 v[58:61], v[156:159], v[192:195], 0
	v_mfma_f32_16x16x32_bf16 v[50:53], v[148:151], v[200:203], 0
	v_mfma_f32_16x16x32_bf16 v[42:45], v[156:159], v[200:203], 0
	v_mfma_f32_16x16x32_bf16 v[34:37], v[148:151], v[208:211], 0
	v_mfma_f32_16x16x32_bf16 v[26:29], v[156:159], v[208:211], 0
	v_mfma_f32_16x16x32_bf16 v[18:21], v[148:151], v[216:219], 0
	v_mfma_f32_16x16x32_bf16 v[10:13], v[156:159], v[216:219], 0
	v_mfma_f32_16x16x32_bf16 v[62:65], v[152:155], v[196:199], v[62:65]
	v_mfma_f32_16x16x32_bf16 v[58:61], v[160:163], v[196:199], v[58:61]
	v_mfma_f32_16x16x32_bf16 v[50:53], v[152:155], v[204:207], v[50:53]
	v_mfma_f32_16x16x32_bf16 v[42:45], v[160:163], v[204:207], v[42:45]
	v_mfma_f32_16x16x32_bf16 v[34:37], v[152:155], v[212:215], v[34:37]
	v_mfma_f32_16x16x32_bf16 v[26:29], v[160:163], v[212:215], v[26:29]
	v_mfma_f32_16x16x32_bf16 v[18:21], v[152:155], v[220:223], v[18:21]
	v_mfma_f32_16x16x32_bf16 v[10:13], v[160:163], v[220:223], v[10:13]
	s_setprio 0
	s_setprio 3
	v_mfma_f32_16x16x32_bf16 v[54:57], v[176:179], v[192:195], 0
	v_mfma_f32_16x16x32_bf16 v[46:49], v[184:187], v[192:195], 0
	v_mfma_f32_16x16x32_bf16 v[38:41], v[176:179], v[200:203], 0
	v_mfma_f32_16x16x32_bf16 v[30:33], v[184:187], v[200:203], 0
	v_mfma_f32_16x16x32_bf16 v[22:25], v[176:179], v[208:211], 0
	v_mfma_f32_16x16x32_bf16 v[14:17], v[184:187], v[208:211], 0
	v_mfma_f32_16x16x32_bf16 v[6:9], v[176:179], v[216:219], 0
	v_mfma_f32_16x16x32_bf16 v[2:5], v[184:187], v[216:219], 0
	v_mfma_f32_16x16x32_bf16 v[54:57], v[180:183], v[196:199], v[54:57]
	v_mfma_f32_16x16x32_bf16 v[46:49], v[188:191], v[196:199], v[46:49]
	v_mfma_f32_16x16x32_bf16 v[38:41], v[180:183], v[204:207], v[38:41]
	v_mfma_f32_16x16x32_bf16 v[30:33], v[188:191], v[204:207], v[30:33]
	v_mfma_f32_16x16x32_bf16 v[22:25], v[180:183], v[212:215], v[22:25]
	v_mfma_f32_16x16x32_bf16 v[14:17], v[188:191], v[212:215], v[14:17]
	v_mfma_f32_16x16x32_bf16 v[6:9], v[180:183], v[220:223], v[6:9]
	v_mfma_f32_16x16x32_bf16 v[2:5], v[188:191], v[220:223], v[2:5]
	s_setprio 0
	s_barrier
	s_add_i32 s61, 0, 0x18000
	s_add_i32 s62, 0, 0x1c000
	v_add_u32_e32 v160, s61, v1
	v_add_u32_e32 v188, s62, v1
	ds_read_b128 v[148:151], v160
	ds_read_b128 v[152:155], v160 offset:1024
	ds_read_b128 v[156:159], v160 offset:2048
	ds_read_b128 v[160:163], v160 offset:3072
	ds_read_b128 v[176:179], v188
	ds_read_b128 v[180:183], v188 offset:1024
	ds_read_b128 v[184:187], v188 offset:2048
	ds_read_b128 v[188:191], v188 offset:3072
	s_add_u32 s28, s28, 0x40000
	s_addc_u32 s29, s29, 0
	s_mov_b32 m0, s34
	v_lshl_add_u64 v[232:233], s[28:29], 0, v[136:137]
	ds_read_b128 v[192:195], v172 offset:32768
	ds_read_b128 v[196:199], v172 offset:33792
	ds_read_b128 v[200:203], v172 offset:34816
	ds_read_b128 v[204:207], v172 offset:35840
	ds_read_b128 v[208:211], v172 offset:36864
	ds_read_b128 v[212:215], v172 offset:37888
	ds_read_b128 v[216:219], v172 offset:38912
	ds_read_b128 v[220:223], v172 offset:39936
	global_load_lds_dwordx4 v[232:233], off
	v_lshl_add_u64 v[232:233], s[28:29], 0, v[132:133]
	s_mov_b32 m0, s35
	s_nop 0
	global_load_lds_dwordx4 v[232:233], off
	s_waitcnt vmcnt(8)
	s_waitcnt lgkmcnt(0)
	s_barrier
	s_setprio 3
	s_waitcnt lgkmcnt(0)
	v_mfma_f32_16x16x32_bf16 v[126:129], v[148:151], v[192:195], v[126:129]
	v_mfma_f32_16x16x32_bf16 v[122:125], v[156:159], v[192:195], v[122:125]
	v_mfma_f32_16x16x32_bf16 v[114:117], v[148:151], v[200:203], v[114:117]
	v_mfma_f32_16x16x32_bf16 v[106:109], v[156:159], v[200:203], v[106:109]
	v_mfma_f32_16x16x32_bf16 v[98:101], v[148:151], v[208:211], v[98:101]
	v_mfma_f32_16x16x32_bf16 v[90:93], v[156:159], v[208:211], v[90:93]
	v_mfma_f32_16x16x32_bf16 v[82:85], v[148:151], v[216:219], v[82:85]
	v_mfma_f32_16x16x32_bf16 v[74:77], v[156:159], v[216:219], v[74:77]
	v_mfma_f32_16x16x32_bf16 v[126:129], v[152:155], v[196:199], v[126:129]
	v_mfma_f32_16x16x32_bf16 v[122:125], v[160:163], v[196:199], v[122:125]
	v_mfma_f32_16x16x32_bf16 v[114:117], v[152:155], v[204:207], v[114:117]
	v_mfma_f32_16x16x32_bf16 v[106:109], v[160:163], v[204:207], v[106:109]
	v_mfma_f32_16x16x32_bf16 v[98:101], v[152:155], v[212:215], v[98:101]
	v_mfma_f32_16x16x32_bf16 v[90:93], v[160:163], v[212:215], v[90:93]
	v_mfma_f32_16x16x32_bf16 v[82:85], v[152:155], v[220:223], v[82:85]
	v_mfma_f32_16x16x32_bf16 v[74:77], v[160:163], v[220:223], v[74:77]
	s_setprio 0
	s_setprio 3
	v_mfma_f32_16x16x32_bf16 v[118:121], v[176:179], v[192:195], v[118:121]
	v_mfma_f32_16x16x32_bf16 v[110:113], v[184:187], v[192:195], v[110:113]
	v_mfma_f32_16x16x32_bf16 v[102:105], v[176:179], v[200:203], v[102:105]
	v_mfma_f32_16x16x32_bf16 v[94:97], v[184:187], v[200:203], v[94:97]
	v_mfma_f32_16x16x32_bf16 v[86:89], v[176:179], v[208:211], v[86:89]
	v_mfma_f32_16x16x32_bf16 v[78:81], v[184:187], v[208:211], v[78:81]
	v_mfma_f32_16x16x32_bf16 v[70:73], v[176:179], v[216:219], v[70:73]
	v_mfma_f32_16x16x32_bf16 v[66:69], v[184:187], v[216:219], v[66:69]
	v_mfma_f32_16x16x32_bf16 v[118:121], v[180:183], v[196:199], v[118:121]
	v_mfma_f32_16x16x32_bf16 v[110:113], v[188:191], v[196:199], v[110:113]
	v_mfma_f32_16x16x32_bf16 v[102:105], v[180:183], v[204:207], v[102:105]
	v_mfma_f32_16x16x32_bf16 v[94:97], v[188:191], v[204:207], v[94:97]
	v_mfma_f32_16x16x32_bf16 v[86:89], v[180:183], v[212:215], v[86:89]
	v_mfma_f32_16x16x32_bf16 v[78:81], v[188:191], v[212:215], v[78:81]
	v_mfma_f32_16x16x32_bf16 v[70:73], v[180:183], v[220:223], v[70:73]
	v_mfma_f32_16x16x32_bf16 v[66:69], v[188:191], v[220:223], v[66:69]
	s_setprio 0
	s_barrier
; #define PG8_STAGE_A(b, h, ptr, NX) do { if constexpr (Sched::GATHER) { unsigned gs_[2]; gs_[0] = ((NX) && last_) ? gN[h][0] : gA[h][0]; gs_[1] = ((NX) && last_) ? gN[h][1] : gA[h][1]; PG8_STAGE(PG8_SA(b, h), ptr, gs_); } \
;         else PG8_STAGE(PG8_SA(b, h), (ptr) + ((h) ? hstep : (size_t)0), voffA); } while (0)
; #define PG8_STAGE(bufoff, gbase, voff) do { _Pragma("unroll") for (int _i = 0; _i < 2; ++_i) \
;         __builtin_amdgcn_global_load_lds((const unsigned*)((const char*)(gbase) + (voff)[_i]), (PG8_LAS unsigned*)(lds + (bufoff) + ldsw + _i * 8192), 16, 0, 0); } while (0)
; #define PG8_LDA(dst, b, h) do { _Pragma("unroll") for (int m = 0; m < 4; ++m) _Pragma("unroll") for (int k = 0; k < 2; ++k) dst[m][k] = *(const PG8_LAS bf16x8*)(lds + PG8_SA(b, h) + aoff + m * 2048 + k * 1024); } while (0)
; #define PG8_MMA(ai, bj, At, Bt) do { __builtin_amdgcn_s_setprio(1); _Pragma("unroll") for (int m = 0; m < 4; ++m) _Pragma("unroll") for (int n = 0; n < 2; ++n) _Pragma("unroll") for (int k = 0; k < 2; ++k) \
;         acc[ai][bj][m][n] = __builtin_amdgcn_mfma_f32_16x16x32_bf16(Bt[n][k], At[m][k], acc[ai][bj][m][n], 0, 0, 0); __builtin_amdgcn_s_setprio(0); } while (0)
; #define PG8_WAIT_V(n) asm volatile("s_waitcnt vmcnt(" #n ")" ::: "memory")
; #define PG8_WAIT_L(n) asm volatile("s_waitcnt lgkmcnt(" #n ")" ::: "memory")
; #define PG8_BAR __builtin_amdgcn_s_barrier()
; #define PG8_SCHED __builtin_amdgcn_sched_barrier(0)
; template <class Epi, class Sched, bool ALIGN_EPI = false, bool SP2 = false>
; __device__ __forceinline__ void gemm_phase(PG8_LAS unsigned char* lds, const Gemm g, const Sched& S, const Epi& E, const bool skip_epi = false) {
;     ...
;             PG8_LDA(At, 1, 1); PG8_STAGE(PG8_SB(1, 0), b3, voffB); PG8_STAGE(PG8_SB(1, 1), b3 + hstep, voffB); PG8_STAGE_A(1, 0, a3, true);
;             PG8_WAIT_V(8); PG8_WAIT_L(0); PG8_BAR; PG8_MMA(1, 0, At, B0); PG8_MMA(1, 1, At, B1); PG8_BAR; PG8_SCHED;
	s_add_i32 s28, s61, s2
	v_lshl_add_u64 v[164:165], v[164:165], 0, s[10:11]
	s_mov_b32 m0, s28
	ds_read_b128 v[192:195], v172 offset:49152
	ds_read_b128 v[196:199], v172 offset:50176
	ds_read_b128 v[200:203], v172 offset:51200
	ds_read_b128 v[204:207], v172 offset:52224
	ds_read_b128 v[208:211], v172 offset:53248
	ds_read_b128 v[212:215], v172 offset:54272
	ds_read_b128 v[216:219], v172 offset:55296
	ds_read_b128 v[220:223], v172 offset:56320
	global_load_lds_dwordx4 v[164:165], off
	s_add_i32 m0, s28, 0x2000
	s_add_u32 s26, s26, 0x40080
	v_lshl_add_u64 v[164:165], v[224:225], 0, s[10:11]
	s_addc_u32 s27, s27, 0
	s_add_i32 s28, s62, s2
	global_load_lds_dwordx4 v[164:165], off
	v_lshl_add_u64 v[164:165], s[26:27], 0, v[134:135]
	s_mov_b32 m0, s28
	s_nop 0
	global_load_lds_dwordx4 v[164:165], off
	v_lshl_add_u64 v[164:165], s[26:27], 0, v[130:131]
	s_add_i32 m0, s28, 0x2000
	s_nop 0
	global_load_lds_dwordx4 v[164:165], off
	v_lshl_add_u64 v[164:165], v[226:227], 0, s[10:11]
	s_mov_b32 m0, s37
	s_nop 0
	global_load_lds_dwordx4 v[164:165], off
	v_lshl_add_u64 v[164:165], v[230:231], 0, s[10:11]
	s_mov_b32 m0, s38
	s_nop 0
	global_load_lds_dwordx4 v[164:165], off
	s_waitcnt vmcnt(8)
	s_waitcnt lgkmcnt(0)
	s_barrier
	s_setprio 3
	s_waitcnt lgkmcnt(0)
	v_mfma_f32_16x16x32_bf16 v[62:65], v[148:151], v[192:195], v[62:65]
	v_mfma_f32_16x16x32_bf16 v[58:61], v[156:159], v[192:195], v[58:61]
	v_mfma_f32_16x16x32_bf16 v[50:53], v[148:151], v[200:203], v[50:53]
	v_mfma_f32_16x16x32_bf16 v[42:45], v[156:159], v[200:203], v[42:45]
	v_mfma_f32_16x16x32_bf16 v[34:37], v[148:151], v[208:211], v[34:37]
	v_mfma_f32_16x16x32_bf16 v[26:29], v[156:159], v[208:211], v[26:29]
	v_mfma_f32_16x16x32_bf16 v[18:21], v[148:151], v[216:219], v[18:21]
	v_mfma_f32_16x16x32_bf16 v[10:13], v[156:159], v[216:219], v[10:13]
	v_mfma_f32_16x16x32_bf16 v[62:65], v[152:155], v[196:199], v[62:65]
	v_mfma_f32_16x16x32_bf16 v[58:61], v[160:163], v[196:199], v[58:61]
	v_mfma_f32_16x16x32_bf16 v[50:53], v[152:155], v[204:207], v[50:53]
	v_mfma_f32_16x16x32_bf16 v[42:45], v[160:163], v[204:207], v[42:45]
	v_mfma_f32_16x16x32_bf16 v[34:37], v[152:155], v[212:215], v[34:37]
	v_mfma_f32_16x16x32_bf16 v[26:29], v[160:163], v[212:215], v[26:29]
	v_mfma_f32_16x16x32_bf16 v[18:21], v[152:155], v[220:223], v[18:21]
	v_mfma_f32_16x16x32_bf16 v[10:13], v[160:163], v[220:223], v[10:13]
	s_setprio 0
	s_setprio 3
	v_mfma_f32_16x16x32_bf16 v[54:57], v[176:179], v[192:195], v[54:57]
	v_mfma_f32_16x16x32_bf16 v[46:49], v[184:187], v[192:195], v[46:49]
	v_mfma_f32_16x16x32_bf16 v[38:41], v[176:179], v[200:203], v[38:41]
	v_mfma_f32_16x16x32_bf16 v[30:33], v[184:187], v[200:203], v[30:33]
	v_mfma_f32_16x16x32_bf16 v[22:25], v[176:179], v[208:211], v[22:25]
	v_mfma_f32_16x16x32_bf16 v[14:17], v[184:187], v[208:211], v[14:17]
	v_mfma_f32_16x16x32_bf16 v[6:9], v[176:179], v[216:219], v[6:9]
	v_mfma_f32_16x16x32_bf16 v[2:5], v[184:187], v[216:219], v[2:5]
	v_mfma_f32_16x16x32_bf16 v[54:57], v[180:183], v[196:199], v[54:57]
	v_mfma_f32_16x16x32_bf16 v[46:49], v[188:191], v[196:199], v[46:49]
	v_mfma_f32_16x16x32_bf16 v[38:41], v[180:183], v[204:207], v[38:41]
	v_mfma_f32_16x16x32_bf16 v[30:33], v[188:191], v[204:207], v[30:33]
	v_mfma_f32_16x16x32_bf16 v[22:25], v[180:183], v[212:215], v[22:25]
	v_mfma_f32_16x16x32_bf16 v[14:17], v[188:191], v[212:215], v[14:17]
	v_mfma_f32_16x16x32_bf16 v[6:9], v[180:183], v[220:223], v[6:9]
	v_mfma_f32_16x16x32_bf16 v[2:5], v[188:191], v[220:223], v[2:5]
	s_setprio 0
	s_barrier
	s_add_i32 s60, s60, 2
	s_add_u32 s24, s24, 0x100
	s_addc_u32 s25, s25, 0
	s_add_u32 s58, s58, 0x100
	s_addc_u32 s59, s59, 0
	s_cmp_gt_u32 s60, 13
	.p2align	3

; #define PG8_STAGE_A(b, h, ptr, NX) do { if constexpr (Sched::GATHER) { unsigned gs_[2]; gs_[0] = ((NX) && last_) ? gN[h][0] : gA[h][0]; gs_[1] = ((NX) && last_) ? gN[h][1] : gA[h][1]; PG8_STAGE(PG8_SA(b, h), ptr, gs_); } \
;         else PG8_STAGE(PG8_SA(b, h), (ptr) + ((h) ? hstep : (size_t)0), voffA); } while (0)
; #define PG8_STAGE(bufoff, gbase, voff) do { _Pragma("unroll") for (int _i = 0; _i < 2; ++_i) \
;         __builtin_amdgcn_global_load_lds((const unsigned*)((const char*)(gbase) + (voff)[_i]), (PG8_LAS unsigned*)(lds + (bufoff) + ldsw + _i * 8192), 16, 0, 0); } while (0)
; #define PG8_LDA(dst, b, h) do { _Pragma("unroll") for (int m = 0; m < 4; ++m) _Pragma("unroll") for (int k = 0; k < 2; ++k) dst[m][k] = *(const PG8_LAS bf16x8*)(lds + PG8_SA(b, h) + aoff + m * 2048 + k * 1024); } while (0)
; #define PG8_WAIT_V(n) asm volatile("s_waitcnt vmcnt(" #n ")" ::: "memory")
; #define PG8_WAIT_L(n) asm volatile("s_waitcnt lgkmcnt(" #n ")" ::: "memory")
; #define PG8_BAR __builtin_amdgcn_s_barrier()
; template <class Epi, class Sched, bool ALIGN_EPI = false, bool SP2 = false>
; __device__ __forceinline__ void gemm_phase(PG8_LAS unsigned char* lds, const Gemm g, const Sched& S, const Epi& E, const bool skip_epi = false) {
;     ...
;         const char* nA = has_next ? (const char*)g.A + (size_t)nxt.pm * pmstepA + nxt.ko : cA; const char* nB = has_next ? (const char*)g.Bt + (size_t)nxt.pn * tstep + nxt.ko : cB;
;         for (int t = 0; t < nt; t += 2) {
;             const bool last = (t == nt - 2); last_ = last && has_next;
;             const char* a1 = cA + (size_t)(t + 1) * kstep;
;             const char* a2 = last ? nA : cA + (size_t)(t + 2) * kstep; const char* b2 = last ? nB : cB + (size_t)(t + 2) * kstep;
;             const char* a3 = a2 + kstep; const char* b3 = b2 + kstep;
;             if (last && has_next) S.a_ready(nxt);
;             if constexpr (SP2) {
;             PG8_LDB(B0, 0, 0); PG8_LDB(B1, 0, 1); PG8_SCHED; PG8_LDA(At, 0, 0); PG8_STAGE_A(1, 1, a1, false);
;             PG8_WAIT_V(8); PG8_WAIT_L(0); PG8_BAR; PG8_MMA(0, 0, At, B0); PG8_MMA(0, 1, At, B1); PG8_BAR; PG8_SCHED;
;             PG8_LDA(At, 0, 1); PG8_STAGE(PG8_SB(0, 0), b2, voffB); PG8_STAGE(PG8_SB(0, 1), b2 + hstep, voffB); PG8_STAGE_A(0, 0, a2, true);
;             PG8_WAIT_V(8); PG8_WAIT_L(0); PG8_BAR; PG8_MMA(1, 0, At, B0); PG8_MMA(1, 1, At, B1); PG8_BAR; PG8_SCHED;
.LBB0_633:
	s_ashr_i32 s19, s18, 31
	s_lshl_b64 s[20:21], s[18:19], 19
	s_add_u32 s20, s46, s20
	s_addc_u32 s21, s47, s21
	s_and_b64 s[22:23], s[6:7], exec
	s_cselect_b32 s19, s21, s27
	s_cselect_b32 s25, s20, s26
	s_ashr_i32 s17, s16, 31
	s_lshl_b64 s[22:23], s[16:17], 19
	v_readlane_b32 s17, v254, 40
	s_add_u32 s22, s17, s22
	v_readlane_b32 s17, v254, 41
	s_addc_u32 s23, s17, s23
	s_and_b64 s[30:31], s[6:7], exec
	s_cselect_b32 s17, s23, s29
	s_cselect_b32 s60, s22, s28
	s_add_u32 s26, s26, 0x40080
	s_addc_u32 s27, s27, 0
	s_add_u32 s61, s28, 0x100
	s_addc_u32 s62, s29, 0
	s_mov_b32 s63, -2
	s_waitcnt lgkmcnt(0)
	ds_read_b128 v[98:101], v234
	ds_read_b128 v[110:113], v234 offset:1024
	ds_read_b128 v[122:125], v234 offset:2048
	ds_read_b128 v[126:129], v234 offset:3072
	ds_read_b128 v[138:141], v235
	ds_read_b128 v[142:145], v235 offset:1024
	ds_read_b128 v[146:149], v235 offset:2048
	ds_read_b128 v[150:153], v235 offset:3072
	s_add_u32 s28, s26, 0xfffc0080
	s_addc_u32 s29, s27, -1
	s_cmp_eq_u32 s63, 12
	s_cselect_b32 s31, s19, s29
	s_cselect_b32 s30, s25, s28
	s_cselect_b32 s29, s17, s62
	s_cselect_b32 s28, s60, s61
	v_lshl_add_u64 v[210:211], s[26:27], 0, v[198:199]
	s_add_i32 m0, s3, 0xc000
	ds_read_b128 v[154:157], v236
	ds_read_b128 v[166:169], v236 offset:1024
	ds_read_b128 v[170:173], v236 offset:2048
	ds_read_b128 v[174:177], v236 offset:3072
	ds_read_b128 v[178:181], v236 offset:4096
	ds_read_b128 v[182:185], v236 offset:5120
	ds_read_b128 v[186:189], v236 offset:6144
	ds_read_b128 v[206:209], v236 offset:7168
	global_load_lds_dwordx4 v[210:211], off
	v_lshl_add_u64 v[210:211], s[26:27], 0, v[200:201]
	s_add_i32 m0, s3, 0xe000
	s_nop 0
	global_load_lds_dwordx4 v[210:211], off
	s_waitcnt vmcnt(8)
	s_waitcnt lgkmcnt(0)
	s_barrier
	s_setprio 3
	s_waitcnt lgkmcnt(0)
	v_mfma_f32_16x16x32_bf16 v[162:165], v[98:101], v[154:157], 0
	v_mfma_f32_16x16x32_bf16 v[158:161], v[122:125], v[154:157], 0
	v_mfma_f32_16x16x32_bf16 v[118:121], v[98:101], v[170:173], 0
	v_mfma_f32_16x16x32_bf16 v[114:117], v[122:125], v[170:173], 0
	v_mfma_f32_16x16x32_bf16 v[94:97], v[98:101], v[178:181], 0
	v_mfma_f32_16x16x32_bf16 v[90:93], v[122:125], v[178:181], 0
	v_mfma_f32_16x16x32_bf16 v[78:81], v[98:101], v[186:189], 0
	v_mfma_f32_16x16x32_bf16 v[74:77], v[122:125], v[186:189], 0
	v_mfma_f32_16x16x32_bf16 v[162:165], v[110:113], v[166:169], v[162:165]
	v_mfma_f32_16x16x32_bf16 v[158:161], v[126:129], v[166:169], v[158:161]
	v_mfma_f32_16x16x32_bf16 v[118:121], v[110:113], v[174:177], v[118:121]
	v_mfma_f32_16x16x32_bf16 v[114:117], v[126:129], v[174:177], v[114:117]
	v_mfma_f32_16x16x32_bf16 v[94:97], v[110:113], v[182:185], v[94:97]
	v_mfma_f32_16x16x32_bf16 v[90:93], v[126:129], v[182:185], v[90:93]
	v_mfma_f32_16x16x32_bf16 v[78:81], v[110:113], v[206:209], v[78:81]
	v_mfma_f32_16x16x32_bf16 v[74:77], v[126:129], v[206:209], v[74:77]
	s_setprio 0
	s_setprio 3
	v_mfma_f32_16x16x32_bf16 v[134:137], v[138:141], v[154:157], 0
	v_mfma_f32_16x16x32_bf16 v[130:133], v[146:149], v[154:157], 0
	v_mfma_f32_16x16x32_bf16 v[106:109], v[138:141], v[170:173], 0
	v_mfma_f32_16x16x32_bf16 v[102:105], v[146:149], v[170:173], 0
	v_mfma_f32_16x16x32_bf16 v[86:89], v[138:141], v[178:181], 0
	v_mfma_f32_16x16x32_bf16 v[82:85], v[146:149], v[178:181], 0
	v_mfma_f32_16x16x32_bf16 v[70:73], v[138:141], v[186:189], 0
	v_mfma_f32_16x16x32_bf16 v[66:69], v[146:149], v[186:189], 0
	v_mfma_f32_16x16x32_bf16 v[134:137], v[142:145], v[166:169], v[134:137]
	v_mfma_f32_16x16x32_bf16 v[130:133], v[150:153], v[166:169], v[130:133]
	v_mfma_f32_16x16x32_bf16 v[106:109], v[142:145], v[174:177], v[106:109]
	v_mfma_f32_16x16x32_bf16 v[102:105], v[150:153], v[174:177], v[102:105]
	v_mfma_f32_16x16x32_bf16 v[86:89], v[142:145], v[182:185], v[86:89]
	v_mfma_f32_16x16x32_bf16 v[82:85], v[150:153], v[182:185], v[82:85]
	v_mfma_f32_16x16x32_bf16 v[70:73], v[142:145], v[206:209], v[70:73]
	v_mfma_f32_16x16x32_bf16 v[66:69], v[150:153], v[206:209], v[66:69]
	s_setprio 0
	s_barrier
	s_add_i32 s64, s57, s2
	v_lshl_add_u64 v[210:211], s[28:29], 0, v[192:193]
	s_mov_b32 m0, s64
	ds_read_b128 v[154:157], v236 offset:16384
	ds_read_b128 v[166:169], v236 offset:17408
	ds_read_b128 v[170:173], v236 offset:18432
	ds_read_b128 v[174:177], v236 offset:19456
	ds_read_b128 v[178:181], v236 offset:20480
	ds_read_b128 v[182:185], v236 offset:21504
	ds_read_b128 v[186:189], v236 offset:22528
	ds_read_b128 v[206:209], v236 offset:23552
	global_load_lds_dwordx4 v[210:211], off
	s_add_i32 m0, s64, 0x2000
	s_add_u32 s64, s28, 0x40000
	v_lshl_add_u64 v[212:213], s[28:29], 0, v[196:197]
	s_addc_u32 s65, s29, 0
	s_add_i32 s66, s58, s2
	global_load_lds_dwordx4 v[212:213], off
	v_lshl_add_u64 v[214:215], s[64:65], 0, v[192:193]
	s_mov_b32 m0, s66
	v_lshl_add_u64 v[216:217], s[30:31], 0, v[194:195]
	global_load_lds_dwordx4 v[214:215], off
	v_lshl_add_u64 v[214:215], s[64:65], 0, v[196:197]
	s_add_i32 m0, s66, 0x2000
	s_nop 0
	global_load_lds_dwordx4 v[214:215], off
	v_lshl_add_u64 v[214:215], s[30:31], 0, v[190:191]
	s_mov_b32 m0, s3
	s_nop 0
	global_load_lds_dwordx4 v[214:215], off
	s_mov_b32 m0, s34
	s_nop 0
	global_load_lds_dwordx4 v[216:217], off
	s_waitcnt vmcnt(8)
	s_waitcnt lgkmcnt(0)
	s_barrier
; #define PG8_STAGE_A(b, h, ptr, NX) do { if constexpr (Sched::GATHER) { unsigned gs_[2]; gs_[0] = ((NX) && last_) ? gN[h][0] : gA[h][0]; gs_[1] = ((NX) && last_) ? gN[h][1] : gA[h][1]; PG8_STAGE(PG8_SA(b, h), ptr, gs_); } \
;         else PG8_STAGE(PG8_SA(b, h), (ptr) + ((h) ? hstep : (size_t)0), voffA); } while (0)
; #define PG8_STAGE(bufoff, gbase, voff) do { _Pragma("unroll") for (int _i = 0; _i < 2; ++_i) \
;         __builtin_amdgcn_global_load_lds((const unsigned*)((const char*)(gbase) + (voff)[_i]), (PG8_LAS unsigned*)(lds + (bufoff) + ldsw + _i * 8192), 16, 0, 0); } while (0)
; #define PG8_LDA(dst, b, h) do { _Pragma("unroll") for (int m = 0; m < 4; ++m) _Pragma("unroll") for (int k = 0; k < 2; ++k) dst[m][k] = *(const PG8_LAS bf16x8*)(lds + PG8_SA(b, h) + aoff + m * 2048 + k * 1024); } while (0)
; #define PG8_LDB(dst, b, h) do { _Pragma("unroll") for (int n = 0; n < 2; ++n) _Pragma("unroll") for (int k = 0; k < 2; ++k) dst[n][k] = *(const PG8_LAS bf16x8*)(lds + PG8_SB(b, h) + boff + n * 2048 + k * 1024); } while (0)
; #define PG8_MMA(ai, bj, At, Bt) do { __builtin_amdgcn_s_setprio(1); _Pragma("unroll") for (int m = 0; m < 4; ++m) _Pragma("unroll") for (int n = 0; n < 2; ++n) _Pragma("unroll") for (int k = 0; k < 2; ++k) \
;         acc[ai][bj][m][n] = __builtin_amdgcn_mfma_f32_16x16x32_bf16(Bt[n][k], At[m][k], acc[ai][bj][m][n], 0, 0, 0); __builtin_amdgcn_s_setprio(0); } while (0)
; #define PG8_WAIT_V(n) asm volatile("s_waitcnt vmcnt(" #n ")" ::: "memory")
; #define PG8_WAIT_L(n) asm volatile("s_waitcnt lgkmcnt(" #n ")" ::: "memory")
; #define PG8_BAR __builtin_amdgcn_s_barrier()
; #define PG8_SCHED __builtin_amdgcn_sched_barrier(0)
; template <class Epi, class Sched, bool ALIGN_EPI = false, bool SP2 = false>
; __device__ __forceinline__ void gemm_phase(PG8_LAS unsigned char* lds, const Gemm g, const Sched& S, const Epi& E, const bool skip_epi = false) {
;     ...
;             PG8_WAIT_V(8); PG8_WAIT_L(0); PG8_BAR; PG8_MMA(1, 0, At, B0); PG8_MMA(1, 1, At, B1); PG8_BAR; PG8_SCHED;
;             PG8_LDB(B0, 1, 0); PG8_LDB(B1, 1, 1); PG8_SCHED; PG8_LDA(At, 1, 0); PG8_STAGE_A(0, 1, a2, true);
;             PG8_WAIT_V(8); PG8_WAIT_L(0); PG8_BAR; PG8_MMA(0, 0, At, B0); PG8_MMA(0, 1, At, B1); PG8_BAR; PG8_SCHED;
;             PG8_LDA(At, 1, 1); PG8_STAGE(PG8_SB(1, 0), b3, voffB); PG8_STAGE(PG8_SB(1, 1), b3 + hstep, voffB); PG8_STAGE_A(1, 0, a3, true);
	s_setprio 3
	s_waitcnt lgkmcnt(0)
	v_mfma_f32_16x16x32_bf16 v[62:65], v[98:101], v[154:157], 0
	v_mfma_f32_16x16x32_bf16 v[58:61], v[122:125], v[154:157], 0
	v_mfma_f32_16x16x32_bf16 v[46:49], v[98:101], v[170:173], 0
	v_mfma_f32_16x16x32_bf16 v[42:45], v[122:125], v[170:173], 0
	v_mfma_f32_16x16x32_bf16 v[30:33], v[98:101], v[178:181], 0
	v_mfma_f32_16x16x32_bf16 v[26:29], v[122:125], v[178:181], 0
	v_mfma_f32_16x16x32_bf16 v[14:17], v[98:101], v[186:189], 0
	v_mfma_f32_16x16x32_bf16 v[10:13], v[122:125], v[186:189], 0
	v_mfma_f32_16x16x32_bf16 v[62:65], v[110:113], v[166:169], v[62:65]
	v_mfma_f32_16x16x32_bf16 v[58:61], v[126:129], v[166:169], v[58:61]
	v_mfma_f32_16x16x32_bf16 v[46:49], v[110:113], v[174:177], v[46:49]
	v_mfma_f32_16x16x32_bf16 v[42:45], v[126:129], v[174:177], v[42:45]
	v_mfma_f32_16x16x32_bf16 v[30:33], v[110:113], v[182:185], v[30:33]
	v_mfma_f32_16x16x32_bf16 v[26:29], v[126:129], v[182:185], v[26:29]
	v_mfma_f32_16x16x32_bf16 v[14:17], v[110:113], v[206:209], v[14:17]
	v_mfma_f32_16x16x32_bf16 v[10:13], v[126:129], v[206:209], v[10:13]
	s_setprio 0
	s_setprio 3
	v_mfma_f32_16x16x32_bf16 v[54:57], v[138:141], v[154:157], 0
	v_mfma_f32_16x16x32_bf16 v[50:53], v[146:149], v[154:157], 0
	v_mfma_f32_16x16x32_bf16 v[38:41], v[138:141], v[170:173], 0
	v_mfma_f32_16x16x32_bf16 v[34:37], v[146:149], v[170:173], 0
	v_mfma_f32_16x16x32_bf16 v[22:25], v[138:141], v[178:181], 0
	v_mfma_f32_16x16x32_bf16 v[18:21], v[146:149], v[178:181], 0
	v_mfma_f32_16x16x32_bf16 v[6:9], v[138:141], v[186:189], 0
	v_mfma_f32_16x16x32_bf16 v[2:5], v[146:149], v[186:189], 0
	v_mfma_f32_16x16x32_bf16 v[54:57], v[142:145], v[166:169], v[54:57]
	v_mfma_f32_16x16x32_bf16 v[50:53], v[150:153], v[166:169], v[50:53]
	v_mfma_f32_16x16x32_bf16 v[38:41], v[142:145], v[174:177], v[38:41]
	v_mfma_f32_16x16x32_bf16 v[34:37], v[150:153], v[174:177], v[34:37]
	v_mfma_f32_16x16x32_bf16 v[22:25], v[142:145], v[182:185], v[22:25]
	v_mfma_f32_16x16x32_bf16 v[18:21], v[150:153], v[182:185], v[18:21]
	v_mfma_f32_16x16x32_bf16 v[6:9], v[142:145], v[206:209], v[6:9]
	v_mfma_f32_16x16x32_bf16 v[2:5], v[150:153], v[206:209], v[2:5]
	s_setprio 0
	s_barrier
	s_add_i32 s64, 0, 0x18000
	s_add_i32 s65, 0, 0x1c000
	v_add_u32_e32 v126, s64, v229
	v_add_u32_e32 v150, s65, v229
	ds_read_b128 v[98:101], v126
	ds_read_b128 v[110:113], v126 offset:1024
	ds_read_b128 v[122:125], v126 offset:2048
	ds_read_b128 v[126:129], v126 offset:3072
	ds_read_b128 v[138:141], v150
	ds_read_b128 v[142:145], v150 offset:1024
	ds_read_b128 v[146:149], v150 offset:2048
	ds_read_b128 v[150:153], v150 offset:3072
	s_add_u32 s30, s30, 0x40000
	s_addc_u32 s31, s31, 0
	s_mov_b32 m0, s35
	v_lshl_add_u64 v[218:219], s[30:31], 0, v[190:191]
	ds_read_b128 v[154:157], v236 offset:32768
	ds_read_b128 v[166:169], v236 offset:33792
	ds_read_b128 v[170:173], v236 offset:34816
	ds_read_b128 v[174:177], v236 offset:35840
	ds_read_b128 v[178:181], v236 offset:36864
	ds_read_b128 v[182:185], v236 offset:37888
	ds_read_b128 v[186:189], v236 offset:38912
	ds_read_b128 v[206:209], v236 offset:39936
	global_load_lds_dwordx4 v[218:219], off
	v_lshl_add_u64 v[218:219], s[30:31], 0, v[194:195]
	s_mov_b32 m0, s36
	s_nop 0
	global_load_lds_dwordx4 v[218:219], off
	s_waitcnt vmcnt(8)
	s_waitcnt lgkmcnt(0)
	s_barrier
	s_setprio 3
	s_waitcnt lgkmcnt(0)
	v_mfma_f32_16x16x32_bf16 v[162:165], v[98:101], v[154:157], v[162:165]
	v_mfma_f32_16x16x32_bf16 v[158:161], v[122:125], v[154:157], v[158:161]
	v_mfma_f32_16x16x32_bf16 v[118:121], v[98:101], v[170:173], v[118:121]
	v_mfma_f32_16x16x32_bf16 v[114:117], v[122:125], v[170:173], v[114:117]
	v_mfma_f32_16x16x32_bf16 v[94:97], v[98:101], v[178:181], v[94:97]
	v_mfma_f32_16x16x32_bf16 v[90:93], v[122:125], v[178:181], v[90:93]
	v_mfma_f32_16x16x32_bf16 v[78:81], v[98:101], v[186:189], v[78:81]
	v_mfma_f32_16x16x32_bf16 v[74:77], v[122:125], v[186:189], v[74:77]
	v_mfma_f32_16x16x32_bf16 v[162:165], v[110:113], v[166:169], v[162:165]
	v_mfma_f32_16x16x32_bf16 v[158:161], v[126:129], v[166:169], v[158:161]
	v_mfma_f32_16x16x32_bf16 v[118:121], v[110:113], v[174:177], v[118:121]
	v_mfma_f32_16x16x32_bf16 v[114:117], v[126:129], v[174:177], v[114:117]
	v_mfma_f32_16x16x32_bf16 v[94:97], v[110:113], v[182:185], v[94:97]
	v_mfma_f32_16x16x32_bf16 v[90:93], v[126:129], v[182:185], v[90:93]
	v_mfma_f32_16x16x32_bf16 v[78:81], v[110:113], v[206:209], v[78:81]
	v_mfma_f32_16x16x32_bf16 v[74:77], v[126:129], v[206:209], v[74:77]
	s_setprio 0
	s_setprio 3
	v_mfma_f32_16x16x32_bf16 v[134:137], v[138:141], v[154:157], v[134:137]
	v_mfma_f32_16x16x32_bf16 v[130:133], v[146:149], v[154:157], v[130:133]
	v_mfma_f32_16x16x32_bf16 v[106:109], v[138:141], v[170:173], v[106:109]
	v_mfma_f32_16x16x32_bf16 v[102:105], v[146:149], v[170:173], v[102:105]
	v_mfma_f32_16x16x32_bf16 v[86:89], v[138:141], v[178:181], v[86:89]
	v_mfma_f32_16x16x32_bf16 v[82:85], v[146:149], v[178:181], v[82:85]
	v_mfma_f32_16x16x32_bf16 v[70:73], v[138:141], v[186:189], v[70:73]
	v_mfma_f32_16x16x32_bf16 v[66:69], v[146:149], v[186:189], v[66:69]
	v_mfma_f32_16x16x32_bf16 v[134:137], v[142:145], v[166:169], v[134:137]
	v_mfma_f32_16x16x32_bf16 v[130:133], v[150:153], v[166:169], v[130:133]
	v_mfma_f32_16x16x32_bf16 v[106:109], v[142:145], v[174:177], v[106:109]
	v_mfma_f32_16x16x32_bf16 v[102:105], v[150:153], v[174:177], v[102:105]
	v_mfma_f32_16x16x32_bf16 v[86:89], v[142:145], v[182:185], v[86:89]
	v_mfma_f32_16x16x32_bf16 v[82:85], v[150:153], v[182:185], v[82:85]
	v_mfma_f32_16x16x32_bf16 v[70:73], v[142:145], v[206:209], v[70:73]
	v_mfma_f32_16x16x32_bf16 v[66:69], v[150:153], v[206:209], v[66:69]
	s_setprio 0
	s_barrier
; #define PG8_STAGE_A(b, h, ptr, NX) do { if constexpr (Sched::GATHER) { unsigned gs_[2]; gs_[0] = ((NX) && last_) ? gN[h][0] : gA[h][0]; gs_[1] = ((NX) && last_) ? gN[h][1] : gA[h][1]; PG8_STAGE(PG8_SA(b, h), ptr, gs_); } \
;         else PG8_STAGE(PG8_SA(b, h), (ptr) + ((h) ? hstep : (size_t)0), voffA); } while (0)
; #define PG8_STAGE(bufoff, gbase, voff) do { _Pragma("unroll") for (int _i = 0; _i < 2; ++_i) \
;         __builtin_amdgcn_global_load_lds((const unsigned*)((const char*)(gbase) + (voff)[_i]), (PG8_LAS unsigned*)(lds + (bufoff) + ldsw + _i * 8192), 16, 0, 0); } while (0)
; #define PG8_LDA(dst, b, h) do { _Pragma("unroll") for (int m = 0; m < 4; ++m) _Pragma("unroll") for (int k = 0; k < 2; ++k) dst[m][k] = *(const PG8_LAS bf16x8*)(lds + PG8_SA(b, h) + aoff + m * 2048 + k * 1024); } while (0)
; #define PG8_MMA(ai, bj, At, Bt) do { __builtin_amdgcn_s_setprio(1); _Pragma("unroll") for (int m = 0; m < 4; ++m) _Pragma("unroll") for (int n = 0; n < 2; ++n) _Pragma("unroll") for (int k = 0; k < 2; ++k) \
;         acc[ai][bj][m][n] = __builtin_amdgcn_mfma_f32_16x16x32_bf16(Bt[n][k], At[m][k], acc[ai][bj][m][n], 0, 0, 0); __builtin_amdgcn_s_setprio(0); } while (0)
; #define PG8_WAIT_V(n) asm volatile("s_waitcnt vmcnt(" #n ")" ::: "memory")
; #define PG8_WAIT_L(n) asm volatile("s_waitcnt lgkmcnt(" #n ")" ::: "memory")
; #define PG8_BAR __builtin_amdgcn_s_barrier()
; #define PG8_SCHED __builtin_amdgcn_sched_barrier(0)
; template <class Epi, class Sched, bool ALIGN_EPI = false, bool SP2 = false>
; __device__ __forceinline__ void gemm_phase(PG8_LAS unsigned char* lds, const Gemm g, const Sched& S, const Epi& E, const bool skip_epi = false) {
;     ...
;             PG8_LDA(At, 1, 1); PG8_STAGE(PG8_SB(1, 0), b3, voffB); PG8_STAGE(PG8_SB(1, 1), b3 + hstep, voffB); PG8_STAGE_A(1, 0, a3, true);
;             PG8_WAIT_V(8); PG8_WAIT_L(0); PG8_BAR; PG8_MMA(1, 0, At, B0); PG8_MMA(1, 1, At, B1); PG8_BAR; PG8_SCHED;
	s_add_i32 s30, s64, s2
	v_lshl_add_u64 v[210:211], v[210:211], 0, s[12:13]
	s_mov_b32 m0, s30
	ds_read_b128 v[154:157], v236 offset:49152
	ds_read_b128 v[166:169], v236 offset:50176
	ds_read_b128 v[170:173], v236 offset:51200
	ds_read_b128 v[174:177], v236 offset:52224
	ds_read_b128 v[178:181], v236 offset:53248
	ds_read_b128 v[182:185], v236 offset:54272
	ds_read_b128 v[186:189], v236 offset:55296
	ds_read_b128 v[206:209], v236 offset:56320
	global_load_lds_dwordx4 v[210:211], off
	s_add_i32 m0, s30, 0x2000
	s_add_u32 s28, s28, 0x40080
	v_lshl_add_u64 v[210:211], v[212:213], 0, s[12:13]
	s_addc_u32 s29, s29, 0
	s_add_i32 s30, s65, s2
	global_load_lds_dwordx4 v[210:211], off
	v_lshl_add_u64 v[210:211], s[28:29], 0, v[192:193]
	s_mov_b32 m0, s30
	s_nop 0
	global_load_lds_dwordx4 v[210:211], off
	v_lshl_add_u64 v[210:211], s[28:29], 0, v[196:197]
	s_add_i32 m0, s30, 0x2000
	s_nop 0
	global_load_lds_dwordx4 v[210:211], off
	v_lshl_add_u64 v[210:211], v[214:215], 0, s[12:13]
	s_mov_b32 m0, s39
	s_nop 0
	global_load_lds_dwordx4 v[210:211], off
	v_lshl_add_u64 v[210:211], v[216:217], 0, s[12:13]
	s_mov_b32 m0, s48
	s_nop 0
	global_load_lds_dwordx4 v[210:211], off
	s_waitcnt vmcnt(8)
	s_waitcnt lgkmcnt(0)
	s_barrier
	s_setprio 3
	s_waitcnt lgkmcnt(0)
	v_mfma_f32_16x16x32_bf16 v[62:65], v[98:101], v[154:157], v[62:65]
	v_mfma_f32_16x16x32_bf16 v[58:61], v[122:125], v[154:157], v[58:61]
	v_mfma_f32_16x16x32_bf16 v[46:49], v[98:101], v[170:173], v[46:49]
	v_mfma_f32_16x16x32_bf16 v[42:45], v[122:125], v[170:173], v[42:45]
	v_mfma_f32_16x16x32_bf16 v[30:33], v[98:101], v[178:181], v[30:33]
	v_mfma_f32_16x16x32_bf16 v[26:29], v[122:125], v[178:181], v[26:29]
	v_mfma_f32_16x16x32_bf16 v[14:17], v[98:101], v[186:189], v[14:17]
	v_mfma_f32_16x16x32_bf16 v[10:13], v[122:125], v[186:189], v[10:13]
	v_mfma_f32_16x16x32_bf16 v[62:65], v[110:113], v[166:169], v[62:65]
	v_mfma_f32_16x16x32_bf16 v[58:61], v[126:129], v[166:169], v[58:61]
	v_mfma_f32_16x16x32_bf16 v[46:49], v[110:113], v[174:177], v[46:49]
	v_mfma_f32_16x16x32_bf16 v[42:45], v[126:129], v[174:177], v[42:45]
	v_mfma_f32_16x16x32_bf16 v[30:33], v[110:113], v[182:185], v[30:33]
	v_mfma_f32_16x16x32_bf16 v[26:29], v[126:129], v[182:185], v[26:29]
	v_mfma_f32_16x16x32_bf16 v[14:17], v[110:113], v[206:209], v[14:17]
	v_mfma_f32_16x16x32_bf16 v[10:13], v[126:129], v[206:209], v[10:13]
	s_setprio 0
	s_setprio 3
	v_mfma_f32_16x16x32_bf16 v[54:57], v[138:141], v[154:157], v[54:57]
	v_mfma_f32_16x16x32_bf16 v[50:53], v[146:149], v[154:157], v[50:53]
	v_mfma_f32_16x16x32_bf16 v[38:41], v[138:141], v[170:173], v[38:41]
	v_mfma_f32_16x16x32_bf16 v[34:37], v[146:149], v[170:173], v[34:37]
	v_mfma_f32_16x16x32_bf16 v[22:25], v[138:141], v[178:181], v[22:25]
	v_mfma_f32_16x16x32_bf16 v[18:21], v[146:149], v[178:181], v[18:21]
	v_mfma_f32_16x16x32_bf16 v[6:9], v[138:141], v[186:189], v[6:9]
	v_mfma_f32_16x16x32_bf16 v[2:5], v[146:149], v[186:189], v[2:5]
	v_mfma_f32_16x16x32_bf16 v[54:57], v[142:145], v[166:169], v[54:57]
	v_mfma_f32_16x16x32_bf16 v[50:53], v[150:153], v[166:169], v[50:53]
	v_mfma_f32_16x16x32_bf16 v[38:41], v[142:145], v[174:177], v[38:41]
	v_mfma_f32_16x16x32_bf16 v[34:37], v[150:153], v[174:177], v[34:37]
	v_mfma_f32_16x16x32_bf16 v[22:25], v[142:145], v[182:185], v[22:25]
	v_mfma_f32_16x16x32_bf16 v[18:21], v[150:153], v[182:185], v[18:21]
	v_mfma_f32_16x16x32_bf16 v[6:9], v[142:145], v[206:209], v[6:9]
	v_mfma_f32_16x16x32_bf16 v[2:5], v[150:153], v[206:209], v[2:5]
	s_setprio 0
	s_barrier
	s_add_i32 s63, s63, 2
	s_add_u32 s26, s26, 0x100
	s_addc_u32 s27, s27, 0
	s_add_u32 s61, s61, 0x100
	s_addc_u32 s62, s62, 0
	s_cmp_gt_u32 s63, 13
	.p2align	3

; #define PG8_STAGE_A(b, h, ptr, NX) do { if constexpr (Sched::GATHER) { unsigned gs_[2]; gs_[0] = ((NX) && last_) ? gN[h][0] : gA[h][0]; gs_[1] = ((NX) && last_) ? gN[h][1] : gA[h][1]; PG8_STAGE(PG8_SA(b, h), ptr, gs_); } \
;         else PG8_STAGE(PG8_SA(b, h), (ptr) + ((h) ? hstep : (size_t)0), voffA); } while (0)
; #define PG8_LDA(dst, b, h) do { _Pragma("unroll") for (int m = 0; m < 4; ++m) _Pragma("unroll") for (int k = 0; k < 2; ++k) dst[m][k] = *(const PG8_LAS bf16x8*)(lds + PG8_SA(b, h) + aoff + m * 2048 + k * 1024); } while (0)
; __device__ __forceinline__ void rstd8(const float* SS, int rowb, int lane, float (&rs)[2][4]) {
;     f32x4 p[2][4];
; #pragma unroll
;     for (int ai = 0; ai < 2; ++ai)
; #pragma unroll
;         for (int m = 0; m < 4; ++m) p[ai][m] = *(const f32x4*)(SS + (size_t)(rowb + HALF * ai + 16 * m + (lane >> 2)) * 16 + 4 * (lane & 3));
;     asm volatile("" : "+v"(p[0][0]), "+v"(p[0][1]), "+v"(p[0][2]), "+v"(p[0][3]), "+v"(p[1][0]), "+v"(p[1][1]), "+v"(p[1][2]), "+v"(p[1][3]));
; template <class Epi, class Sched, bool ALIGN_EPI = false, bool SP2 = false>
; __device__ __forceinline__ void gemm_phase(PG8_LAS unsigned char* lds, const Gemm g, const Sched& S, const Epi& E, const bool skip_epi = false) {
;     ...
;         const char* nA = has_next ? (const char*)g.A + (size_t)nxt.pm * pmstepA + nxt.ko : cA; const char* nB = has_next ? (const char*)g.Bt + (size_t)nxt.pn * tstep + nxt.ko : cB;
;         for (int t = 0; t < nt; t += 2) {
;             const bool last = (t == nt - 2); last_ = last && has_next;
;             const char* a1 = cA + (size_t)(t + 1) * kstep;
;             const char* a2 = last ? nA : cA + (size_t)(t + 2) * kstep; const char* b2 = last ? nB : cB + (size_t)(t + 2) * kstep;
;             const char* a3 = a2 + kstep; const char* b3 = b2 + kstep;
;             if (last && has_next) S.a_ready(nxt);
;             if constexpr (SP2) {
;             PG8_LDB(B0, 0, 0); PG8_LDB(B1, 0, 1); PG8_SCHED; PG8_LDA(At, 0, 0); PG8_STAGE_A(1, 1, a1, false);
;             PG8_WAIT_V(8); PG8_WAIT_L(0); PG8_BAR; PG8_MMA(0, 0, At, B0); PG8_MMA(0, 1, At, B1); PG8_BAR; PG8_SCHED;
;             PG8_LDA(At, 0, 1); PG8_STAGE(PG8_SB(0, 0), b2, voffB); PG8_STAGE(PG8_SB(0, 1), b2 + hstep, voffB); PG8_STAGE_A(0, 0, a2, true);
;             PG8_WAIT_V(8); PG8_WAIT_L(0); PG8_BAR; PG8_MMA(1, 0, At, B0); PG8_MMA(1, 1, At, B1); PG8_BAR; PG8_SCHED;
.LBB0_720:
	s_ashr_i32 s15, s14, 31
	s_lshl_b64 s[16:17], s[14:15], 19
	s_add_u32 s16, s86, s16
	s_addc_u32 s17, s87, s17
	s_and_b64 s[18:19], s[4:5], exec
	s_cselect_b32 s15, s17, s23
	s_cselect_b32 s56, s16, s22
	s_ashr_i32 s13, s12, 31
	s_lshl_b64 s[18:19], s[12:13], 19
	v_readlane_b32 s26, v254, 15
	v_readlane_b32 s27, v254, 16
	s_add_u32 s18, s26, s18
	s_addc_u32 s19, s27, s19
	s_and_b64 s[26:27], s[4:5], exec
	s_cselect_b32 s13, s19, s25
	s_cselect_b32 s57, s18, s24
	s_add_u32 s22, s22, 0x40080
	s_addc_u32 s23, s23, 0
	s_add_u32 s58, s24, 0x100
	s_addc_u32 s59, s25, 0
	s_mov_b32 s60, -2
	s_waitcnt vmcnt(0)
	v_lshl_add_u32 v130, s20, 8, v175
	v_ashrrev_i32_e32 v131, 31, v130
	v_lshlrev_b64 v[130:131], 6, v[130:131]
	v_lshl_add_u64 v[130:131], v[150:151], 0, v[130:131]
	global_load_dwordx4 v[238:241], v[130:131], off
	global_load_dwordx4 v[242:245], v[130:131], off offset:1024
	global_load_dwordx4 v[246:249], v[130:131], off offset:2048
	global_load_dwordx4 v[250:253], v[130:131], off offset:3072
	ds_read_b128 v[130:133], v187
	ds_read_b128 v[134:137], v187 offset:1024
	ds_read_b128 v[138:141], v187 offset:2048
	ds_read_b128 v[160:163], v187 offset:3072
	ds_read_b128 v[164:167], v188
	ds_read_b128 v[182:185], v188 offset:1024
	ds_read_b128 v[192:195], v188 offset:2048
	ds_read_b128 v[196:199], v188 offset:3072
	s_add_u32 s24, s22, 0xfffc0080
	s_addc_u32 s25, s23, -1
	s_cmp_eq_u32 s60, 12
	s_cselect_b32 s27, s15, s25
	s_cselect_b32 s26, s56, s24
	s_cselect_b32 s25, s13, s59
	s_cselect_b32 s24, s57, s58
	v_lshl_add_u64 v[168:169], s[22:23], 0, v[152:153]
	s_add_i32 m0, s29, 0xc000
	ds_read_b128 v[200:203], v189
	ds_read_b128 v[204:207], v189 offset:1024
	ds_read_b128 v[208:211], v189 offset:2048
	ds_read_b128 v[212:215], v189 offset:3072
	ds_read_b128 v[216:219], v189 offset:4096
	ds_read_b128 v[220:223], v189 offset:5120
	ds_read_b128 v[224:227], v189 offset:6144
	ds_read_b128 v[230:233], v189 offset:7168
	global_load_lds_dwordx4 v[168:169], off
	v_lshl_add_u64 v[168:169], s[22:23], 0, v[154:155]
	s_add_i32 m0, s29, 0xe000
	s_nop 0
	global_load_lds_dwordx4 v[168:169], off
	s_waitcnt vmcnt(8)
	s_waitcnt lgkmcnt(0)
	s_barrier
	s_setprio 3
	s_waitcnt lgkmcnt(0)
	v_mfma_f32_16x16x32_bf16 v[126:129], v[130:133], v[200:203], 0
	v_mfma_f32_16x16x32_bf16 v[122:125], v[138:141], v[200:203], 0
	v_mfma_f32_16x16x32_bf16 v[110:113], v[130:133], v[208:211], 0
	v_mfma_f32_16x16x32_bf16 v[106:109], v[138:141], v[208:211], 0
	v_mfma_f32_16x16x32_bf16 v[94:97], v[130:133], v[216:219], 0
	v_mfma_f32_16x16x32_bf16 v[90:93], v[138:141], v[216:219], 0
	v_mfma_f32_16x16x32_bf16 v[78:81], v[130:133], v[224:227], 0
	v_mfma_f32_16x16x32_bf16 v[74:77], v[138:141], v[224:227], 0
	v_mfma_f32_16x16x32_bf16 v[126:129], v[134:137], v[204:207], v[126:129]
	v_mfma_f32_16x16x32_bf16 v[122:125], v[160:163], v[204:207], v[122:125]
	v_mfma_f32_16x16x32_bf16 v[110:113], v[134:137], v[212:215], v[110:113]
	v_mfma_f32_16x16x32_bf16 v[106:109], v[160:163], v[212:215], v[106:109]
	v_mfma_f32_16x16x32_bf16 v[94:97], v[134:137], v[220:223], v[94:97]
	v_mfma_f32_16x16x32_bf16 v[90:93], v[160:163], v[220:223], v[90:93]
	v_mfma_f32_16x16x32_bf16 v[78:81], v[134:137], v[230:233], v[78:81]
	v_mfma_f32_16x16x32_bf16 v[74:77], v[160:163], v[230:233], v[74:77]
	s_setprio 0
	s_setprio 3
	v_mfma_f32_16x16x32_bf16 v[118:121], v[164:167], v[200:203], 0
	v_mfma_f32_16x16x32_bf16 v[114:117], v[192:195], v[200:203], 0
	v_mfma_f32_16x16x32_bf16 v[102:105], v[164:167], v[208:211], 0
	v_mfma_f32_16x16x32_bf16 v[98:101], v[192:195], v[208:211], 0
	v_mfma_f32_16x16x32_bf16 v[86:89], v[164:167], v[216:219], 0
	v_mfma_f32_16x16x32_bf16 v[82:85], v[192:195], v[216:219], 0
	v_mfma_f32_16x16x32_bf16 v[70:73], v[164:167], v[224:227], 0
	v_mfma_f32_16x16x32_bf16 v[66:69], v[192:195], v[224:227], 0
	v_mfma_f32_16x16x32_bf16 v[118:121], v[182:185], v[204:207], v[118:121]
	v_mfma_f32_16x16x32_bf16 v[114:117], v[196:199], v[204:207], v[114:117]
	v_mfma_f32_16x16x32_bf16 v[102:105], v[182:185], v[212:215], v[102:105]
	v_mfma_f32_16x16x32_bf16 v[98:101], v[196:199], v[212:215], v[98:101]
	v_mfma_f32_16x16x32_bf16 v[86:89], v[182:185], v[220:223], v[86:89]
	v_mfma_f32_16x16x32_bf16 v[82:85], v[196:199], v[220:223], v[82:85]
	v_mfma_f32_16x16x32_bf16 v[70:73], v[182:185], v[230:233], v[70:73]
	v_mfma_f32_16x16x32_bf16 v[66:69], v[196:199], v[230:233], v[66:69]
	s_setprio 0
	s_barrier
	s_add_i32 s61, s39, s2
	v_lshl_add_u64 v[168:169], s[24:25], 0, v[146:147]
	s_mov_b32 m0, s61
	ds_read_b128 v[200:203], v189 offset:16384
	ds_read_b128 v[204:207], v189 offset:17408
	ds_read_b128 v[208:211], v189 offset:18432
	ds_read_b128 v[212:215], v189 offset:19456
	ds_read_b128 v[216:219], v189 offset:20480
	ds_read_b128 v[220:223], v189 offset:21504
	ds_read_b128 v[224:227], v189 offset:22528
	ds_read_b128 v[230:233], v189 offset:23552
	global_load_lds_dwordx4 v[168:169], off
	s_add_i32 m0, s61, 0x2000
	s_add_u32 s62, s24, 0x40000
	v_lshl_add_u64 v[172:173], s[24:25], 0, v[142:143]
	s_addc_u32 s63, s25, 0
	s_add_i32 s61, s48, s2
	global_load_lds_dwordx4 v[172:173], off
	v_lshl_add_u64 v[176:177], s[62:63], 0, v[146:147]
	s_mov_b32 m0, s61
	v_lshl_add_u64 v[234:235], s[26:27], 0, v[144:145]
	global_load_lds_dwordx4 v[176:177], off
	v_lshl_add_u64 v[176:177], s[62:63], 0, v[142:143]
	s_add_i32 m0, s61, 0x2000
	s_nop 0
	global_load_lds_dwordx4 v[176:177], off
	v_lshl_add_u64 v[176:177], s[26:27], 0, v[148:149]
	s_mov_b32 m0, s29
	s_nop 0
	global_load_lds_dwordx4 v[176:177], off
	s_mov_b32 m0, s30
	s_nop 0
	global_load_lds_dwordx4 v[234:235], off
	s_waitcnt vmcnt(8)
	s_waitcnt lgkmcnt(0)
	s_barrier
; #define PG8_STAGE_A(b, h, ptr, NX) do { if constexpr (Sched::GATHER) { unsigned gs_[2]; gs_[0] = ((NX) && last_) ? gN[h][0] : gA[h][0]; gs_[1] = ((NX) && last_) ? gN[h][1] : gA[h][1]; PG8_STAGE(PG8_SA(b, h), ptr, gs_); } \
;         else PG8_STAGE(PG8_SA(b, h), (ptr) + ((h) ? hstep : (size_t)0), voffA); } while (0)
; #define PG8_STAGE(bufoff, gbase, voff) do { _Pragma("unroll") for (int _i = 0; _i < 2; ++_i) \
;         __builtin_amdgcn_global_load_lds((const unsigned*)((const char*)(gbase) + (voff)[_i]), (PG8_LAS unsigned*)(lds + (bufoff) + ldsw + _i * 8192), 16, 0, 0); } while (0)
; #define PG8_LDA(dst, b, h) do { _Pragma("unroll") for (int m = 0; m < 4; ++m) _Pragma("unroll") for (int k = 0; k < 2; ++k) dst[m][k] = *(const PG8_LAS bf16x8*)(lds + PG8_SA(b, h) + aoff + m * 2048 + k * 1024); } while (0)
; #define PG8_LDB(dst, b, h) do { _Pragma("unroll") for (int n = 0; n < 2; ++n) _Pragma("unroll") for (int k = 0; k < 2; ++k) dst[n][k] = *(const PG8_LAS bf16x8*)(lds + PG8_SB(b, h) + boff + n * 2048 + k * 1024); } while (0)
; #define PG8_MMA(ai, bj, At, Bt) do { __builtin_amdgcn_s_setprio(1); _Pragma("unroll") for (int m = 0; m < 4; ++m) _Pragma("unroll") for (int n = 0; n < 2; ++n) _Pragma("unroll") for (int k = 0; k < 2; ++k) \
;         acc[ai][bj][m][n] = __builtin_amdgcn_mfma_f32_16x16x32_bf16(Bt[n][k], At[m][k], acc[ai][bj][m][n], 0, 0, 0); __builtin_amdgcn_s_setprio(0); } while (0)
; #define PG8_WAIT_V(n) asm volatile("s_waitcnt vmcnt(" #n ")" ::: "memory")
; #define PG8_WAIT_L(n) asm volatile("s_waitcnt lgkmcnt(" #n ")" ::: "memory")
; #define PG8_BAR __builtin_amdgcn_s_barrier()
; #define PG8_SCHED __builtin_amdgcn_sched_barrier(0)
; template <class Epi, class Sched, bool ALIGN_EPI = false, bool SP2 = false>
; __device__ __forceinline__ void gemm_phase(PG8_LAS unsigned char* lds, const Gemm g, const Sched& S, const Epi& E, const bool skip_epi = false) {
;     ...
;             PG8_WAIT_V(8); PG8_WAIT_L(0); PG8_BAR; PG8_MMA(1, 0, At, B0); PG8_MMA(1, 1, At, B1); PG8_BAR; PG8_SCHED;
;             PG8_LDB(B0, 1, 0); PG8_LDB(B1, 1, 1); PG8_SCHED; PG8_LDA(At, 1, 0); PG8_STAGE_A(0, 1, a2, true);
;             PG8_WAIT_V(8); PG8_WAIT_L(0); PG8_BAR; PG8_MMA(0, 0, At, B0); PG8_MMA(0, 1, At, B1); PG8_BAR; PG8_SCHED;
;             PG8_LDA(At, 1, 1); PG8_STAGE(PG8_SB(1, 0), b3, voffB); PG8_STAGE(PG8_SB(1, 1), b3 + hstep, voffB); PG8_STAGE_A(1, 0, a3, true);
	s_setprio 3
	s_waitcnt lgkmcnt(0)
	v_mfma_f32_16x16x32_bf16 v[62:65], v[130:133], v[200:203], 0
	v_mfma_f32_16x16x32_bf16 v[58:61], v[138:141], v[200:203], 0
	v_mfma_f32_16x16x32_bf16 v[46:49], v[130:133], v[208:211], 0
	v_mfma_f32_16x16x32_bf16 v[42:45], v[138:141], v[208:211], 0
	v_mfma_f32_16x16x32_bf16 v[30:33], v[130:133], v[216:219], 0
	v_mfma_f32_16x16x32_bf16 v[26:29], v[138:141], v[216:219], 0
	v_mfma_f32_16x16x32_bf16 v[14:17], v[130:133], v[224:227], 0
	v_mfma_f32_16x16x32_bf16 v[10:13], v[138:141], v[224:227], 0
	v_mfma_f32_16x16x32_bf16 v[62:65], v[134:137], v[204:207], v[62:65]
	v_mfma_f32_16x16x32_bf16 v[58:61], v[160:163], v[204:207], v[58:61]
	v_mfma_f32_16x16x32_bf16 v[46:49], v[134:137], v[212:215], v[46:49]
	v_mfma_f32_16x16x32_bf16 v[42:45], v[160:163], v[212:215], v[42:45]
	v_mfma_f32_16x16x32_bf16 v[30:33], v[134:137], v[220:223], v[30:33]
	v_mfma_f32_16x16x32_bf16 v[26:29], v[160:163], v[220:223], v[26:29]
	v_mfma_f32_16x16x32_bf16 v[14:17], v[134:137], v[230:233], v[14:17]
	v_mfma_f32_16x16x32_bf16 v[10:13], v[160:163], v[230:233], v[10:13]
	s_setprio 0
	s_setprio 3
	v_mfma_f32_16x16x32_bf16 v[54:57], v[164:167], v[200:203], 0
	v_mfma_f32_16x16x32_bf16 v[50:53], v[192:195], v[200:203], 0
	v_mfma_f32_16x16x32_bf16 v[38:41], v[164:167], v[208:211], 0
	v_mfma_f32_16x16x32_bf16 v[34:37], v[192:195], v[208:211], 0
	v_mfma_f32_16x16x32_bf16 v[22:25], v[164:167], v[216:219], 0
	v_mfma_f32_16x16x32_bf16 v[18:21], v[192:195], v[216:219], 0
	v_mfma_f32_16x16x32_bf16 v[6:9], v[164:167], v[224:227], 0
	v_mfma_f32_16x16x32_bf16 v[2:5], v[192:195], v[224:227], 0
	v_mfma_f32_16x16x32_bf16 v[54:57], v[182:185], v[204:207], v[54:57]
	v_mfma_f32_16x16x32_bf16 v[50:53], v[196:199], v[204:207], v[50:53]
	v_mfma_f32_16x16x32_bf16 v[38:41], v[182:185], v[212:215], v[38:41]
	v_mfma_f32_16x16x32_bf16 v[34:37], v[196:199], v[212:215], v[34:37]
	v_mfma_f32_16x16x32_bf16 v[22:25], v[182:185], v[220:223], v[22:25]
	v_mfma_f32_16x16x32_bf16 v[18:21], v[196:199], v[220:223], v[18:21]
	v_mfma_f32_16x16x32_bf16 v[6:9], v[182:185], v[230:233], v[6:9]
	v_mfma_f32_16x16x32_bf16 v[2:5], v[196:199], v[230:233], v[2:5]
	s_setprio 0
	s_barrier
	s_add_i32 s61, 0, 0x18000
	s_add_i32 s62, 0, 0x1c000
	v_add_u32_e32 v160, s61, v1
	v_add_u32_e32 v170, s62, v1
	ds_read_b128 v[130:133], v160
	ds_read_b128 v[134:137], v160 offset:1024
	ds_read_b128 v[138:141], v160 offset:2048
	ds_read_b128 v[160:163], v160 offset:3072
	ds_read_b128 v[164:167], v170
	ds_read_b128 v[182:185], v170 offset:1024
	ds_read_b128 v[192:195], v170 offset:2048
	ds_read_b128 v[196:199], v170 offset:3072
	s_add_u32 s26, s26, 0x40000
	s_addc_u32 s27, s27, 0
	s_mov_b32 m0, s31
	v_lshl_add_u64 v[236:237], s[26:27], 0, v[148:149]
	ds_read_b128 v[200:203], v189 offset:32768
	ds_read_b128 v[204:207], v189 offset:33792
	ds_read_b128 v[208:211], v189 offset:34816
	ds_read_b128 v[212:215], v189 offset:35840
	ds_read_b128 v[216:219], v189 offset:36864
	ds_read_b128 v[220:223], v189 offset:37888
	ds_read_b128 v[224:227], v189 offset:38912
	ds_read_b128 v[230:233], v189 offset:39936
	global_load_lds_dwordx4 v[236:237], off
	v_lshl_add_u64 v[236:237], s[26:27], 0, v[144:145]
	s_mov_b32 m0, s34
	s_nop 0
	global_load_lds_dwordx4 v[236:237], off
	s_waitcnt vmcnt(8)
	s_waitcnt lgkmcnt(0)
	s_barrier
	s_setprio 3
	s_waitcnt lgkmcnt(0)
	v_mfma_f32_16x16x32_bf16 v[126:129], v[130:133], v[200:203], v[126:129]
	v_mfma_f32_16x16x32_bf16 v[122:125], v[138:141], v[200:203], v[122:125]
	v_mfma_f32_16x16x32_bf16 v[110:113], v[130:133], v[208:211], v[110:113]
	v_mfma_f32_16x16x32_bf16 v[106:109], v[138:141], v[208:211], v[106:109]
	v_mfma_f32_16x16x32_bf16 v[94:97], v[130:133], v[216:219], v[94:97]
	v_mfma_f32_16x16x32_bf16 v[90:93], v[138:141], v[216:219], v[90:93]
	v_mfma_f32_16x16x32_bf16 v[78:81], v[130:133], v[224:227], v[78:81]
	v_mfma_f32_16x16x32_bf16 v[74:77], v[138:141], v[224:227], v[74:77]
	v_mfma_f32_16x16x32_bf16 v[126:129], v[134:137], v[204:207], v[126:129]
	v_mfma_f32_16x16x32_bf16 v[122:125], v[160:163], v[204:207], v[122:125]
	v_mfma_f32_16x16x32_bf16 v[110:113], v[134:137], v[212:215], v[110:113]
	v_mfma_f32_16x16x32_bf16 v[106:109], v[160:163], v[212:215], v[106:109]
	v_mfma_f32_16x16x32_bf16 v[94:97], v[134:137], v[220:223], v[94:97]
	v_mfma_f32_16x16x32_bf16 v[90:93], v[160:163], v[220:223], v[90:93]
	v_mfma_f32_16x16x32_bf16 v[78:81], v[134:137], v[230:233], v[78:81]
	v_mfma_f32_16x16x32_bf16 v[74:77], v[160:163], v[230:233], v[74:77]
	s_setprio 0
	s_setprio 3
	v_mfma_f32_16x16x32_bf16 v[118:121], v[164:167], v[200:203], v[118:121]
	v_mfma_f32_16x16x32_bf16 v[114:117], v[192:195], v[200:203], v[114:117]
	v_mfma_f32_16x16x32_bf16 v[102:105], v[164:167], v[208:211], v[102:105]
	v_mfma_f32_16x16x32_bf16 v[98:101], v[192:195], v[208:211], v[98:101]
	v_mfma_f32_16x16x32_bf16 v[86:89], v[164:167], v[216:219], v[86:89]
	v_mfma_f32_16x16x32_bf16 v[82:85], v[192:195], v[216:219], v[82:85]
	v_mfma_f32_16x16x32_bf16 v[70:73], v[164:167], v[224:227], v[70:73]
	v_mfma_f32_16x16x32_bf16 v[66:69], v[192:195], v[224:227], v[66:69]
	v_mfma_f32_16x16x32_bf16 v[118:121], v[182:185], v[204:207], v[118:121]
	v_mfma_f32_16x16x32_bf16 v[114:117], v[196:199], v[204:207], v[114:117]
	v_mfma_f32_16x16x32_bf16 v[102:105], v[182:185], v[212:215], v[102:105]
	v_mfma_f32_16x16x32_bf16 v[98:101], v[196:199], v[212:215], v[98:101]
	v_mfma_f32_16x16x32_bf16 v[86:89], v[182:185], v[220:223], v[86:89]
	v_mfma_f32_16x16x32_bf16 v[82:85], v[196:199], v[220:223], v[82:85]
	v_mfma_f32_16x16x32_bf16 v[70:73], v[182:185], v[230:233], v[70:73]
	v_mfma_f32_16x16x32_bf16 v[66:69], v[196:199], v[230:233], v[66:69]
	s_setprio 0
	s_barrier
; #define PG8_STAGE_A(b, h, ptr, NX) do { if constexpr (Sched::GATHER) { unsigned gs_[2]; gs_[0] = ((NX) && last_) ? gN[h][0] : gA[h][0]; gs_[1] = ((NX) && last_) ? gN[h][1] : gA[h][1]; PG8_STAGE(PG8_SA(b, h), ptr, gs_); } \
;         else PG8_STAGE(PG8_SA(b, h), (ptr) + ((h) ? hstep : (size_t)0), voffA); } while (0)
; #define PG8_STAGE(bufoff, gbase, voff) do { _Pragma("unroll") for (int _i = 0; _i < 2; ++_i) \
;         __builtin_amdgcn_global_load_lds((const unsigned*)((const char*)(gbase) + (voff)[_i]), (PG8_LAS unsigned*)(lds + (bufoff) + ldsw + _i * 8192), 16, 0, 0); } while (0)
; #define PG8_LDA(dst, b, h) do { _Pragma("unroll") for (int m = 0; m < 4; ++m) _Pragma("unroll") for (int k = 0; k < 2; ++k) dst[m][k] = *(const PG8_LAS bf16x8*)(lds + PG8_SA(b, h) + aoff + m * 2048 + k * 1024); } while (0)
; #define PG8_MMA(ai, bj, At, Bt) do { __builtin_amdgcn_s_setprio(1); _Pragma("unroll") for (int m = 0; m < 4; ++m) _Pragma("unroll") for (int n = 0; n < 2; ++n) _Pragma("unroll") for (int k = 0; k < 2; ++k) \
;         acc[ai][bj][m][n] = __builtin_amdgcn_mfma_f32_16x16x32_bf16(Bt[n][k], At[m][k], acc[ai][bj][m][n], 0, 0, 0); __builtin_amdgcn_s_setprio(0); } while (0)
; #define PG8_WAIT_V(n) asm volatile("s_waitcnt vmcnt(" #n ")" ::: "memory")
; #define PG8_WAIT_L(n) asm volatile("s_waitcnt lgkmcnt(" #n ")" ::: "memory")
; #define PG8_BAR __builtin_amdgcn_s_barrier()
; #define PG8_SCHED __builtin_amdgcn_sched_barrier(0)
; template <class Epi, class Sched, bool ALIGN_EPI = false, bool SP2 = false>
; __device__ __forceinline__ void gemm_phase(PG8_LAS unsigned char* lds, const Gemm g, const Sched& S, const Epi& E, const bool skip_epi = false) {
;     ...
;             PG8_LDA(At, 1, 1); PG8_STAGE(PG8_SB(1, 0), b3, voffB); PG8_STAGE(PG8_SB(1, 1), b3 + hstep, voffB); PG8_STAGE_A(1, 0, a3, true);
;             PG8_WAIT_V(8); PG8_WAIT_L(0); PG8_BAR; PG8_MMA(1, 0, At, B0); PG8_MMA(1, 1, At, B1); PG8_BAR; PG8_SCHED;
	s_add_i32 s26, s61, s2
	v_lshl_add_u64 v[168:169], v[168:169], 0, s[8:9]
	s_mov_b32 m0, s26
	ds_read_b128 v[200:203], v189 offset:49152
	ds_read_b128 v[204:207], v189 offset:50176
	ds_read_b128 v[208:211], v189 offset:51200
	ds_read_b128 v[212:215], v189 offset:52224
	ds_read_b128 v[216:219], v189 offset:53248
	ds_read_b128 v[220:223], v189 offset:54272
	ds_read_b128 v[224:227], v189 offset:55296
	ds_read_b128 v[230:233], v189 offset:56320
	global_load_lds_dwordx4 v[168:169], off
	s_add_i32 m0, s26, 0x2000
	s_add_u32 s24, s24, 0x40080
	v_lshl_add_u64 v[168:169], v[172:173], 0, s[8:9]
	s_addc_u32 s25, s25, 0
	s_add_i32 s26, s62, s2
	global_load_lds_dwordx4 v[168:169], off
	v_lshl_add_u64 v[168:169], s[24:25], 0, v[146:147]
	s_mov_b32 m0, s26
	s_nop 0
	global_load_lds_dwordx4 v[168:169], off
	v_lshl_add_u64 v[168:169], s[24:25], 0, v[142:143]
	s_add_i32 m0, s26, 0x2000
	s_nop 0
	global_load_lds_dwordx4 v[168:169], off
	v_lshl_add_u64 v[168:169], v[176:177], 0, s[8:9]
	s_mov_b32 m0, s36
	s_nop 0
	global_load_lds_dwordx4 v[168:169], off
	v_lshl_add_u64 v[168:169], v[234:235], 0, s[8:9]
	s_mov_b32 m0, s37
	s_nop 0
	global_load_lds_dwordx4 v[168:169], off
	s_waitcnt vmcnt(8)
	s_waitcnt lgkmcnt(0)
	s_barrier
	s_setprio 3
	s_waitcnt lgkmcnt(0)
	v_mfma_f32_16x16x32_bf16 v[62:65], v[130:133], v[200:203], v[62:65]
	v_mfma_f32_16x16x32_bf16 v[58:61], v[138:141], v[200:203], v[58:61]
	v_mfma_f32_16x16x32_bf16 v[46:49], v[130:133], v[208:211], v[46:49]
	v_mfma_f32_16x16x32_bf16 v[42:45], v[138:141], v[208:211], v[42:45]
	v_mfma_f32_16x16x32_bf16 v[30:33], v[130:133], v[216:219], v[30:33]
	v_mfma_f32_16x16x32_bf16 v[26:29], v[138:141], v[216:219], v[26:29]
	v_mfma_f32_16x16x32_bf16 v[14:17], v[130:133], v[224:227], v[14:17]
	v_mfma_f32_16x16x32_bf16 v[10:13], v[138:141], v[224:227], v[10:13]
	v_mfma_f32_16x16x32_bf16 v[62:65], v[134:137], v[204:207], v[62:65]
	v_mfma_f32_16x16x32_bf16 v[58:61], v[160:163], v[204:207], v[58:61]
	v_mfma_f32_16x16x32_bf16 v[46:49], v[134:137], v[212:215], v[46:49]
	v_mfma_f32_16x16x32_bf16 v[42:45], v[160:163], v[212:215], v[42:45]
	v_mfma_f32_16x16x32_bf16 v[30:33], v[134:137], v[220:223], v[30:33]
	v_mfma_f32_16x16x32_bf16 v[26:29], v[160:163], v[220:223], v[26:29]
	v_mfma_f32_16x16x32_bf16 v[14:17], v[134:137], v[230:233], v[14:17]
	v_mfma_f32_16x16x32_bf16 v[10:13], v[160:163], v[230:233], v[10:13]
	s_setprio 0
	s_setprio 3
	v_mfma_f32_16x16x32_bf16 v[54:57], v[164:167], v[200:203], v[54:57]
	v_mfma_f32_16x16x32_bf16 v[50:53], v[192:195], v[200:203], v[50:53]
	v_mfma_f32_16x16x32_bf16 v[38:41], v[164:167], v[208:211], v[38:41]
	v_mfma_f32_16x16x32_bf16 v[34:37], v[192:195], v[208:211], v[34:37]
	v_mfma_f32_16x16x32_bf16 v[22:25], v[164:167], v[216:219], v[22:25]
	v_mfma_f32_16x16x32_bf16 v[18:21], v[192:195], v[216:219], v[18:21]
	v_mfma_f32_16x16x32_bf16 v[6:9], v[164:167], v[224:227], v[6:9]
	v_mfma_f32_16x16x32_bf16 v[2:5], v[192:195], v[224:227], v[2:5]
	v_mfma_f32_16x16x32_bf16 v[54:57], v[182:185], v[204:207], v[54:57]
	v_mfma_f32_16x16x32_bf16 v[50:53], v[196:199], v[204:207], v[50:53]
	v_mfma_f32_16x16x32_bf16 v[38:41], v[182:185], v[212:215], v[38:41]
	v_mfma_f32_16x16x32_bf16 v[34:37], v[196:199], v[212:215], v[34:37]
	v_mfma_f32_16x16x32_bf16 v[22:25], v[182:185], v[220:223], v[22:25]
	v_mfma_f32_16x16x32_bf16 v[18:21], v[196:199], v[220:223], v[18:21]
	v_mfma_f32_16x16x32_bf16 v[6:9], v[182:185], v[230:233], v[6:9]
	v_mfma_f32_16x16x32_bf16 v[2:5], v[196:199], v[230:233], v[2:5]
	s_setprio 0
	s_barrier
	s_add_i32 s60, s60, 2
	s_add_u32 s22, s22, 0x100
	s_addc_u32 s23, s23, 0
	s_add_u32 s58, s58, 0x100
	s_addc_u32 s59, s59, 0
	s_cmp_gt_u32 s60, 13
	.p2align	3

; #define PG8_STAGE_A(b, h, ptr, NX) do { if constexpr (Sched::GATHER) { unsigned gs_[2]; gs_[0] = ((NX) && last_) ? gN[h][0] : gA[h][0]; gs_[1] = ((NX) && last_) ? gN[h][1] : gA[h][1]; PG8_STAGE(PG8_SA(b, h), ptr, gs_); } \
;         else PG8_STAGE(PG8_SA(b, h), (ptr) + ((h) ? hstep : (size_t)0), voffA); } while (0)
; #define PG8_STAGE(bufoff, gbase, voff) do { _Pragma("unroll") for (int _i = 0; _i < 2; ++_i) \
;         __builtin_amdgcn_global_load_lds((const unsigned*)((const char*)(gbase) + (voff)[_i]), (PG8_LAS unsigned*)(lds + (bufoff) + ldsw + _i * 8192), 16, 0, 0); } while (0)
; #define PG8_LDA(dst, b, h) do { _Pragma("unroll") for (int m = 0; m < 4; ++m) _Pragma("unroll") for (int k = 0; k < 2; ++k) dst[m][k] = *(const PG8_LAS bf16x8*)(lds + PG8_SA(b, h) + aoff + m * 2048 + k * 1024); } while (0)
; #define PG8_LDB(dst, b, h) do { _Pragma("unroll") for (int n = 0; n < 2; ++n) _Pragma("unroll") for (int k = 0; k < 2; ++k) dst[n][k] = *(const PG8_LAS bf16x8*)(lds + PG8_SB(b, h) + boff + n * 2048 + k * 1024); } while (0)
; #define PG8_WAIT_V(n) asm volatile("s_waitcnt vmcnt(" #n ")" ::: "memory")
; #define PG8_WAIT_L(n) asm volatile("s_waitcnt lgkmcnt(" #n ")" ::: "memory")
; template <class Epi, class Sched, bool ALIGN_EPI = false, bool SP2 = false>
; __device__ __forceinline__ void gemm_phase(PG8_LAS unsigned char* lds, const Gemm g, const Sched& S, const Epi& E, const bool skip_epi = false) {
;     ...
;         for (int t = 0; t < nt; t += 2) {
;             const bool last = (t == nt - 2); last_ = last && has_next;
;             const char* a1 = cA + (size_t)(t + 1) * kstep;
;             const char* a2 = last ? nA : cA + (size_t)(t + 2) * kstep; const char* b2 = last ? nB : cB + (size_t)(t + 2) * kstep;
;             const char* a3 = a2 + kstep; const char* b3 = b2 + kstep;
;             if (last && has_next) S.a_ready(nxt);
;             if constexpr (SP2) {
;             PG8_LDB(B0, 0, 0); PG8_LDB(B1, 0, 1); PG8_SCHED; PG8_LDA(At, 0, 0); PG8_STAGE_A(1, 1, a1, false);
;             PG8_WAIT_V(8); PG8_WAIT_L(0); PG8_BAR; PG8_MMA(0, 0, At, B0); PG8_MMA(0, 1, At, B1); PG8_BAR; PG8_SCHED;
;             PG8_LDA(At, 0, 1); PG8_STAGE(PG8_SB(0, 0), b2, voffB); PG8_STAGE(PG8_SB(0, 1), b2 + hstep, voffB); PG8_STAGE_A(0, 0, a2, true);
;             PG8_WAIT_V(8); PG8_WAIT_L(0); PG8_BAR; PG8_MMA(1, 0, At, B0); PG8_MMA(1, 1, At, B1); PG8_BAR; PG8_SCHED;
.LBB0_856:
	s_add_u32 s55, s22, 0x100
	s_addc_u32 s56, s23, 0
	s_mov_b32 s57, -2
	s_waitcnt vmcnt(0)
	s_waitcnt lgkmcnt(0)
	ds_read_b128 v[98:101], v234
	ds_read_b128 v[110:113], v234 offset:1024
	ds_read_b128 v[122:125], v234 offset:2048
	ds_read_b128 v[126:129], v234 offset:3072
	ds_read_b128 v[138:141], v235
	ds_read_b128 v[142:145], v235 offset:1024
	ds_read_b128 v[146:149], v235 offset:2048
	ds_read_b128 v[150:153], v235 offset:3072
	s_add_u32 s22, s20, 0x100
	s_addc_u32 s23, s21, 0
	s_cmp_eq_u32 s57, 40
	s_cselect_b32 s27, s9, s23
	s_cselect_b32 s26, s8, s22
	s_cselect_b32 s25, s19, s56
	s_cselect_b32 s24, s18, s55
	v_lshl_add_u64 v[210:211], s[20:21], 0, v[198:199]
	s_add_i32 m0, s3, 0xc000
	ds_read_b128 v[154:157], v236
	ds_read_b128 v[166:169], v236 offset:1024
	ds_read_b128 v[170:173], v236 offset:2048
	ds_read_b128 v[174:177], v236 offset:3072
	ds_read_b128 v[178:181], v236 offset:4096
	ds_read_b128 v[182:185], v236 offset:5120
	ds_read_b128 v[186:189], v236 offset:6144
	ds_read_b128 v[206:209], v236 offset:7168
	global_load_lds_dwordx4 v[210:211], off
	v_lshl_add_u64 v[210:211], s[20:21], 0, v[200:201]
	s_add_i32 m0, s3, 0xe000
	s_nop 0
	global_load_lds_dwordx4 v[210:211], off
	s_waitcnt vmcnt(8)
	s_waitcnt lgkmcnt(0)
	s_barrier
	s_setprio 3
	s_waitcnt lgkmcnt(0)
	v_mfma_f32_16x16x32_bf16 v[162:165], v[98:101], v[154:157], 0
	v_mfma_f32_16x16x32_bf16 v[158:161], v[122:125], v[154:157], 0
	v_mfma_f32_16x16x32_bf16 v[118:121], v[98:101], v[170:173], 0
	v_mfma_f32_16x16x32_bf16 v[114:117], v[122:125], v[170:173], 0
	v_mfma_f32_16x16x32_bf16 v[94:97], v[98:101], v[178:181], 0
	v_mfma_f32_16x16x32_bf16 v[90:93], v[122:125], v[178:181], 0
	v_mfma_f32_16x16x32_bf16 v[78:81], v[98:101], v[186:189], 0
	v_mfma_f32_16x16x32_bf16 v[74:77], v[122:125], v[186:189], 0
	v_mfma_f32_16x16x32_bf16 v[162:165], v[110:113], v[166:169], v[162:165]
	v_mfma_f32_16x16x32_bf16 v[158:161], v[126:129], v[166:169], v[158:161]
	v_mfma_f32_16x16x32_bf16 v[118:121], v[110:113], v[174:177], v[118:121]
	v_mfma_f32_16x16x32_bf16 v[114:117], v[126:129], v[174:177], v[114:117]
	v_mfma_f32_16x16x32_bf16 v[94:97], v[110:113], v[182:185], v[94:97]
	v_mfma_f32_16x16x32_bf16 v[90:93], v[126:129], v[182:185], v[90:93]
	v_mfma_f32_16x16x32_bf16 v[78:81], v[110:113], v[206:209], v[78:81]
	v_mfma_f32_16x16x32_bf16 v[74:77], v[126:129], v[206:209], v[74:77]
	s_setprio 0
	s_setprio 3
	v_mfma_f32_16x16x32_bf16 v[134:137], v[138:141], v[154:157], 0
	v_mfma_f32_16x16x32_bf16 v[130:133], v[146:149], v[154:157], 0
	v_mfma_f32_16x16x32_bf16 v[106:109], v[138:141], v[170:173], 0
	v_mfma_f32_16x16x32_bf16 v[102:105], v[146:149], v[170:173], 0
	v_mfma_f32_16x16x32_bf16 v[86:89], v[138:141], v[178:181], 0
	v_mfma_f32_16x16x32_bf16 v[82:85], v[146:149], v[178:181], 0
	v_mfma_f32_16x16x32_bf16 v[70:73], v[138:141], v[186:189], 0
	v_mfma_f32_16x16x32_bf16 v[66:69], v[146:149], v[186:189], 0
	v_mfma_f32_16x16x32_bf16 v[134:137], v[142:145], v[166:169], v[134:137]
	v_mfma_f32_16x16x32_bf16 v[130:133], v[150:153], v[166:169], v[130:133]
	v_mfma_f32_16x16x32_bf16 v[106:109], v[142:145], v[174:177], v[106:109]
	v_mfma_f32_16x16x32_bf16 v[102:105], v[150:153], v[174:177], v[102:105]
	v_mfma_f32_16x16x32_bf16 v[86:89], v[142:145], v[182:185], v[86:89]
	v_mfma_f32_16x16x32_bf16 v[82:85], v[150:153], v[182:185], v[82:85]
	v_mfma_f32_16x16x32_bf16 v[70:73], v[142:145], v[206:209], v[70:73]
	v_mfma_f32_16x16x32_bf16 v[66:69], v[150:153], v[206:209], v[66:69]
	s_setprio 0
	s_barrier
	s_add_i32 s20, s39, s2
	v_lshl_add_u64 v[210:211], s[24:25], 0, v[192:193]
	s_mov_b32 m0, s20
	ds_read_b128 v[154:157], v236 offset:16384
	ds_read_b128 v[166:169], v236 offset:17408
	ds_read_b128 v[170:173], v236 offset:18432
	ds_read_b128 v[174:177], v236 offset:19456
	ds_read_b128 v[178:181], v236 offset:20480
	ds_read_b128 v[182:185], v236 offset:21504
	ds_read_b128 v[186:189], v236 offset:22528
	ds_read_b128 v[206:209], v236 offset:23552
	global_load_lds_dwordx4 v[210:211], off
	s_add_i32 m0, s20, 0x2000
	s_add_u32 s20, s24, 0xb0000
	v_lshl_add_u64 v[212:213], s[24:25], 0, v[196:197]
	s_addc_u32 s21, s25, 0
	s_add_i32 s58, s48, s2
	global_load_lds_dwordx4 v[212:213], off
	v_lshl_add_u64 v[214:215], s[20:21], 0, v[192:193]
	s_mov_b32 m0, s58
	v_lshl_add_u64 v[216:217], s[26:27], 0, v[194:195]
	global_load_lds_dwordx4 v[214:215], off
	v_lshl_add_u64 v[214:215], s[20:21], 0, v[196:197]
	s_add_i32 m0, s58, 0x2000
	s_nop 0
	global_load_lds_dwordx4 v[214:215], off
	v_lshl_add_u64 v[214:215], s[26:27], 0, v[190:191]
	s_mov_b32 m0, s3
	s_nop 0
	global_load_lds_dwordx4 v[214:215], off
	s_mov_b32 m0, s28
	s_nop 0
	global_load_lds_dwordx4 v[216:217], off
	s_waitcnt vmcnt(8)
	s_waitcnt lgkmcnt(0)
	s_barrier
; #define PG8_STAGE_A(b, h, ptr, NX) do { if constexpr (Sched::GATHER) { unsigned gs_[2]; gs_[0] = ((NX) && last_) ? gN[h][0] : gA[h][0]; gs_[1] = ((NX) && last_) ? gN[h][1] : gA[h][1]; PG8_STAGE(PG8_SA(b, h), ptr, gs_); } \
;         else PG8_STAGE(PG8_SA(b, h), (ptr) + ((h) ? hstep : (size_t)0), voffA); } while (0)
; #define PG8_STAGE(bufoff, gbase, voff) do { _Pragma("unroll") for (int _i = 0; _i < 2; ++_i) \
;         __builtin_amdgcn_global_load_lds((const unsigned*)((const char*)(gbase) + (voff)[_i]), (PG8_LAS unsigned*)(lds + (bufoff) + ldsw + _i * 8192), 16, 0, 0); } while (0)
; #define PG8_LDA(dst, b, h) do { _Pragma("unroll") for (int m = 0; m < 4; ++m) _Pragma("unroll") for (int k = 0; k < 2; ++k) dst[m][k] = *(const PG8_LAS bf16x8*)(lds + PG8_SA(b, h) + aoff + m * 2048 + k * 1024); } while (0)
; #define PG8_LDB(dst, b, h) do { _Pragma("unroll") for (int n = 0; n < 2; ++n) _Pragma("unroll") for (int k = 0; k < 2; ++k) dst[n][k] = *(const PG8_LAS bf16x8*)(lds + PG8_SB(b, h) + boff + n * 2048 + k * 1024); } while (0)
; #define PG8_MMA(ai, bj, At, Bt) do { __builtin_amdgcn_s_setprio(1); _Pragma("unroll") for (int m = 0; m < 4; ++m) _Pragma("unroll") for (int n = 0; n < 2; ++n) _Pragma("unroll") for (int k = 0; k < 2; ++k) \
;         acc[ai][bj][m][n] = __builtin_amdgcn_mfma_f32_16x16x32_bf16(Bt[n][k], At[m][k], acc[ai][bj][m][n], 0, 0, 0); __builtin_amdgcn_s_setprio(0); } while (0)
; #define PG8_WAIT_V(n) asm volatile("s_waitcnt vmcnt(" #n ")" ::: "memory")
; #define PG8_WAIT_L(n) asm volatile("s_waitcnt lgkmcnt(" #n ")" ::: "memory")
; #define PG8_BAR __builtin_amdgcn_s_barrier()
; #define PG8_SCHED __builtin_amdgcn_sched_barrier(0)
; template <class Epi, class Sched, bool ALIGN_EPI = false, bool SP2 = false>
; __device__ __forceinline__ void gemm_phase(PG8_LAS unsigned char* lds, const Gemm g, const Sched& S, const Epi& E, const bool skip_epi = false) {
;     ...
;             PG8_WAIT_V(8); PG8_WAIT_L(0); PG8_BAR; PG8_MMA(1, 0, At, B0); PG8_MMA(1, 1, At, B1); PG8_BAR; PG8_SCHED;
;             PG8_LDB(B0, 1, 0); PG8_LDB(B1, 1, 1); PG8_SCHED; PG8_LDA(At, 1, 0); PG8_STAGE_A(0, 1, a2, true);
;             PG8_WAIT_V(8); PG8_WAIT_L(0); PG8_BAR; PG8_MMA(0, 0, At, B0); PG8_MMA(0, 1, At, B1); PG8_BAR; PG8_SCHED;
;             PG8_LDA(At, 1, 1); PG8_STAGE(PG8_SB(1, 0), b3, voffB); PG8_STAGE(PG8_SB(1, 1), b3 + hstep, voffB); PG8_STAGE_A(1, 0, a3, true);
	s_setprio 3
	s_waitcnt lgkmcnt(0)
	v_mfma_f32_16x16x32_bf16 v[62:65], v[98:101], v[154:157], 0
	v_mfma_f32_16x16x32_bf16 v[58:61], v[122:125], v[154:157], 0
	v_mfma_f32_16x16x32_bf16 v[46:49], v[98:101], v[170:173], 0
	v_mfma_f32_16x16x32_bf16 v[42:45], v[122:125], v[170:173], 0
	v_mfma_f32_16x16x32_bf16 v[30:33], v[98:101], v[178:181], 0
	v_mfma_f32_16x16x32_bf16 v[26:29], v[122:125], v[178:181], 0
	v_mfma_f32_16x16x32_bf16 v[14:17], v[98:101], v[186:189], 0
	v_mfma_f32_16x16x32_bf16 v[10:13], v[122:125], v[186:189], 0
	v_mfma_f32_16x16x32_bf16 v[62:65], v[110:113], v[166:169], v[62:65]
	v_mfma_f32_16x16x32_bf16 v[58:61], v[126:129], v[166:169], v[58:61]
	v_mfma_f32_16x16x32_bf16 v[46:49], v[110:113], v[174:177], v[46:49]
	v_mfma_f32_16x16x32_bf16 v[42:45], v[126:129], v[174:177], v[42:45]
	v_mfma_f32_16x16x32_bf16 v[30:33], v[110:113], v[182:185], v[30:33]
	v_mfma_f32_16x16x32_bf16 v[26:29], v[126:129], v[182:185], v[26:29]
	v_mfma_f32_16x16x32_bf16 v[14:17], v[110:113], v[206:209], v[14:17]
	v_mfma_f32_16x16x32_bf16 v[10:13], v[126:129], v[206:209], v[10:13]
	s_setprio 0
	s_setprio 3
	v_mfma_f32_16x16x32_bf16 v[54:57], v[138:141], v[154:157], 0
	v_mfma_f32_16x16x32_bf16 v[50:53], v[146:149], v[154:157], 0
	v_mfma_f32_16x16x32_bf16 v[38:41], v[138:141], v[170:173], 0
	v_mfma_f32_16x16x32_bf16 v[34:37], v[146:149], v[170:173], 0
	v_mfma_f32_16x16x32_bf16 v[22:25], v[138:141], v[178:181], 0
	v_mfma_f32_16x16x32_bf16 v[18:21], v[146:149], v[178:181], 0
	v_mfma_f32_16x16x32_bf16 v[6:9], v[138:141], v[186:189], 0
	v_mfma_f32_16x16x32_bf16 v[2:5], v[146:149], v[186:189], 0
	v_mfma_f32_16x16x32_bf16 v[54:57], v[142:145], v[166:169], v[54:57]
	v_mfma_f32_16x16x32_bf16 v[50:53], v[150:153], v[166:169], v[50:53]
	v_mfma_f32_16x16x32_bf16 v[38:41], v[142:145], v[174:177], v[38:41]
	v_mfma_f32_16x16x32_bf16 v[34:37], v[150:153], v[174:177], v[34:37]
	v_mfma_f32_16x16x32_bf16 v[22:25], v[142:145], v[182:185], v[22:25]
	v_mfma_f32_16x16x32_bf16 v[18:21], v[150:153], v[182:185], v[18:21]
	v_mfma_f32_16x16x32_bf16 v[6:9], v[142:145], v[206:209], v[6:9]
	v_mfma_f32_16x16x32_bf16 v[2:5], v[150:153], v[206:209], v[2:5]
	s_setprio 0
	s_barrier
	s_add_i32 s58, 0, 0x18000
	s_add_i32 s59, 0, 0x1c000
	v_add_u32_e32 v126, s58, v229
	v_add_u32_e32 v150, s59, v229
	ds_read_b128 v[98:101], v126
	ds_read_b128 v[110:113], v126 offset:1024
	ds_read_b128 v[122:125], v126 offset:2048
	ds_read_b128 v[126:129], v126 offset:3072
	ds_read_b128 v[138:141], v150
	ds_read_b128 v[142:145], v150 offset:1024
	ds_read_b128 v[146:149], v150 offset:2048
	ds_read_b128 v[150:153], v150 offset:3072
	s_add_u32 s20, s26, 0xb0000
	s_addc_u32 s21, s27, 0
	s_mov_b32 m0, s29
	v_lshl_add_u64 v[218:219], s[20:21], 0, v[190:191]
	ds_read_b128 v[154:157], v236 offset:32768
	ds_read_b128 v[166:169], v236 offset:33792
	ds_read_b128 v[170:173], v236 offset:34816
	ds_read_b128 v[174:177], v236 offset:35840
	ds_read_b128 v[178:181], v236 offset:36864
	ds_read_b128 v[182:185], v236 offset:37888
	ds_read_b128 v[186:189], v236 offset:38912
	ds_read_b128 v[206:209], v236 offset:39936
	global_load_lds_dwordx4 v[218:219], off
	v_lshl_add_u64 v[218:219], s[20:21], 0, v[194:195]
	s_mov_b32 m0, s30
	s_nop 0
	global_load_lds_dwordx4 v[218:219], off
	s_waitcnt vmcnt(8)
	s_waitcnt lgkmcnt(0)
	s_barrier
	s_setprio 3
	s_waitcnt lgkmcnt(0)
	v_mfma_f32_16x16x32_bf16 v[162:165], v[98:101], v[154:157], v[162:165]
	v_mfma_f32_16x16x32_bf16 v[158:161], v[122:125], v[154:157], v[158:161]
	v_mfma_f32_16x16x32_bf16 v[118:121], v[98:101], v[170:173], v[118:121]
	v_mfma_f32_16x16x32_bf16 v[114:117], v[122:125], v[170:173], v[114:117]
	v_mfma_f32_16x16x32_bf16 v[94:97], v[98:101], v[178:181], v[94:97]
	v_mfma_f32_16x16x32_bf16 v[90:93], v[122:125], v[178:181], v[90:93]
	v_mfma_f32_16x16x32_bf16 v[78:81], v[98:101], v[186:189], v[78:81]
	v_mfma_f32_16x16x32_bf16 v[74:77], v[122:125], v[186:189], v[74:77]
	v_mfma_f32_16x16x32_bf16 v[162:165], v[110:113], v[166:169], v[162:165]
	v_mfma_f32_16x16x32_bf16 v[158:161], v[126:129], v[166:169], v[158:161]
	v_mfma_f32_16x16x32_bf16 v[118:121], v[110:113], v[174:177], v[118:121]
	v_mfma_f32_16x16x32_bf16 v[114:117], v[126:129], v[174:177], v[114:117]
	v_mfma_f32_16x16x32_bf16 v[94:97], v[110:113], v[182:185], v[94:97]
	v_mfma_f32_16x16x32_bf16 v[90:93], v[126:129], v[182:185], v[90:93]
	v_mfma_f32_16x16x32_bf16 v[78:81], v[110:113], v[206:209], v[78:81]
	v_mfma_f32_16x16x32_bf16 v[74:77], v[126:129], v[206:209], v[74:77]
	s_setprio 0
	s_setprio 3
	v_mfma_f32_16x16x32_bf16 v[134:137], v[138:141], v[154:157], v[134:137]
	v_mfma_f32_16x16x32_bf16 v[130:133], v[146:149], v[154:157], v[130:133]
	v_mfma_f32_16x16x32_bf16 v[106:109], v[138:141], v[170:173], v[106:109]
	v_mfma_f32_16x16x32_bf16 v[102:105], v[146:149], v[170:173], v[102:105]
	v_mfma_f32_16x16x32_bf16 v[86:89], v[138:141], v[178:181], v[86:89]
	v_mfma_f32_16x16x32_bf16 v[82:85], v[146:149], v[178:181], v[82:85]
	v_mfma_f32_16x16x32_bf16 v[70:73], v[138:141], v[186:189], v[70:73]
	v_mfma_f32_16x16x32_bf16 v[66:69], v[146:149], v[186:189], v[66:69]
	v_mfma_f32_16x16x32_bf16 v[134:137], v[142:145], v[166:169], v[134:137]
	v_mfma_f32_16x16x32_bf16 v[130:133], v[150:153], v[166:169], v[130:133]
	v_mfma_f32_16x16x32_bf16 v[106:109], v[142:145], v[174:177], v[106:109]
	v_mfma_f32_16x16x32_bf16 v[102:105], v[150:153], v[174:177], v[102:105]
	v_mfma_f32_16x16x32_bf16 v[86:89], v[142:145], v[182:185], v[86:89]
	v_mfma_f32_16x16x32_bf16 v[82:85], v[150:153], v[182:185], v[82:85]
	v_mfma_f32_16x16x32_bf16 v[70:73], v[142:145], v[206:209], v[70:73]
	v_mfma_f32_16x16x32_bf16 v[66:69], v[150:153], v[206:209], v[66:69]
	s_setprio 0
	s_barrier
; #define PG8_STAGE_A(b, h, ptr, NX) do { if constexpr (Sched::GATHER) { unsigned gs_[2]; gs_[0] = ((NX) && last_) ? gN[h][0] : gA[h][0]; gs_[1] = ((NX) && last_) ? gN[h][1] : gA[h][1]; PG8_STAGE(PG8_SA(b, h), ptr, gs_); } \
;         else PG8_STAGE(PG8_SA(b, h), (ptr) + ((h) ? hstep : (size_t)0), voffA); } while (0)
; #define PG8_STAGE(bufoff, gbase, voff) do { _Pragma("unroll") for (int _i = 0; _i < 2; ++_i) \
;         __builtin_amdgcn_global_load_lds((const unsigned*)((const char*)(gbase) + (voff)[_i]), (PG8_LAS unsigned*)(lds + (bufoff) + ldsw + _i * 8192), 16, 0, 0); } while (0)
; #define PG8_LDA(dst, b, h) do { _Pragma("unroll") for (int m = 0; m < 4; ++m) _Pragma("unroll") for (int k = 0; k < 2; ++k) dst[m][k] = *(const PG8_LAS bf16x8*)(lds + PG8_SA(b, h) + aoff + m * 2048 + k * 1024); } while (0)
; #define PG8_MMA(ai, bj, At, Bt) do { __builtin_amdgcn_s_setprio(1); _Pragma("unroll") for (int m = 0; m < 4; ++m) _Pragma("unroll") for (int n = 0; n < 2; ++n) _Pragma("unroll") for (int k = 0; k < 2; ++k) \
;         acc[ai][bj][m][n] = __builtin_amdgcn_mfma_f32_16x16x32_bf16(Bt[n][k], At[m][k], acc[ai][bj][m][n], 0, 0, 0); __builtin_amdgcn_s_setprio(0); } while (0)
; #define PG8_WAIT_V(n) asm volatile("s_waitcnt vmcnt(" #n ")" ::: "memory")
; #define PG8_WAIT_L(n) asm volatile("s_waitcnt lgkmcnt(" #n ")" ::: "memory")
; #define PG8_BAR __builtin_amdgcn_s_barrier()
; #define PG8_SCHED __builtin_amdgcn_sched_barrier(0)
; template <class Epi, class Sched, bool ALIGN_EPI = false, bool SP2 = false>
; __device__ __forceinline__ void gemm_phase(PG8_LAS unsigned char* lds, const Gemm g, const Sched& S, const Epi& E, const bool skip_epi = false) {
;     ...
;             PG8_LDA(At, 1, 1); PG8_STAGE(PG8_SB(1, 0), b3, voffB); PG8_STAGE(PG8_SB(1, 1), b3 + hstep, voffB); PG8_STAGE_A(1, 0, a3, true);
;             PG8_WAIT_V(8); PG8_WAIT_L(0); PG8_BAR; PG8_MMA(1, 0, At, B0); PG8_MMA(1, 1, At, B1); PG8_BAR; PG8_SCHED;
	s_add_i32 s20, s58, s2
	v_lshl_add_u64 v[210:211], v[210:211], 0, s[14:15]
	s_mov_b32 m0, s20
	ds_read_b128 v[154:157], v236 offset:49152
	ds_read_b128 v[166:169], v236 offset:50176
	ds_read_b128 v[170:173], v236 offset:51200
	ds_read_b128 v[174:177], v236 offset:52224
	ds_read_b128 v[178:181], v236 offset:53248
	ds_read_b128 v[182:185], v236 offset:54272
	ds_read_b128 v[186:189], v236 offset:55296
	ds_read_b128 v[206:209], v236 offset:56320
	global_load_lds_dwordx4 v[210:211], off
	s_add_i32 m0, s20, 0x2000
	s_add_u32 s20, s24, 0xb0080
	v_lshl_add_u64 v[210:211], v[212:213], 0, s[14:15]
	s_addc_u32 s21, s25, 0
	s_add_i32 s24, s59, s2
	global_load_lds_dwordx4 v[210:211], off
	v_lshl_add_u64 v[210:211], s[20:21], 0, v[192:193]
	s_mov_b32 m0, s24
	s_nop 0
	global_load_lds_dwordx4 v[210:211], off
	v_lshl_add_u64 v[210:211], s[20:21], 0, v[196:197]
	s_add_i32 m0, s24, 0x2000
	s_nop 0
	global_load_lds_dwordx4 v[210:211], off
	v_lshl_add_u64 v[210:211], v[214:215], 0, s[14:15]
	s_mov_b32 m0, s35
	s_nop 0
	global_load_lds_dwordx4 v[210:211], off
	v_lshl_add_u64 v[210:211], v[216:217], 0, s[14:15]
	s_mov_b32 m0, s36
	s_nop 0
	global_load_lds_dwordx4 v[210:211], off
	s_waitcnt vmcnt(8)
	s_waitcnt lgkmcnt(0)
	s_barrier
	s_setprio 3
	s_waitcnt lgkmcnt(0)
	v_mfma_f32_16x16x32_bf16 v[62:65], v[98:101], v[154:157], v[62:65]
	v_mfma_f32_16x16x32_bf16 v[58:61], v[122:125], v[154:157], v[58:61]
	v_mfma_f32_16x16x32_bf16 v[46:49], v[98:101], v[170:173], v[46:49]
	v_mfma_f32_16x16x32_bf16 v[42:45], v[122:125], v[170:173], v[42:45]
	v_mfma_f32_16x16x32_bf16 v[30:33], v[98:101], v[178:181], v[30:33]
	v_mfma_f32_16x16x32_bf16 v[26:29], v[122:125], v[178:181], v[26:29]
	v_mfma_f32_16x16x32_bf16 v[14:17], v[98:101], v[186:189], v[14:17]
	v_mfma_f32_16x16x32_bf16 v[10:13], v[122:125], v[186:189], v[10:13]
	v_mfma_f32_16x16x32_bf16 v[62:65], v[110:113], v[166:169], v[62:65]
	v_mfma_f32_16x16x32_bf16 v[58:61], v[126:129], v[166:169], v[58:61]
	v_mfma_f32_16x16x32_bf16 v[46:49], v[110:113], v[174:177], v[46:49]
	v_mfma_f32_16x16x32_bf16 v[42:45], v[126:129], v[174:177], v[42:45]
	v_mfma_f32_16x16x32_bf16 v[30:33], v[110:113], v[182:185], v[30:33]
	v_mfma_f32_16x16x32_bf16 v[26:29], v[126:129], v[182:185], v[26:29]
	v_mfma_f32_16x16x32_bf16 v[14:17], v[110:113], v[206:209], v[14:17]
	v_mfma_f32_16x16x32_bf16 v[10:13], v[126:129], v[206:209], v[10:13]
	s_setprio 0
	s_setprio 3
	v_mfma_f32_16x16x32_bf16 v[54:57], v[138:141], v[154:157], v[54:57]
	v_mfma_f32_16x16x32_bf16 v[50:53], v[146:149], v[154:157], v[50:53]
	v_mfma_f32_16x16x32_bf16 v[38:41], v[138:141], v[170:173], v[38:41]
	v_mfma_f32_16x16x32_bf16 v[34:37], v[146:149], v[170:173], v[34:37]
	v_mfma_f32_16x16x32_bf16 v[22:25], v[138:141], v[178:181], v[22:25]
	v_mfma_f32_16x16x32_bf16 v[18:21], v[146:149], v[178:181], v[18:21]
	v_mfma_f32_16x16x32_bf16 v[6:9], v[138:141], v[186:189], v[6:9]
	v_mfma_f32_16x16x32_bf16 v[2:5], v[146:149], v[186:189], v[2:5]
	v_mfma_f32_16x16x32_bf16 v[54:57], v[142:145], v[166:169], v[54:57]
	v_mfma_f32_16x16x32_bf16 v[50:53], v[150:153], v[166:169], v[50:53]
	v_mfma_f32_16x16x32_bf16 v[38:41], v[142:145], v[174:177], v[38:41]
	v_mfma_f32_16x16x32_bf16 v[34:37], v[150:153], v[174:177], v[34:37]
	v_mfma_f32_16x16x32_bf16 v[22:25], v[142:145], v[182:185], v[22:25]
	v_mfma_f32_16x16x32_bf16 v[18:21], v[150:153], v[182:185], v[18:21]
	v_mfma_f32_16x16x32_bf16 v[6:9], v[142:145], v[206:209], v[6:9]
	v_mfma_f32_16x16x32_bf16 v[2:5], v[150:153], v[206:209], v[2:5]
	s_setprio 0
	s_barrier
	s_add_i32 s57, s57, 2
	s_add_u32 s55, s55, 0x100
	s_addc_u32 s56, s56, 0
	s_cmp_gt_u32 s57, 41
	s_mov_b64 s[20:21], s[22:23]
	.p2align	3

; #define PG8_STAGE_A(b, h, ptr, NX) do { if constexpr (Sched::GATHER) { unsigned gs_[2]; gs_[0] = ((NX) && last_) ? gN[h][0] : gA[h][0]; gs_[1] = ((NX) && last_) ? gN[h][1] : gA[h][1]; PG8_STAGE(PG8_SA(b, h), ptr, gs_); } \
;         else PG8_STAGE(PG8_SA(b, h), (ptr) + ((h) ? hstep : (size_t)0), voffA); } while (0)
; #define PG8_STAGE(bufoff, gbase, voff) do { _Pragma("unroll") for (int _i = 0; _i < 2; ++_i) \
;         __builtin_amdgcn_global_load_lds((const unsigned*)((const char*)(gbase) + (voff)[_i]), (PG8_LAS unsigned*)(lds + (bufoff) + ldsw + _i * 8192), 16, 0, 0); } while (0)
; #define PG8_LDA(dst, b, h) do { _Pragma("unroll") for (int m = 0; m < 4; ++m) _Pragma("unroll") for (int k = 0; k < 2; ++k) dst[m][k] = *(const PG8_LAS bf16x8*)(lds + PG8_SA(b, h) + aoff + m * 2048 + k * 1024); } while (0)
; #define PG8_WAIT_V(n) asm volatile("s_waitcnt vmcnt(" #n ")" ::: "memory")
; #define PG8_WAIT_L(n) asm volatile("s_waitcnt lgkmcnt(" #n ")" ::: "memory")
; #define PG8_BAR __builtin_amdgcn_s_barrier()
; template <class Epi, class Sched, bool ALIGN_EPI = false, bool SP2 = false>
; __device__ __forceinline__ void gemm_phase(PG8_LAS unsigned char* lds, const Gemm g, const Sched& S, const Epi& E, const bool skip_epi = false) {
;     ...
;         const char* nA = has_next ? (const char*)g.A + (size_t)nxt.pm * pmstepA + nxt.ko : cA; const char* nB = has_next ? (const char*)g.Bt + (size_t)nxt.pn * tstep + nxt.ko : cB;
;         for (int t = 0; t < nt; t += 2) {
;             const bool last = (t == nt - 2); last_ = last && has_next;
;             const char* a1 = cA + (size_t)(t + 1) * kstep;
;             const char* a2 = last ? nA : cA + (size_t)(t + 2) * kstep; const char* b2 = last ? nB : cB + (size_t)(t + 2) * kstep;
;             const char* a3 = a2 + kstep; const char* b3 = b2 + kstep;
;             if (last && has_next) S.a_ready(nxt);
;             if constexpr (SP2) {
;             PG8_LDB(B0, 0, 0); PG8_LDB(B1, 0, 1); PG8_SCHED; PG8_LDA(At, 0, 0); PG8_STAGE_A(1, 1, a1, false);
;             PG8_WAIT_V(8); PG8_WAIT_L(0); PG8_BAR; PG8_MMA(0, 0, At, B0); PG8_MMA(0, 1, At, B1); PG8_BAR; PG8_SCHED;
;             PG8_LDA(At, 0, 1); PG8_STAGE(PG8_SB(0, 0), b2, voffB); PG8_STAGE(PG8_SB(0, 1), b2 + hstep, voffB); PG8_STAGE_A(0, 0, a2, true);
;             PG8_WAIT_V(8); PG8_WAIT_L(0); PG8_BAR; PG8_MMA(1, 0, At, B0); PG8_MMA(1, 1, At, B1); PG8_BAR; PG8_SCHED;
.LBB0_943:
	s_ashr_i32 s15, s14, 31
	s_lshl_b64 s[16:17], s[14:15], 19
	s_add_u32 s16, s86, s16
	s_addc_u32 s17, s87, s17
	s_and_b64 s[18:19], s[4:5], exec
	s_cselect_b32 s15, s17, s23
	s_cselect_b32 s54, s16, s22
	s_ashr_i32 s13, s12, 31
	s_lshl_b64 s[18:19], s[12:13], 19
	s_add_u32 s18, s2, s18
	s_addc_u32 s19, s3, s19
	s_and_b64 s[26:27], s[4:5], exec
	s_cselect_b32 s13, s19, s25
	s_cselect_b32 s55, s18, s24
	s_add_u32 s22, s22, 0x40080
	s_addc_u32 s23, s23, 0
	s_add_u32 s56, s24, 0x100
	s_addc_u32 s57, s25, 0
	s_mov_b32 s58, -2
	s_waitcnt vmcnt(0)
	ds_read_b128 v[148:151], v170
	ds_read_b128 v[152:155], v170 offset:1024
	ds_read_b128 v[156:159], v170 offset:2048
	ds_read_b128 v[160:163], v170 offset:3072
	ds_read_b128 v[176:179], v171
	ds_read_b128 v[180:183], v171 offset:1024
	ds_read_b128 v[184:187], v171 offset:2048
	ds_read_b128 v[188:191], v171 offset:3072
	s_add_u32 s24, s22, 0xfffc0080
	s_addc_u32 s25, s23, -1
	s_cmp_eq_u32 s58, 12
	s_cselect_b32 s27, s15, s25
	s_cselect_b32 s26, s54, s24
	s_cselect_b32 s25, s13, s57
	s_cselect_b32 s24, s55, s56
	v_lshl_add_u64 v[164:165], s[22:23], 0, v[140:141]
	s_add_i32 m0, s21, 0xc000
	ds_read_b128 v[192:195], v172
	ds_read_b128 v[196:199], v172 offset:1024
	ds_read_b128 v[200:203], v172 offset:2048
	ds_read_b128 v[204:207], v172 offset:3072
	ds_read_b128 v[208:211], v172 offset:4096
	ds_read_b128 v[212:215], v172 offset:5120
	ds_read_b128 v[216:219], v172 offset:6144
	ds_read_b128 v[220:223], v172 offset:7168
	global_load_lds_dwordx4 v[164:165], off
	v_lshl_add_u64 v[164:165], s[22:23], 0, v[142:143]
	s_add_i32 m0, s21, 0xe000
	s_nop 0
	global_load_lds_dwordx4 v[164:165], off
	s_waitcnt vmcnt(8)
	s_waitcnt lgkmcnt(0)
	s_barrier
	s_setprio 3
	s_waitcnt lgkmcnt(0)
	v_mfma_f32_16x16x32_bf16 v[126:129], v[148:151], v[192:195], 0
	v_mfma_f32_16x16x32_bf16 v[122:125], v[156:159], v[192:195], 0
	v_mfma_f32_16x16x32_bf16 v[114:117], v[148:151], v[200:203], 0
	v_mfma_f32_16x16x32_bf16 v[106:109], v[156:159], v[200:203], 0
	v_mfma_f32_16x16x32_bf16 v[98:101], v[148:151], v[208:211], 0
	v_mfma_f32_16x16x32_bf16 v[90:93], v[156:159], v[208:211], 0
	v_mfma_f32_16x16x32_bf16 v[82:85], v[148:151], v[216:219], 0
	v_mfma_f32_16x16x32_bf16 v[74:77], v[156:159], v[216:219], 0
	v_mfma_f32_16x16x32_bf16 v[126:129], v[152:155], v[196:199], v[126:129]
	v_mfma_f32_16x16x32_bf16 v[122:125], v[160:163], v[196:199], v[122:125]
	v_mfma_f32_16x16x32_bf16 v[114:117], v[152:155], v[204:207], v[114:117]
	v_mfma_f32_16x16x32_bf16 v[106:109], v[160:163], v[204:207], v[106:109]
	v_mfma_f32_16x16x32_bf16 v[98:101], v[152:155], v[212:215], v[98:101]
	v_mfma_f32_16x16x32_bf16 v[90:93], v[160:163], v[212:215], v[90:93]
	v_mfma_f32_16x16x32_bf16 v[82:85], v[152:155], v[220:223], v[82:85]
	v_mfma_f32_16x16x32_bf16 v[74:77], v[160:163], v[220:223], v[74:77]
	s_setprio 0
	s_setprio 3
	v_mfma_f32_16x16x32_bf16 v[118:121], v[176:179], v[192:195], 0
	v_mfma_f32_16x16x32_bf16 v[110:113], v[184:187], v[192:195], 0
	v_mfma_f32_16x16x32_bf16 v[102:105], v[176:179], v[200:203], 0
	v_mfma_f32_16x16x32_bf16 v[94:97], v[184:187], v[200:203], 0
	v_mfma_f32_16x16x32_bf16 v[86:89], v[176:179], v[208:211], 0
	v_mfma_f32_16x16x32_bf16 v[78:81], v[184:187], v[208:211], 0
	v_mfma_f32_16x16x32_bf16 v[70:73], v[176:179], v[216:219], 0
	v_mfma_f32_16x16x32_bf16 v[66:69], v[184:187], v[216:219], 0
	v_mfma_f32_16x16x32_bf16 v[118:121], v[180:183], v[196:199], v[118:121]
	v_mfma_f32_16x16x32_bf16 v[110:113], v[188:191], v[196:199], v[110:113]
	v_mfma_f32_16x16x32_bf16 v[102:105], v[180:183], v[204:207], v[102:105]
	v_mfma_f32_16x16x32_bf16 v[94:97], v[188:191], v[204:207], v[94:97]
	v_mfma_f32_16x16x32_bf16 v[86:89], v[180:183], v[212:215], v[86:89]
	v_mfma_f32_16x16x32_bf16 v[78:81], v[188:191], v[212:215], v[78:81]
	v_mfma_f32_16x16x32_bf16 v[70:73], v[180:183], v[220:223], v[70:73]
	v_mfma_f32_16x16x32_bf16 v[66:69], v[188:191], v[220:223], v[66:69]
	s_setprio 0
	s_barrier
	s_add_i32 s59, s48, s28
	v_lshl_add_u64 v[164:165], s[24:25], 0, v[134:135]
	s_mov_b32 m0, s59
	ds_read_b128 v[192:195], v172 offset:16384
	ds_read_b128 v[196:199], v172 offset:17408
	ds_read_b128 v[200:203], v172 offset:18432
	ds_read_b128 v[204:207], v172 offset:19456
	ds_read_b128 v[208:211], v172 offset:20480
	ds_read_b128 v[212:215], v172 offset:21504
	ds_read_b128 v[216:219], v172 offset:22528
	ds_read_b128 v[220:223], v172 offset:23552
	global_load_lds_dwordx4 v[164:165], off
	s_add_i32 m0, s59, 0x2000
	s_add_u32 s60, s24, 0x40000
	v_lshl_add_u64 v[224:225], s[24:25], 0, v[130:131]
	s_addc_u32 s61, s25, 0
	s_add_i32 s59, s49, s28
	global_load_lds_dwordx4 v[224:225], off
	v_lshl_add_u64 v[226:227], s[60:61], 0, v[134:135]
	s_mov_b32 m0, s59
	v_lshl_add_u64 v[230:231], s[26:27], 0, v[132:133]
	global_load_lds_dwordx4 v[226:227], off
	v_lshl_add_u64 v[226:227], s[60:61], 0, v[130:131]
	s_add_i32 m0, s59, 0x2000
	s_nop 0
	global_load_lds_dwordx4 v[226:227], off
	v_lshl_add_u64 v[226:227], s[26:27], 0, v[136:137]
	s_mov_b32 m0, s21
	s_nop 0
	global_load_lds_dwordx4 v[226:227], off
	s_mov_b32 m0, s31
	s_nop 0
	global_load_lds_dwordx4 v[230:231], off
	s_waitcnt vmcnt(8)
	s_waitcnt lgkmcnt(0)
	s_barrier
; #define PG8_STAGE_A(b, h, ptr, NX) do { if constexpr (Sched::GATHER) { unsigned gs_[2]; gs_[0] = ((NX) && last_) ? gN[h][0] : gA[h][0]; gs_[1] = ((NX) && last_) ? gN[h][1] : gA[h][1]; PG8_STAGE(PG8_SA(b, h), ptr, gs_); } \
;         else PG8_STAGE(PG8_SA(b, h), (ptr) + ((h) ? hstep : (size_t)0), voffA); } while (0)
; #define PG8_STAGE(bufoff, gbase, voff) do { _Pragma("unroll") for (int _i = 0; _i < 2; ++_i) \
;         __builtin_amdgcn_global_load_lds((const unsigned*)((const char*)(gbase) + (voff)[_i]), (PG8_LAS unsigned*)(lds + (bufoff) + ldsw + _i * 8192), 16, 0, 0); } while (0)
; #define PG8_LDA(dst, b, h) do { _Pragma("unroll") for (int m = 0; m < 4; ++m) _Pragma("unroll") for (int k = 0; k < 2; ++k) dst[m][k] = *(const PG8_LAS bf16x8*)(lds + PG8_SA(b, h) + aoff + m * 2048 + k * 1024); } while (0)
; #define PG8_LDB(dst, b, h) do { _Pragma("unroll") for (int n = 0; n < 2; ++n) _Pragma("unroll") for (int k = 0; k < 2; ++k) dst[n][k] = *(const PG8_LAS bf16x8*)(lds + PG8_SB(b, h) + boff + n * 2048 + k * 1024); } while (0)
; #define PG8_MMA(ai, bj, At, Bt) do { __builtin_amdgcn_s_setprio(1); _Pragma("unroll") for (int m = 0; m < 4; ++m) _Pragma("unroll") for (int n = 0; n < 2; ++n) _Pragma("unroll") for (int k = 0; k < 2; ++k) \
;         acc[ai][bj][m][n] = __builtin_amdgcn_mfma_f32_16x16x32_bf16(Bt[n][k], At[m][k], acc[ai][bj][m][n], 0, 0, 0); __builtin_amdgcn_s_setprio(0); } while (0)
; #define PG8_WAIT_V(n) asm volatile("s_waitcnt vmcnt(" #n ")" ::: "memory")
; #define PG8_WAIT_L(n) asm volatile("s_waitcnt lgkmcnt(" #n ")" ::: "memory")
; #define PG8_BAR __builtin_amdgcn_s_barrier()
; #define PG8_SCHED __builtin_amdgcn_sched_barrier(0)
; template <class Epi, class Sched, bool ALIGN_EPI = false, bool SP2 = false>
; __device__ __forceinline__ void gemm_phase(PG8_LAS unsigned char* lds, const Gemm g, const Sched& S, const Epi& E, const bool skip_epi = false) {
;     ...
;             PG8_WAIT_V(8); PG8_WAIT_L(0); PG8_BAR; PG8_MMA(1, 0, At, B0); PG8_MMA(1, 1, At, B1); PG8_BAR; PG8_SCHED;
;             PG8_LDB(B0, 1, 0); PG8_LDB(B1, 1, 1); PG8_SCHED; PG8_LDA(At, 1, 0); PG8_STAGE_A(0, 1, a2, true);
;             PG8_WAIT_V(8); PG8_WAIT_L(0); PG8_BAR; PG8_MMA(0, 0, At, B0); PG8_MMA(0, 1, At, B1); PG8_BAR; PG8_SCHED;
;             PG8_LDA(At, 1, 1); PG8_STAGE(PG8_SB(1, 0), b3, voffB); PG8_STAGE(PG8_SB(1, 1), b3 + hstep, voffB); PG8_STAGE_A(1, 0, a3, true);
	s_setprio 3
	s_waitcnt lgkmcnt(0)
	v_mfma_f32_16x16x32_bf16 v[62:65], v[148:151], v[192:195], 0
	v_mfma_f32_16x16x32_bf16 v[58:61], v[156:159], v[192:195], 0
	v_mfma_f32_16x16x32_bf16 v[50:53], v[148:151], v[200:203], 0
	v_mfma_f32_16x16x32_bf16 v[42:45], v[156:159], v[200:203], 0
	v_mfma_f32_16x16x32_bf16 v[34:37], v[148:151], v[208:211], 0
	v_mfma_f32_16x16x32_bf16 v[26:29], v[156:159], v[208:211], 0
	v_mfma_f32_16x16x32_bf16 v[18:21], v[148:151], v[216:219], 0
	v_mfma_f32_16x16x32_bf16 v[10:13], v[156:159], v[216:219], 0
	v_mfma_f32_16x16x32_bf16 v[62:65], v[152:155], v[196:199], v[62:65]
	v_mfma_f32_16x16x32_bf16 v[58:61], v[160:163], v[196:199], v[58:61]
	v_mfma_f32_16x16x32_bf16 v[50:53], v[152:155], v[204:207], v[50:53]
	v_mfma_f32_16x16x32_bf16 v[42:45], v[160:163], v[204:207], v[42:45]
	v_mfma_f32_16x16x32_bf16 v[34:37], v[152:155], v[212:215], v[34:37]
	v_mfma_f32_16x16x32_bf16 v[26:29], v[160:163], v[212:215], v[26:29]
	v_mfma_f32_16x16x32_bf16 v[18:21], v[152:155], v[220:223], v[18:21]
	v_mfma_f32_16x16x32_bf16 v[10:13], v[160:163], v[220:223], v[10:13]
	s_setprio 0
	s_setprio 3
	v_mfma_f32_16x16x32_bf16 v[54:57], v[176:179], v[192:195], 0
	v_mfma_f32_16x16x32_bf16 v[46:49], v[184:187], v[192:195], 0
	v_mfma_f32_16x16x32_bf16 v[38:41], v[176:179], v[200:203], 0
	v_mfma_f32_16x16x32_bf16 v[30:33], v[184:187], v[200:203], 0
	v_mfma_f32_16x16x32_bf16 v[22:25], v[176:179], v[208:211], 0
	v_mfma_f32_16x16x32_bf16 v[14:17], v[184:187], v[208:211], 0
	v_mfma_f32_16x16x32_bf16 v[6:9], v[176:179], v[216:219], 0
	v_mfma_f32_16x16x32_bf16 v[2:5], v[184:187], v[216:219], 0
	v_mfma_f32_16x16x32_bf16 v[54:57], v[180:183], v[196:199], v[54:57]
	v_mfma_f32_16x16x32_bf16 v[46:49], v[188:191], v[196:199], v[46:49]
	v_mfma_f32_16x16x32_bf16 v[38:41], v[180:183], v[204:207], v[38:41]
	v_mfma_f32_16x16x32_bf16 v[30:33], v[188:191], v[204:207], v[30:33]
	v_mfma_f32_16x16x32_bf16 v[22:25], v[180:183], v[212:215], v[22:25]
	v_mfma_f32_16x16x32_bf16 v[14:17], v[188:191], v[212:215], v[14:17]
	v_mfma_f32_16x16x32_bf16 v[6:9], v[180:183], v[220:223], v[6:9]
	v_mfma_f32_16x16x32_bf16 v[2:5], v[188:191], v[220:223], v[2:5]
	s_setprio 0
	s_barrier
	s_add_i32 s59, 0, 0x18000
	s_add_i32 s60, 0, 0x1c000
	v_add_u32_e32 v160, s59, v1
	v_add_u32_e32 v188, s60, v1
	ds_read_b128 v[148:151], v160
	ds_read_b128 v[152:155], v160 offset:1024
	ds_read_b128 v[156:159], v160 offset:2048
	ds_read_b128 v[160:163], v160 offset:3072
	ds_read_b128 v[176:179], v188
	ds_read_b128 v[180:183], v188 offset:1024
	ds_read_b128 v[184:187], v188 offset:2048
	ds_read_b128 v[188:191], v188 offset:3072
	s_add_u32 s26, s26, 0x40000
	s_addc_u32 s27, s27, 0
	s_mov_b32 m0, s34
	v_lshl_add_u64 v[232:233], s[26:27], 0, v[136:137]
	ds_read_b128 v[192:195], v172 offset:32768
	ds_read_b128 v[196:199], v172 offset:33792
	ds_read_b128 v[200:203], v172 offset:34816
	ds_read_b128 v[204:207], v172 offset:35840
	ds_read_b128 v[208:211], v172 offset:36864
	ds_read_b128 v[212:215], v172 offset:37888
	ds_read_b128 v[216:219], v172 offset:38912
	ds_read_b128 v[220:223], v172 offset:39936
	global_load_lds_dwordx4 v[232:233], off
	v_lshl_add_u64 v[232:233], s[26:27], 0, v[132:133]
	s_mov_b32 m0, s35
	s_nop 0
	global_load_lds_dwordx4 v[232:233], off
	s_waitcnt vmcnt(8)
	s_waitcnt lgkmcnt(0)
	s_barrier
	s_setprio 3
	s_waitcnt lgkmcnt(0)
	v_mfma_f32_16x16x32_bf16 v[126:129], v[148:151], v[192:195], v[126:129]
	v_mfma_f32_16x16x32_bf16 v[122:125], v[156:159], v[192:195], v[122:125]
	v_mfma_f32_16x16x32_bf16 v[114:117], v[148:151], v[200:203], v[114:117]
	v_mfma_f32_16x16x32_bf16 v[106:109], v[156:159], v[200:203], v[106:109]
	v_mfma_f32_16x16x32_bf16 v[98:101], v[148:151], v[208:211], v[98:101]
	v_mfma_f32_16x16x32_bf16 v[90:93], v[156:159], v[208:211], v[90:93]
	v_mfma_f32_16x16x32_bf16 v[82:85], v[148:151], v[216:219], v[82:85]
	v_mfma_f32_16x16x32_bf16 v[74:77], v[156:159], v[216:219], v[74:77]
	v_mfma_f32_16x16x32_bf16 v[126:129], v[152:155], v[196:199], v[126:129]
	v_mfma_f32_16x16x32_bf16 v[122:125], v[160:163], v[196:199], v[122:125]
	v_mfma_f32_16x16x32_bf16 v[114:117], v[152:155], v[204:207], v[114:117]
	v_mfma_f32_16x16x32_bf16 v[106:109], v[160:163], v[204:207], v[106:109]
	v_mfma_f32_16x16x32_bf16 v[98:101], v[152:155], v[212:215], v[98:101]
	v_mfma_f32_16x16x32_bf16 v[90:93], v[160:163], v[212:215], v[90:93]
	v_mfma_f32_16x16x32_bf16 v[82:85], v[152:155], v[220:223], v[82:85]
	v_mfma_f32_16x16x32_bf16 v[74:77], v[160:163], v[220:223], v[74:77]
	s_setprio 0
	s_setprio 3
	v_mfma_f32_16x16x32_bf16 v[118:121], v[176:179], v[192:195], v[118:121]
	v_mfma_f32_16x16x32_bf16 v[110:113], v[184:187], v[192:195], v[110:113]
	v_mfma_f32_16x16x32_bf16 v[102:105], v[176:179], v[200:203], v[102:105]
	v_mfma_f32_16x16x32_bf16 v[94:97], v[184:187], v[200:203], v[94:97]
	v_mfma_f32_16x16x32_bf16 v[86:89], v[176:179], v[208:211], v[86:89]
	v_mfma_f32_16x16x32_bf16 v[78:81], v[184:187], v[208:211], v[78:81]
	v_mfma_f32_16x16x32_bf16 v[70:73], v[176:179], v[216:219], v[70:73]
	v_mfma_f32_16x16x32_bf16 v[66:69], v[184:187], v[216:219], v[66:69]
	v_mfma_f32_16x16x32_bf16 v[118:121], v[180:183], v[196:199], v[118:121]
	v_mfma_f32_16x16x32_bf16 v[110:113], v[188:191], v[196:199], v[110:113]
	v_mfma_f32_16x16x32_bf16 v[102:105], v[180:183], v[204:207], v[102:105]
	v_mfma_f32_16x16x32_bf16 v[94:97], v[188:191], v[204:207], v[94:97]
	v_mfma_f32_16x16x32_bf16 v[86:89], v[180:183], v[212:215], v[86:89]
	v_mfma_f32_16x16x32_bf16 v[78:81], v[188:191], v[212:215], v[78:81]
	v_mfma_f32_16x16x32_bf16 v[70:73], v[180:183], v[220:223], v[70:73]
	v_mfma_f32_16x16x32_bf16 v[66:69], v[188:191], v[220:223], v[66:69]
	s_setprio 0
	s_barrier
; #define PG8_STAGE_A(b, h, ptr, NX) do { if constexpr (Sched::GATHER) { unsigned gs_[2]; gs_[0] = ((NX) && last_) ? gN[h][0] : gA[h][0]; gs_[1] = ((NX) && last_) ? gN[h][1] : gA[h][1]; PG8_STAGE(PG8_SA(b, h), ptr, gs_); } \
;         else PG8_STAGE(PG8_SA(b, h), (ptr) + ((h) ? hstep : (size_t)0), voffA); } while (0)
; #define PG8_STAGE(bufoff, gbase, voff) do { _Pragma("unroll") for (int _i = 0; _i < 2; ++_i) \
;         __builtin_amdgcn_global_load_lds((const unsigned*)((const char*)(gbase) + (voff)[_i]), (PG8_LAS unsigned*)(lds + (bufoff) + ldsw + _i * 8192), 16, 0, 0); } while (0)
; #define PG8_LDA(dst, b, h) do { _Pragma("unroll") for (int m = 0; m < 4; ++m) _Pragma("unroll") for (int k = 0; k < 2; ++k) dst[m][k] = *(const PG8_LAS bf16x8*)(lds + PG8_SA(b, h) + aoff + m * 2048 + k * 1024); } while (0)
; #define PG8_MMA(ai, bj, At, Bt) do { __builtin_amdgcn_s_setprio(1); _Pragma("unroll") for (int m = 0; m < 4; ++m) _Pragma("unroll") for (int n = 0; n < 2; ++n) _Pragma("unroll") for (int k = 0; k < 2; ++k) \
;         acc[ai][bj][m][n] = __builtin_amdgcn_mfma_f32_16x16x32_bf16(Bt[n][k], At[m][k], acc[ai][bj][m][n], 0, 0, 0); __builtin_amdgcn_s_setprio(0); } while (0)
; #define PG8_WAIT_V(n) asm volatile("s_waitcnt vmcnt(" #n ")" ::: "memory")
; #define PG8_WAIT_L(n) asm volatile("s_waitcnt lgkmcnt(" #n ")" ::: "memory")
; #define PG8_BAR __builtin_amdgcn_s_barrier()
; #define PG8_SCHED __builtin_amdgcn_sched_barrier(0)
; template <class Epi, class Sched, bool ALIGN_EPI = false, bool SP2 = false>
; __device__ __forceinline__ void gemm_phase(PG8_LAS unsigned char* lds, const Gemm g, const Sched& S, const Epi& E, const bool skip_epi = false) {
;     ...
;             PG8_LDA(At, 1, 1); PG8_STAGE(PG8_SB(1, 0), b3, voffB); PG8_STAGE(PG8_SB(1, 1), b3 + hstep, voffB); PG8_STAGE_A(1, 0, a3, true);
;             PG8_WAIT_V(8); PG8_WAIT_L(0); PG8_BAR; PG8_MMA(1, 0, At, B0); PG8_MMA(1, 1, At, B1); PG8_BAR; PG8_SCHED;
	s_add_i32 s26, s59, s28
	v_lshl_add_u64 v[164:165], v[164:165], 0, s[8:9]
	s_mov_b32 m0, s26
	ds_read_b128 v[192:195], v172 offset:49152
	ds_read_b128 v[196:199], v172 offset:50176
	ds_read_b128 v[200:203], v172 offset:51200
	ds_read_b128 v[204:207], v172 offset:52224
	ds_read_b128 v[208:211], v172 offset:53248
	ds_read_b128 v[212:215], v172 offset:54272
	ds_read_b128 v[216:219], v172 offset:55296
	ds_read_b128 v[220:223], v172 offset:56320
	global_load_lds_dwordx4 v[164:165], off
	s_add_i32 m0, s26, 0x2000
	s_add_u32 s24, s24, 0x40080
	v_lshl_add_u64 v[164:165], v[224:225], 0, s[8:9]
	s_addc_u32 s25, s25, 0
	s_add_i32 s26, s60, s28
	global_load_lds_dwordx4 v[164:165], off
	v_lshl_add_u64 v[164:165], s[24:25], 0, v[134:135]
	s_mov_b32 m0, s26
	s_nop 0
	global_load_lds_dwordx4 v[164:165], off
	v_lshl_add_u64 v[164:165], s[24:25], 0, v[130:131]
	s_add_i32 m0, s26, 0x2000
	s_nop 0
	global_load_lds_dwordx4 v[164:165], off
	v_lshl_add_u64 v[164:165], v[226:227], 0, s[8:9]
	s_mov_b32 m0, s37
	s_nop 0
	global_load_lds_dwordx4 v[164:165], off
	v_lshl_add_u64 v[164:165], v[230:231], 0, s[8:9]
	s_mov_b32 m0, s38
	s_nop 0
	global_load_lds_dwordx4 v[164:165], off
	s_waitcnt vmcnt(8)
	s_waitcnt lgkmcnt(0)
	s_barrier
	s_setprio 3
	s_waitcnt lgkmcnt(0)
	v_mfma_f32_16x16x32_bf16 v[62:65], v[148:151], v[192:195], v[62:65]
	v_mfma_f32_16x16x32_bf16 v[58:61], v[156:159], v[192:195], v[58:61]
	v_mfma_f32_16x16x32_bf16 v[50:53], v[148:151], v[200:203], v[50:53]
	v_mfma_f32_16x16x32_bf16 v[42:45], v[156:159], v[200:203], v[42:45]
	v_mfma_f32_16x16x32_bf16 v[34:37], v[148:151], v[208:211], v[34:37]
	v_mfma_f32_16x16x32_bf16 v[26:29], v[156:159], v[208:211], v[26:29]
	v_mfma_f32_16x16x32_bf16 v[18:21], v[148:151], v[216:219], v[18:21]
	v_mfma_f32_16x16x32_bf16 v[10:13], v[156:159], v[216:219], v[10:13]
	v_mfma_f32_16x16x32_bf16 v[62:65], v[152:155], v[196:199], v[62:65]
	v_mfma_f32_16x16x32_bf16 v[58:61], v[160:163], v[196:199], v[58:61]
	v_mfma_f32_16x16x32_bf16 v[50:53], v[152:155], v[204:207], v[50:53]
	v_mfma_f32_16x16x32_bf16 v[42:45], v[160:163], v[204:207], v[42:45]
	v_mfma_f32_16x16x32_bf16 v[34:37], v[152:155], v[212:215], v[34:37]
	v_mfma_f32_16x16x32_bf16 v[26:29], v[160:163], v[212:215], v[26:29]
	v_mfma_f32_16x16x32_bf16 v[18:21], v[152:155], v[220:223], v[18:21]
	v_mfma_f32_16x16x32_bf16 v[10:13], v[160:163], v[220:223], v[10:13]
	s_setprio 0
	s_setprio 3
	v_mfma_f32_16x16x32_bf16 v[54:57], v[176:179], v[192:195], v[54:57]
	v_mfma_f32_16x16x32_bf16 v[46:49], v[184:187], v[192:195], v[46:49]
	v_mfma_f32_16x16x32_bf16 v[38:41], v[176:179], v[200:203], v[38:41]
	v_mfma_f32_16x16x32_bf16 v[30:33], v[184:187], v[200:203], v[30:33]
	v_mfma_f32_16x16x32_bf16 v[22:25], v[176:179], v[208:211], v[22:25]
	v_mfma_f32_16x16x32_bf16 v[14:17], v[184:187], v[208:211], v[14:17]
	v_mfma_f32_16x16x32_bf16 v[6:9], v[176:179], v[216:219], v[6:9]
	v_mfma_f32_16x16x32_bf16 v[2:5], v[184:187], v[216:219], v[2:5]
	v_mfma_f32_16x16x32_bf16 v[54:57], v[180:183], v[196:199], v[54:57]
	v_mfma_f32_16x16x32_bf16 v[46:49], v[188:191], v[196:199], v[46:49]
	v_mfma_f32_16x16x32_bf16 v[38:41], v[180:183], v[204:207], v[38:41]
	v_mfma_f32_16x16x32_bf16 v[30:33], v[188:191], v[204:207], v[30:33]
	v_mfma_f32_16x16x32_bf16 v[22:25], v[180:183], v[212:215], v[22:25]
	v_mfma_f32_16x16x32_bf16 v[14:17], v[188:191], v[212:215], v[14:17]
	v_mfma_f32_16x16x32_bf16 v[6:9], v[180:183], v[220:223], v[6:9]
	v_mfma_f32_16x16x32_bf16 v[2:5], v[188:191], v[220:223], v[2:5]
	s_setprio 0
	s_barrier
	s_add_i32 s58, s58, 2
	s_add_u32 s22, s22, 0x100
	s_addc_u32 s23, s23, 0
	s_add_u32 s56, s56, 0x100
	s_addc_u32 s57, s57, 0
	s_cmp_gt_u32 s58, 13
	.p2align	3

; #define PG8_STAGE_A(b, h, ptr, NX) do { if constexpr (Sched::GATHER) { unsigned gs_[2]; gs_[0] = ((NX) && last_) ? gN[h][0] : gA[h][0]; gs_[1] = ((NX) && last_) ? gN[h][1] : gA[h][1]; PG8_STAGE(PG8_SA(b, h), ptr, gs_); } \
;         else PG8_STAGE(PG8_SA(b, h), (ptr) + ((h) ? hstep : (size_t)0), voffA); } while (0)
; #define PG8_STAGE(bufoff, gbase, voff) do { _Pragma("unroll") for (int _i = 0; _i < 2; ++_i) \
;         __builtin_amdgcn_global_load_lds((const unsigned*)((const char*)(gbase) + (voff)[_i]), (PG8_LAS unsigned*)(lds + (bufoff) + ldsw + _i * 8192), 16, 0, 0); } while (0)
; #define PG8_LDA(dst, b, h) do { _Pragma("unroll") for (int m = 0; m < 4; ++m) _Pragma("unroll") for (int k = 0; k < 2; ++k) dst[m][k] = *(const PG8_LAS bf16x8*)(lds + PG8_SA(b, h) + aoff + m * 2048 + k * 1024); } while (0)
; #define PG8_WAIT_V(n) asm volatile("s_waitcnt vmcnt(" #n ")" ::: "memory")
; #define PG8_WAIT_L(n) asm volatile("s_waitcnt lgkmcnt(" #n ")" ::: "memory")
; #define PG8_BAR __builtin_amdgcn_s_barrier()
; template <class Epi, class Sched, bool ALIGN_EPI = false, bool SP2 = false>
; __device__ __forceinline__ void gemm_phase(PG8_LAS unsigned char* lds, const Gemm g, const Sched& S, const Epi& E, const bool skip_epi = false) {
;     ...
;         const char* nA = has_next ? (const char*)g.A + (size_t)nxt.pm * pmstepA + nxt.ko : cA; const char* nB = has_next ? (const char*)g.Bt + (size_t)nxt.pn * tstep + nxt.ko : cB;
;         for (int t = 0; t < nt; t += 2) {
;             const bool last = (t == nt - 2); last_ = last && has_next;
;             const char* a1 = cA + (size_t)(t + 1) * kstep;
;             const char* a2 = last ? nA : cA + (size_t)(t + 2) * kstep; const char* b2 = last ? nB : cB + (size_t)(t + 2) * kstep;
;             const char* a3 = a2 + kstep; const char* b3 = b2 + kstep;
;             if (last && has_next) S.a_ready(nxt);
;             if constexpr (SP2) {
;             PG8_LDB(B0, 0, 0); PG8_LDB(B1, 0, 1); PG8_SCHED; PG8_LDA(At, 0, 0); PG8_STAGE_A(1, 1, a1, false);
;             PG8_WAIT_V(8); PG8_WAIT_L(0); PG8_BAR; PG8_MMA(0, 0, At, B0); PG8_MMA(0, 1, At, B1); PG8_BAR; PG8_SCHED;
;             PG8_LDA(At, 0, 1); PG8_STAGE(PG8_SB(0, 0), b2, voffB); PG8_STAGE(PG8_SB(0, 1), b2 + hstep, voffB); PG8_STAGE_A(0, 0, a2, true);
;             PG8_WAIT_V(8); PG8_WAIT_L(0); PG8_BAR; PG8_MMA(1, 0, At, B0); PG8_MMA(1, 1, At, B1); PG8_BAR; PG8_SCHED;
.LBB0_1323:
	s_ashr_i32 s25, s24, 31
	s_lshl_b64 s[26:27], s[24:25], 19
	s_add_u32 s26, s46, s26
	s_addc_u32 s27, s47, s27
	s_and_b64 s[28:29], s[6:7], exec
	s_cselect_b32 s25, s27, s35
	s_cselect_b32 s31, s26, s34
	s_ashr_i32 s23, s22, 31
	s_lshl_b64 s[28:29], s[22:23], 19
	s_add_u32 s28, s2, s28
	s_addc_u32 s29, s3, s29
	s_and_b64 s[38:39], s[6:7], exec
	s_cselect_b32 s23, s29, s37
	s_cselect_b32 s60, s28, s36
	s_add_u32 s34, s34, 0x40080
	s_addc_u32 s35, s35, 0
	s_add_u32 s61, s36, 0x100
	s_addc_u32 s62, s37, 0
	s_mov_b32 s63, -2
	s_waitcnt vmcnt(0)
	s_waitcnt lgkmcnt(0)
	ds_read_b128 v[98:101], v225
	ds_read_b128 v[110:113], v225 offset:1024
	ds_read_b128 v[122:125], v225 offset:2048
	ds_read_b128 v[130:133], v225 offset:3072
	ds_read_b128 v[146:149], v226
	ds_read_b128 v[150:153], v226 offset:1024
	ds_read_b128 v[154:157], v226 offset:2048
	ds_read_b128 v[158:161], v226 offset:3072
	s_add_u32 s36, s34, 0xfffc0080
	s_addc_u32 s37, s35, -1
	s_cmp_eq_u32 s63, 12
	s_cselect_b32 s39, s25, s37
	s_cselect_b32 s38, s31, s36
	s_cselect_b32 s37, s23, s62
	s_cselect_b32 s36, s60, s61
	v_lshl_add_u64 v[210:211], s[34:35], 0, v[194:195]
	s_add_i32 m0, s41, 0xc000
	ds_read_b128 v[162:165], v227
	ds_read_b128 v[166:169], v227 offset:1024
	ds_read_b128 v[170:173], v227 offset:2048
	ds_read_b128 v[174:177], v227 offset:3072
	ds_read_b128 v[178:181], v227 offset:4096
	ds_read_b128 v[182:185], v227 offset:5120
	ds_read_b128 v[202:205], v227 offset:6144
	ds_read_b128 v[206:209], v227 offset:7168
	global_load_lds_dwordx4 v[210:211], off
	v_lshl_add_u64 v[210:211], s[34:35], 0, v[196:197]
	s_add_i32 m0, s41, 0xe000
	s_nop 0
	global_load_lds_dwordx4 v[210:211], off
	s_waitcnt vmcnt(8)
	s_waitcnt lgkmcnt(0)
	s_barrier
	s_setprio 3
	s_waitcnt lgkmcnt(0)
	v_mfma_f32_16x16x32_bf16 v[142:145], v[98:101], v[162:165], 0
	v_mfma_f32_16x16x32_bf16 v[138:141], v[122:125], v[162:165], 0
	v_mfma_f32_16x16x32_bf16 v[118:121], v[98:101], v[170:173], 0
	v_mfma_f32_16x16x32_bf16 v[114:117], v[122:125], v[170:173], 0
	v_mfma_f32_16x16x32_bf16 v[94:97], v[98:101], v[178:181], 0
	v_mfma_f32_16x16x32_bf16 v[90:93], v[122:125], v[178:181], 0
	v_mfma_f32_16x16x32_bf16 v[78:81], v[98:101], v[202:205], 0
	v_mfma_f32_16x16x32_bf16 v[74:77], v[122:125], v[202:205], 0
	v_mfma_f32_16x16x32_bf16 v[142:145], v[110:113], v[166:169], v[142:145]
	v_mfma_f32_16x16x32_bf16 v[138:141], v[130:133], v[166:169], v[138:141]
	v_mfma_f32_16x16x32_bf16 v[118:121], v[110:113], v[174:177], v[118:121]
	v_mfma_f32_16x16x32_bf16 v[114:117], v[130:133], v[174:177], v[114:117]
	v_mfma_f32_16x16x32_bf16 v[94:97], v[110:113], v[182:185], v[94:97]
	v_mfma_f32_16x16x32_bf16 v[90:93], v[130:133], v[182:185], v[90:93]
	v_mfma_f32_16x16x32_bf16 v[78:81], v[110:113], v[206:209], v[78:81]
	v_mfma_f32_16x16x32_bf16 v[74:77], v[130:133], v[206:209], v[74:77]
	s_setprio 0
	s_setprio 3
	v_mfma_f32_16x16x32_bf16 v[134:137], v[146:149], v[162:165], 0
	v_mfma_f32_16x16x32_bf16 v[126:129], v[154:157], v[162:165], 0
	v_mfma_f32_16x16x32_bf16 v[106:109], v[146:149], v[170:173], 0
	v_mfma_f32_16x16x32_bf16 v[102:105], v[154:157], v[170:173], 0
	v_mfma_f32_16x16x32_bf16 v[86:89], v[146:149], v[178:181], 0
	v_mfma_f32_16x16x32_bf16 v[82:85], v[154:157], v[178:181], 0
	v_mfma_f32_16x16x32_bf16 v[70:73], v[146:149], v[202:205], 0
	v_mfma_f32_16x16x32_bf16 v[66:69], v[154:157], v[202:205], 0
	v_mfma_f32_16x16x32_bf16 v[134:137], v[150:153], v[166:169], v[134:137]
	v_mfma_f32_16x16x32_bf16 v[126:129], v[158:161], v[166:169], v[126:129]
	v_mfma_f32_16x16x32_bf16 v[106:109], v[150:153], v[174:177], v[106:109]
	v_mfma_f32_16x16x32_bf16 v[102:105], v[158:161], v[174:177], v[102:105]
	v_mfma_f32_16x16x32_bf16 v[86:89], v[150:153], v[182:185], v[86:89]
	v_mfma_f32_16x16x32_bf16 v[82:85], v[158:161], v[182:185], v[82:85]
	v_mfma_f32_16x16x32_bf16 v[70:73], v[150:153], v[206:209], v[70:73]
	v_mfma_f32_16x16x32_bf16 v[66:69], v[158:161], v[206:209], v[66:69]
	s_setprio 0
	s_barrier
	s_add_i32 s64, s57, s40
	v_lshl_add_u64 v[210:211], s[36:37], 0, v[188:189]
	s_mov_b32 m0, s64
	ds_read_b128 v[162:165], v227 offset:16384
	ds_read_b128 v[166:169], v227 offset:17408
	ds_read_b128 v[170:173], v227 offset:18432
	ds_read_b128 v[174:177], v227 offset:19456
	ds_read_b128 v[178:181], v227 offset:20480
	ds_read_b128 v[182:185], v227 offset:21504
	ds_read_b128 v[202:205], v227 offset:22528
	ds_read_b128 v[206:209], v227 offset:23552
	global_load_lds_dwordx4 v[210:211], off
	s_add_i32 m0, s64, 0x2000
	s_add_u32 s64, s36, 0x40000
	v_lshl_add_u64 v[212:213], s[36:37], 0, v[192:193]
	s_addc_u32 s65, s37, 0
	s_add_i32 s66, s58, s40
	global_load_lds_dwordx4 v[212:213], off
	v_lshl_add_u64 v[214:215], s[64:65], 0, v[188:189]
	s_mov_b32 m0, s66
	v_lshl_add_u64 v[216:217], s[38:39], 0, v[190:191]
	global_load_lds_dwordx4 v[214:215], off
	v_lshl_add_u64 v[214:215], s[64:65], 0, v[192:193]
	s_add_i32 m0, s66, 0x2000
	s_nop 0
	global_load_lds_dwordx4 v[214:215], off
	v_lshl_add_u64 v[214:215], s[38:39], 0, v[186:187]
	s_mov_b32 m0, s41
	s_nop 0
	global_load_lds_dwordx4 v[214:215], off
	s_mov_b32 m0, s44
	s_nop 0
	global_load_lds_dwordx4 v[216:217], off
	s_waitcnt vmcnt(8)
	s_waitcnt lgkmcnt(0)
	s_barrier
; #define PG8_STAGE_A(b, h, ptr, NX) do { if constexpr (Sched::GATHER) { unsigned gs_[2]; gs_[0] = ((NX) && last_) ? gN[h][0] : gA[h][0]; gs_[1] = ((NX) && last_) ? gN[h][1] : gA[h][1]; PG8_STAGE(PG8_SA(b, h), ptr, gs_); } \
;         else PG8_STAGE(PG8_SA(b, h), (ptr) + ((h) ? hstep : (size_t)0), voffA); } while (0)
; #define PG8_STAGE(bufoff, gbase, voff) do { _Pragma("unroll") for (int _i = 0; _i < 2; ++_i) \
;         __builtin_amdgcn_global_load_lds((const unsigned*)((const char*)(gbase) + (voff)[_i]), (PG8_LAS unsigned*)(lds + (bufoff) + ldsw + _i * 8192), 16, 0, 0); } while (0)
; #define PG8_LDA(dst, b, h) do { _Pragma("unroll") for (int m = 0; m < 4; ++m) _Pragma("unroll") for (int k = 0; k < 2; ++k) dst[m][k] = *(const PG8_LAS bf16x8*)(lds + PG8_SA(b, h) + aoff + m * 2048 + k * 1024); } while (0)
; #define PG8_LDB(dst, b, h) do { _Pragma("unroll") for (int n = 0; n < 2; ++n) _Pragma("unroll") for (int k = 0; k < 2; ++k) dst[n][k] = *(const PG8_LAS bf16x8*)(lds + PG8_SB(b, h) + boff + n * 2048 + k * 1024); } while (0)
; #define PG8_MMA(ai, bj, At, Bt) do { __builtin_amdgcn_s_setprio(1); _Pragma("unroll") for (int m = 0; m < 4; ++m) _Pragma("unroll") for (int n = 0; n < 2; ++n) _Pragma("unroll") for (int k = 0; k < 2; ++k) \
;         acc[ai][bj][m][n] = __builtin_amdgcn_mfma_f32_16x16x32_bf16(Bt[n][k], At[m][k], acc[ai][bj][m][n], 0, 0, 0); __builtin_amdgcn_s_setprio(0); } while (0)
; #define PG8_WAIT_V(n) asm volatile("s_waitcnt vmcnt(" #n ")" ::: "memory")
; #define PG8_WAIT_L(n) asm volatile("s_waitcnt lgkmcnt(" #n ")" ::: "memory")
; #define PG8_BAR __builtin_amdgcn_s_barrier()
; #define PG8_SCHED __builtin_amdgcn_sched_barrier(0)
; template <class Epi, class Sched, bool ALIGN_EPI = false, bool SP2 = false>
; __device__ __forceinline__ void gemm_phase(PG8_LAS unsigned char* lds, const Gemm g, const Sched& S, const Epi& E, const bool skip_epi = false) {
;     ...
;             PG8_WAIT_V(8); PG8_WAIT_L(0); PG8_BAR; PG8_MMA(1, 0, At, B0); PG8_MMA(1, 1, At, B1); PG8_BAR; PG8_SCHED;
;             PG8_LDB(B0, 1, 0); PG8_LDB(B1, 1, 1); PG8_SCHED; PG8_LDA(At, 1, 0); PG8_STAGE_A(0, 1, a2, true);
;             PG8_WAIT_V(8); PG8_WAIT_L(0); PG8_BAR; PG8_MMA(0, 0, At, B0); PG8_MMA(0, 1, At, B1); PG8_BAR; PG8_SCHED;
;             PG8_LDA(At, 1, 1); PG8_STAGE(PG8_SB(1, 0), b3, voffB); PG8_STAGE(PG8_SB(1, 1), b3 + hstep, voffB); PG8_STAGE_A(1, 0, a3, true);
	s_setprio 3
	s_waitcnt lgkmcnt(0)
	v_mfma_f32_16x16x32_bf16 v[62:65], v[98:101], v[162:165], 0
	v_mfma_f32_16x16x32_bf16 v[58:61], v[122:125], v[162:165], 0
	v_mfma_f32_16x16x32_bf16 v[46:49], v[98:101], v[170:173], 0
	v_mfma_f32_16x16x32_bf16 v[42:45], v[122:125], v[170:173], 0
	v_mfma_f32_16x16x32_bf16 v[30:33], v[98:101], v[178:181], 0
	v_mfma_f32_16x16x32_bf16 v[26:29], v[122:125], v[178:181], 0
	v_mfma_f32_16x16x32_bf16 v[14:17], v[98:101], v[202:205], 0
	v_mfma_f32_16x16x32_bf16 v[10:13], v[122:125], v[202:205], 0
	v_mfma_f32_16x16x32_bf16 v[62:65], v[110:113], v[166:169], v[62:65]
	v_mfma_f32_16x16x32_bf16 v[58:61], v[130:133], v[166:169], v[58:61]
	v_mfma_f32_16x16x32_bf16 v[46:49], v[110:113], v[174:177], v[46:49]
	v_mfma_f32_16x16x32_bf16 v[42:45], v[130:133], v[174:177], v[42:45]
	v_mfma_f32_16x16x32_bf16 v[30:33], v[110:113], v[182:185], v[30:33]
	v_mfma_f32_16x16x32_bf16 v[26:29], v[130:133], v[182:185], v[26:29]
	v_mfma_f32_16x16x32_bf16 v[14:17], v[110:113], v[206:209], v[14:17]
	v_mfma_f32_16x16x32_bf16 v[10:13], v[130:133], v[206:209], v[10:13]
	s_setprio 0
	s_setprio 3
	v_mfma_f32_16x16x32_bf16 v[54:57], v[146:149], v[162:165], 0
	v_mfma_f32_16x16x32_bf16 v[50:53], v[154:157], v[162:165], 0
	v_mfma_f32_16x16x32_bf16 v[38:41], v[146:149], v[170:173], 0
	v_mfma_f32_16x16x32_bf16 v[34:37], v[154:157], v[170:173], 0
	v_mfma_f32_16x16x32_bf16 v[22:25], v[146:149], v[178:181], 0
	v_mfma_f32_16x16x32_bf16 v[18:21], v[154:157], v[178:181], 0
	v_mfma_f32_16x16x32_bf16 v[6:9], v[146:149], v[202:205], 0
	v_mfma_f32_16x16x32_bf16 v[2:5], v[154:157], v[202:205], 0
	v_mfma_f32_16x16x32_bf16 v[54:57], v[150:153], v[166:169], v[54:57]
	v_mfma_f32_16x16x32_bf16 v[50:53], v[158:161], v[166:169], v[50:53]
	v_mfma_f32_16x16x32_bf16 v[38:41], v[150:153], v[174:177], v[38:41]
	v_mfma_f32_16x16x32_bf16 v[34:37], v[158:161], v[174:177], v[34:37]
	v_mfma_f32_16x16x32_bf16 v[22:25], v[150:153], v[182:185], v[22:25]
	v_mfma_f32_16x16x32_bf16 v[18:21], v[158:161], v[182:185], v[18:21]
	v_mfma_f32_16x16x32_bf16 v[6:9], v[150:153], v[206:209], v[6:9]
	v_mfma_f32_16x16x32_bf16 v[2:5], v[158:161], v[206:209], v[2:5]
	s_setprio 0
	s_barrier
	s_add_i32 s64, 0, 0x18000
	s_add_i32 s65, 0, 0x1c000
	v_add_u32_e32 v130, s64, v220
	v_add_u32_e32 v158, s65, v220
	ds_read_b128 v[98:101], v130
	ds_read_b128 v[110:113], v130 offset:1024
	ds_read_b128 v[122:125], v130 offset:2048
	ds_read_b128 v[130:133], v130 offset:3072
	ds_read_b128 v[146:149], v158
	ds_read_b128 v[150:153], v158 offset:1024
	ds_read_b128 v[154:157], v158 offset:2048
	ds_read_b128 v[158:161], v158 offset:3072
	s_add_u32 s38, s38, 0x40000
	s_addc_u32 s39, s39, 0
	s_mov_b32 m0, s45
	v_lshl_add_u64 v[218:219], s[38:39], 0, v[186:187]
	ds_read_b128 v[162:165], v227 offset:32768
	ds_read_b128 v[166:169], v227 offset:33792
	ds_read_b128 v[170:173], v227 offset:34816
	ds_read_b128 v[174:177], v227 offset:35840
	ds_read_b128 v[178:181], v227 offset:36864
	ds_read_b128 v[182:185], v227 offset:37888
	ds_read_b128 v[202:205], v227 offset:38912
	ds_read_b128 v[206:209], v227 offset:39936
	global_load_lds_dwordx4 v[218:219], off
	v_lshl_add_u64 v[218:219], s[38:39], 0, v[190:191]
	s_mov_b32 m0, s48
	s_nop 0
	global_load_lds_dwordx4 v[218:219], off
	s_waitcnt vmcnt(8)
	s_waitcnt lgkmcnt(0)
	s_barrier
	s_setprio 3
	s_waitcnt lgkmcnt(0)
	v_mfma_f32_16x16x32_bf16 v[142:145], v[98:101], v[162:165], v[142:145]
	v_mfma_f32_16x16x32_bf16 v[138:141], v[122:125], v[162:165], v[138:141]
	v_mfma_f32_16x16x32_bf16 v[118:121], v[98:101], v[170:173], v[118:121]
	v_mfma_f32_16x16x32_bf16 v[114:117], v[122:125], v[170:173], v[114:117]
	v_mfma_f32_16x16x32_bf16 v[94:97], v[98:101], v[178:181], v[94:97]
	v_mfma_f32_16x16x32_bf16 v[90:93], v[122:125], v[178:181], v[90:93]
	v_mfma_f32_16x16x32_bf16 v[78:81], v[98:101], v[202:205], v[78:81]
	v_mfma_f32_16x16x32_bf16 v[74:77], v[122:125], v[202:205], v[74:77]
	v_mfma_f32_16x16x32_bf16 v[142:145], v[110:113], v[166:169], v[142:145]
	v_mfma_f32_16x16x32_bf16 v[138:141], v[130:133], v[166:169], v[138:141]
	v_mfma_f32_16x16x32_bf16 v[118:121], v[110:113], v[174:177], v[118:121]
	v_mfma_f32_16x16x32_bf16 v[114:117], v[130:133], v[174:177], v[114:117]
	v_mfma_f32_16x16x32_bf16 v[94:97], v[110:113], v[182:185], v[94:97]
	v_mfma_f32_16x16x32_bf16 v[90:93], v[130:133], v[182:185], v[90:93]
	v_mfma_f32_16x16x32_bf16 v[78:81], v[110:113], v[206:209], v[78:81]
	v_mfma_f32_16x16x32_bf16 v[74:77], v[130:133], v[206:209], v[74:77]
	s_setprio 0
	s_setprio 3
	v_mfma_f32_16x16x32_bf16 v[134:137], v[146:149], v[162:165], v[134:137]
	v_mfma_f32_16x16x32_bf16 v[126:129], v[154:157], v[162:165], v[126:129]
	v_mfma_f32_16x16x32_bf16 v[106:109], v[146:149], v[170:173], v[106:109]
	v_mfma_f32_16x16x32_bf16 v[102:105], v[154:157], v[170:173], v[102:105]
	v_mfma_f32_16x16x32_bf16 v[86:89], v[146:149], v[178:181], v[86:89]
	v_mfma_f32_16x16x32_bf16 v[82:85], v[154:157], v[178:181], v[82:85]
	v_mfma_f32_16x16x32_bf16 v[70:73], v[146:149], v[202:205], v[70:73]
	v_mfma_f32_16x16x32_bf16 v[66:69], v[154:157], v[202:205], v[66:69]
	v_mfma_f32_16x16x32_bf16 v[134:137], v[150:153], v[166:169], v[134:137]
	v_mfma_f32_16x16x32_bf16 v[126:129], v[158:161], v[166:169], v[126:129]
	v_mfma_f32_16x16x32_bf16 v[106:109], v[150:153], v[174:177], v[106:109]
	v_mfma_f32_16x16x32_bf16 v[102:105], v[158:161], v[174:177], v[102:105]
	v_mfma_f32_16x16x32_bf16 v[86:89], v[150:153], v[182:185], v[86:89]
	v_mfma_f32_16x16x32_bf16 v[82:85], v[158:161], v[182:185], v[82:85]
	v_mfma_f32_16x16x32_bf16 v[70:73], v[150:153], v[206:209], v[70:73]
	v_mfma_f32_16x16x32_bf16 v[66:69], v[158:161], v[206:209], v[66:69]
	s_setprio 0
	s_barrier
; #define PG8_STAGE_A(b, h, ptr, NX) do { if constexpr (Sched::GATHER) { unsigned gs_[2]; gs_[0] = ((NX) && last_) ? gN[h][0] : gA[h][0]; gs_[1] = ((NX) && last_) ? gN[h][1] : gA[h][1]; PG8_STAGE(PG8_SA(b, h), ptr, gs_); } \
;         else PG8_STAGE(PG8_SA(b, h), (ptr) + ((h) ? hstep : (size_t)0), voffA); } while (0)
; #define PG8_STAGE(bufoff, gbase, voff) do { _Pragma("unroll") for (int _i = 0; _i < 2; ++_i) \
;         __builtin_amdgcn_global_load_lds((const unsigned*)((const char*)(gbase) + (voff)[_i]), (PG8_LAS unsigned*)(lds + (bufoff) + ldsw + _i * 8192), 16, 0, 0); } while (0)
; #define PG8_LDA(dst, b, h) do { _Pragma("unroll") for (int m = 0; m < 4; ++m) _Pragma("unroll") for (int k = 0; k < 2; ++k) dst[m][k] = *(const PG8_LAS bf16x8*)(lds + PG8_SA(b, h) + aoff + m * 2048 + k * 1024); } while (0)
; #define PG8_MMA(ai, bj, At, Bt) do { __builtin_amdgcn_s_setprio(1); _Pragma("unroll") for (int m = 0; m < 4; ++m) _Pragma("unroll") for (int n = 0; n < 2; ++n) _Pragma("unroll") for (int k = 0; k < 2; ++k) \
;         acc[ai][bj][m][n] = __builtin_amdgcn_mfma_f32_16x16x32_bf16(Bt[n][k], At[m][k], acc[ai][bj][m][n], 0, 0, 0); __builtin_amdgcn_s_setprio(0); } while (0)
; #define PG8_WAIT_V(n) asm volatile("s_waitcnt vmcnt(" #n ")" ::: "memory")
; #define PG8_WAIT_L(n) asm volatile("s_waitcnt lgkmcnt(" #n ")" ::: "memory")
; #define PG8_BAR __builtin_amdgcn_s_barrier()
; #define PG8_SCHED __builtin_amdgcn_sched_barrier(0)
; template <class Epi, class Sched, bool ALIGN_EPI = false, bool SP2 = false>
; __device__ __forceinline__ void gemm_phase(PG8_LAS unsigned char* lds, const Gemm g, const Sched& S, const Epi& E, const bool skip_epi = false) {
;     ...
;             PG8_LDA(At, 1, 1); PG8_STAGE(PG8_SB(1, 0), b3, voffB); PG8_STAGE(PG8_SB(1, 1), b3 + hstep, voffB); PG8_STAGE_A(1, 0, a3, true);
;             PG8_WAIT_V(8); PG8_WAIT_L(0); PG8_BAR; PG8_MMA(1, 0, At, B0); PG8_MMA(1, 1, At, B1); PG8_BAR; PG8_SCHED;
	s_add_i32 s38, s64, s40
	v_lshl_add_u64 v[210:211], v[210:211], 0, s[12:13]
	s_mov_b32 m0, s38
	ds_read_b128 v[162:165], v227 offset:49152
	ds_read_b128 v[166:169], v227 offset:50176
	ds_read_b128 v[170:173], v227 offset:51200
	ds_read_b128 v[174:177], v227 offset:52224
	ds_read_b128 v[178:181], v227 offset:53248
	ds_read_b128 v[182:185], v227 offset:54272
	ds_read_b128 v[202:205], v227 offset:55296
	ds_read_b128 v[206:209], v227 offset:56320
	global_load_lds_dwordx4 v[210:211], off
	s_add_i32 m0, s38, 0x2000
	s_add_u32 s36, s36, 0x40080
	v_lshl_add_u64 v[210:211], v[212:213], 0, s[12:13]
	s_addc_u32 s37, s37, 0
	s_add_i32 s38, s65, s40
	global_load_lds_dwordx4 v[210:211], off
	v_lshl_add_u64 v[210:211], s[36:37], 0, v[188:189]
	s_mov_b32 m0, s38
	s_nop 0
	global_load_lds_dwordx4 v[210:211], off
	v_lshl_add_u64 v[210:211], s[36:37], 0, v[192:193]
	s_add_i32 m0, s38, 0x2000
	s_nop 0
	global_load_lds_dwordx4 v[210:211], off
	v_lshl_add_u64 v[210:211], v[214:215], 0, s[12:13]
	s_mov_b32 m0, s53
	s_nop 0
	global_load_lds_dwordx4 v[210:211], off
	v_lshl_add_u64 v[210:211], v[216:217], 0, s[12:13]
	s_mov_b32 m0, s54
	s_nop 0
	global_load_lds_dwordx4 v[210:211], off
	s_waitcnt vmcnt(8)
	s_waitcnt lgkmcnt(0)
	s_barrier
	s_setprio 3
	s_waitcnt lgkmcnt(0)
	v_mfma_f32_16x16x32_bf16 v[62:65], v[98:101], v[162:165], v[62:65]
	v_mfma_f32_16x16x32_bf16 v[58:61], v[122:125], v[162:165], v[58:61]
	v_mfma_f32_16x16x32_bf16 v[46:49], v[98:101], v[170:173], v[46:49]
	v_mfma_f32_16x16x32_bf16 v[42:45], v[122:125], v[170:173], v[42:45]
	v_mfma_f32_16x16x32_bf16 v[30:33], v[98:101], v[178:181], v[30:33]
	v_mfma_f32_16x16x32_bf16 v[26:29], v[122:125], v[178:181], v[26:29]
	v_mfma_f32_16x16x32_bf16 v[14:17], v[98:101], v[202:205], v[14:17]
	v_mfma_f32_16x16x32_bf16 v[10:13], v[122:125], v[202:205], v[10:13]
	v_mfma_f32_16x16x32_bf16 v[62:65], v[110:113], v[166:169], v[62:65]
	v_mfma_f32_16x16x32_bf16 v[58:61], v[130:133], v[166:169], v[58:61]
	v_mfma_f32_16x16x32_bf16 v[46:49], v[110:113], v[174:177], v[46:49]
	v_mfma_f32_16x16x32_bf16 v[42:45], v[130:133], v[174:177], v[42:45]
	v_mfma_f32_16x16x32_bf16 v[30:33], v[110:113], v[182:185], v[30:33]
	v_mfma_f32_16x16x32_bf16 v[26:29], v[130:133], v[182:185], v[26:29]
	v_mfma_f32_16x16x32_bf16 v[14:17], v[110:113], v[206:209], v[14:17]
	v_mfma_f32_16x16x32_bf16 v[10:13], v[130:133], v[206:209], v[10:13]
	s_setprio 0
	s_setprio 3
	v_mfma_f32_16x16x32_bf16 v[54:57], v[146:149], v[162:165], v[54:57]
	v_mfma_f32_16x16x32_bf16 v[50:53], v[154:157], v[162:165], v[50:53]
	v_mfma_f32_16x16x32_bf16 v[38:41], v[146:149], v[170:173], v[38:41]
	v_mfma_f32_16x16x32_bf16 v[34:37], v[154:157], v[170:173], v[34:37]
	v_mfma_f32_16x16x32_bf16 v[22:25], v[146:149], v[178:181], v[22:25]
	v_mfma_f32_16x16x32_bf16 v[18:21], v[154:157], v[178:181], v[18:21]
	v_mfma_f32_16x16x32_bf16 v[6:9], v[146:149], v[202:205], v[6:9]
	v_mfma_f32_16x16x32_bf16 v[2:5], v[154:157], v[202:205], v[2:5]
	v_mfma_f32_16x16x32_bf16 v[54:57], v[150:153], v[166:169], v[54:57]
	v_mfma_f32_16x16x32_bf16 v[50:53], v[158:161], v[166:169], v[50:53]
	v_mfma_f32_16x16x32_bf16 v[38:41], v[150:153], v[174:177], v[38:41]
	v_mfma_f32_16x16x32_bf16 v[34:37], v[158:161], v[174:177], v[34:37]
	v_mfma_f32_16x16x32_bf16 v[22:25], v[150:153], v[182:185], v[22:25]
	v_mfma_f32_16x16x32_bf16 v[18:21], v[158:161], v[182:185], v[18:21]
	v_mfma_f32_16x16x32_bf16 v[6:9], v[150:153], v[206:209], v[6:9]
	v_mfma_f32_16x16x32_bf16 v[2:5], v[158:161], v[206:209], v[2:5]
	s_setprio 0
	s_barrier
	s_add_i32 s63, s63, 2
	s_add_u32 s34, s34, 0x100
	s_addc_u32 s35, s35, 0
	s_add_u32 s61, s61, 0x100
	s_addc_u32 s62, s62, 0
	s_cmp_gt_u32 s63, 13
	.p2align	3

; #define PG8_GIDX(G_, PM_) do { if constexpr (Sched::GATHER) { _Pragma("unroll") for (int h_ = 0; h_ < 2; ++h_) _Pragma("unroll") for (int i_ = 0; i_ < 2; ++i_) { int R_, C_; stage_rc(tid * 16 + i_ * 8192, R_, C_); \
;         const int src_ = S.rowsrc[(PM_) * BM + h_ * HALF + R_]; G_[h_][i_] = (unsigned)(src_ * K + C_) * 2u; } } } while (0)
; template <class Epi, class Sched, bool ALIGN_EPI = false, bool SP2 = false>
; __device__ __forceinline__ void gemm_phase(PG8_LAS unsigned char* lds, const Gemm g, const Sched& S, const Epi& E, const bool skip_epi = false) {
;     ...
;         const bool has_next = S.next(ui + 1, nxt);
;         if (has_next) PG8_GIDX(gN, nxt.pm);
;         const char* nA = has_next ? (const char*)g.A + (size_t)nxt.pm * pmstepA + nxt.ko : cA; const char* nB = has_next ? (const char*)g.Bt + (size_t)nxt.pn * tstep + nxt.ko : cB;
;         for (int t = 0; t < nt; t += 2) {
;             const bool last = (t == nt - 2); last_ = last && has_next;
.Lg5_nonext:
	.p2align	3

; #define PG8_STAGE_A(b, h, ptr, NX) do { if constexpr (Sched::GATHER) { unsigned gs_[2]; gs_[0] = ((NX) && last_) ? gN[h][0] : gA[h][0]; gs_[1] = ((NX) && last_) ? gN[h][1] : gA[h][1]; PG8_STAGE(PG8_SA(b, h), ptr, gs_); } \
;         else PG8_STAGE(PG8_SA(b, h), (ptr) + ((h) ? hstep : (size_t)0), voffA); } while (0)
; #define PG8_STAGE(bufoff, gbase, voff) do { _Pragma("unroll") for (int _i = 0; _i < 2; ++_i) \
;         __builtin_amdgcn_global_load_lds((const unsigned*)((const char*)(gbase) + (voff)[_i]), (PG8_LAS unsigned*)(lds + (bufoff) + ldsw + _i * 8192), 16, 0, 0); } while (0)
; #define PG8_LDA(dst, b, h) do { _Pragma("unroll") for (int m = 0; m < 4; ++m) _Pragma("unroll") for (int k = 0; k < 2; ++k) dst[m][k] = *(const PG8_LAS bf16x8*)(lds + PG8_SA(b, h) + aoff + m * 2048 + k * 1024); } while (0)
; #define PG8_LDB(dst, b, h) do { _Pragma("unroll") for (int n = 0; n < 2; ++n) _Pragma("unroll") for (int k = 0; k < 2; ++k) dst[n][k] = *(const PG8_LAS bf16x8*)(lds + PG8_SB(b, h) + boff + n * 2048 + k * 1024); } while (0)
; #define PG8_WAIT_V(n) asm volatile("s_waitcnt vmcnt(" #n ")" ::: "memory")
; #define PG8_WAIT_L(n) asm volatile("s_waitcnt lgkmcnt(" #n ")" ::: "memory")
; template <class Epi, class Sched, bool ALIGN_EPI = false, bool SP2 = false>
; __device__ __forceinline__ void gemm_phase(PG8_LAS unsigned char* lds, const Gemm g, const Sched& S, const Epi& E, const bool skip_epi = false) {
;     ...
;         for (int t = 0; t < nt; t += 2) {
;             const bool last = (t == nt - 2); last_ = last && has_next;
;             const char* a1 = cA + (size_t)(t + 1) * kstep;
;             const char* a2 = last ? nA : cA + (size_t)(t + 2) * kstep; const char* b2 = last ? nB : cB + (size_t)(t + 2) * kstep;
;             const char* a3 = a2 + kstep; const char* b3 = b2 + kstep;
;             if (last && has_next) S.a_ready(nxt);
;             if constexpr (SP2) {
;             PG8_LDB(B0, 0, 0); PG8_LDB(B1, 0, 1); PG8_SCHED; PG8_LDA(At, 0, 0); PG8_STAGE_A(1, 1, a1, false);
;             PG8_WAIT_V(8); PG8_WAIT_L(0); PG8_BAR; PG8_MMA(0, 0, At, B0); PG8_MMA(0, 1, At, B1); PG8_BAR; PG8_SCHED;
;             PG8_LDA(At, 0, 1); PG8_STAGE(PG8_SB(0, 0), b2, voffB); PG8_STAGE(PG8_SB(0, 1), b2 + hstep, voffB); PG8_STAGE_A(0, 0, a2, true);
;             PG8_WAIT_V(8); PG8_WAIT_L(0); PG8_BAR; PG8_MMA(1, 0, At, B0); PG8_MMA(1, 1, At, B1); PG8_BAR; PG8_SCHED;
.LBB0_1822:
	s_add_u32 s67, s40, 0x100
	s_addc_u32 s68, s41, 0
	s_mov_b32 s69, -2
	ds_read_b128 v[160:163], v157
	ds_read_b128 v[164:167], v157 offset:1024
	ds_read_b128 v[168:171], v157 offset:2048
	ds_read_b128 v[172:175], v157 offset:3072
	ds_read_b128 v[176:179], v158
	ds_read_b128 v[180:183], v158 offset:1024
	ds_read_b128 v[184:187], v158 offset:2048
	ds_read_b128 v[188:191], v158 offset:3072
	s_add_u32 s40, s38, 0x100
	s_addc_u32 s41, s39, 0
	s_cmp_eq_u32 s69, 52
	s_cselect_b32 s45, s7, s41
	s_cselect_b32 s44, s6, s40
	s_cselect_b32 s43, s35, s68
	s_cselect_b32 s42, s34, s67
	v_lshl_add_u64 v[152:153], s[38:39], 0, v[140:141]
	s_add_i32 m0, s37, 0xc000
	ds_read_b128 v[192:195], v159
	ds_read_b128 v[196:199], v159 offset:1024
	ds_read_b128 v[200:203], v159 offset:2048
	ds_read_b128 v[204:207], v159 offset:3072
	ds_read_b128 v[208:211], v159 offset:4096
	ds_read_b128 v[212:215], v159 offset:5120
	ds_read_b128 v[216:219], v159 offset:6144
	ds_read_b128 v[220:223], v159 offset:7168
	global_load_lds_dwordx4 v[152:153], off
	v_lshl_add_u64 v[152:153], s[38:39], 0, v[142:143]
	s_add_i32 m0, s37, 0xe000
	s_nop 0
	global_load_lds_dwordx4 v[152:153], off
	s_waitcnt vmcnt(8)
	s_waitcnt lgkmcnt(0)
	s_barrier
	s_setprio 3
	s_waitcnt lgkmcnt(0)
	v_mfma_f32_16x16x32_bf16 v[126:129], v[160:163], v[192:195], 0
	v_mfma_f32_16x16x32_bf16 v[122:125], v[168:171], v[192:195], 0
	v_mfma_f32_16x16x32_bf16 v[118:121], v[160:163], v[200:203], 0
	v_mfma_f32_16x16x32_bf16 v[114:117], v[168:171], v[200:203], 0
	v_mfma_f32_16x16x32_bf16 v[106:109], v[160:163], v[208:211], 0
	v_mfma_f32_16x16x32_bf16 v[98:101], v[168:171], v[208:211], 0
	v_mfma_f32_16x16x32_bf16 v[78:81], v[160:163], v[216:219], 0
	v_mfma_f32_16x16x32_bf16 v[74:77], v[168:171], v[216:219], 0
	v_mfma_f32_16x16x32_bf16 v[126:129], v[164:167], v[196:199], v[126:129]
	v_mfma_f32_16x16x32_bf16 v[122:125], v[172:175], v[196:199], v[122:125]
	v_mfma_f32_16x16x32_bf16 v[118:121], v[164:167], v[204:207], v[118:121]
	v_mfma_f32_16x16x32_bf16 v[114:117], v[172:175], v[204:207], v[114:117]
	v_mfma_f32_16x16x32_bf16 v[106:109], v[164:167], v[212:215], v[106:109]
	v_mfma_f32_16x16x32_bf16 v[98:101], v[172:175], v[212:215], v[98:101]
	v_mfma_f32_16x16x32_bf16 v[78:81], v[164:167], v[220:223], v[78:81]
	v_mfma_f32_16x16x32_bf16 v[74:77], v[172:175], v[220:223], v[74:77]
	s_setprio 0
	s_setprio 3
	v_mfma_f32_16x16x32_bf16 v[110:113], v[176:179], v[192:195], 0
	v_mfma_f32_16x16x32_bf16 v[102:105], v[184:187], v[192:195], 0
	v_mfma_f32_16x16x32_bf16 v[94:97], v[176:179], v[200:203], 0
	v_mfma_f32_16x16x32_bf16 v[90:93], v[184:187], v[200:203], 0
	v_mfma_f32_16x16x32_bf16 v[86:89], v[176:179], v[208:211], 0
	v_mfma_f32_16x16x32_bf16 v[82:85], v[184:187], v[208:211], 0
	v_mfma_f32_16x16x32_bf16 v[70:73], v[176:179], v[216:219], 0
	v_mfma_f32_16x16x32_bf16 v[66:69], v[184:187], v[216:219], 0
	v_mfma_f32_16x16x32_bf16 v[110:113], v[180:183], v[196:199], v[110:113]
	v_mfma_f32_16x16x32_bf16 v[102:105], v[188:191], v[196:199], v[102:105]
	v_mfma_f32_16x16x32_bf16 v[94:97], v[180:183], v[204:207], v[94:97]
	v_mfma_f32_16x16x32_bf16 v[90:93], v[188:191], v[204:207], v[90:93]
	v_mfma_f32_16x16x32_bf16 v[86:89], v[180:183], v[212:215], v[86:89]
	v_mfma_f32_16x16x32_bf16 v[82:85], v[188:191], v[212:215], v[82:85]
	v_mfma_f32_16x16x32_bf16 v[70:73], v[180:183], v[220:223], v[70:73]
	v_mfma_f32_16x16x32_bf16 v[66:69], v[188:191], v[220:223], v[66:69]
	s_setprio 0
	s_barrier
	s_add_i32 s38, s60, s51
	v_lshl_add_u64 v[152:153], s[42:43], 0, v[134:135]
	s_mov_b32 m0, s38
	ds_read_b128 v[192:195], v159 offset:16384
	ds_read_b128 v[196:199], v159 offset:17408
	ds_read_b128 v[200:203], v159 offset:18432
	ds_read_b128 v[204:207], v159 offset:19456
	ds_read_b128 v[208:211], v159 offset:20480
	ds_read_b128 v[212:215], v159 offset:21504
	ds_read_b128 v[216:219], v159 offset:22528
	ds_read_b128 v[220:223], v159 offset:23552
	global_load_lds_dwordx4 v[152:153], off
	s_add_i32 m0, s38, 0x2000
	s_add_u32 s38, s42, 0xe0000
	v_lshl_add_u64 v[224:225], s[42:43], 0, v[138:139]
	s_addc_u32 s39, s43, 0
	s_add_i32 s70, s61, s51
	global_load_lds_dwordx4 v[224:225], off
	v_lshl_add_u64 v[226:227], s[38:39], 0, v[134:135]
	s_mov_b32 m0, s70
	v_lshl_add_u64 v[230:231], s[44:45], 0, v[136:137]
	global_load_lds_dwordx4 v[226:227], off
	v_lshl_add_u64 v[226:227], s[38:39], 0, v[138:139]
	s_add_i32 m0, s70, 0x2000
	s_nop 0
	global_load_lds_dwordx4 v[226:227], off
	v_lshl_add_u64 v[226:227], s[44:45], 0, v[132:133]
	s_mov_b32 m0, s37
	s_nop 0
	global_load_lds_dwordx4 v[226:227], off
	s_mov_b32 m0, s52
	s_nop 0
	global_load_lds_dwordx4 v[230:231], off
	s_waitcnt vmcnt(8)
	s_waitcnt lgkmcnt(0)
	s_barrier
; #define PG8_STAGE_A(b, h, ptr, NX) do { if constexpr (Sched::GATHER) { unsigned gs_[2]; gs_[0] = ((NX) && last_) ? gN[h][0] : gA[h][0]; gs_[1] = ((NX) && last_) ? gN[h][1] : gA[h][1]; PG8_STAGE(PG8_SA(b, h), ptr, gs_); } \
;         else PG8_STAGE(PG8_SA(b, h), (ptr) + ((h) ? hstep : (size_t)0), voffA); } while (0)
; #define PG8_STAGE(bufoff, gbase, voff) do { _Pragma("unroll") for (int _i = 0; _i < 2; ++_i) \
;         __builtin_amdgcn_global_load_lds((const unsigned*)((const char*)(gbase) + (voff)[_i]), (PG8_LAS unsigned*)(lds + (bufoff) + ldsw + _i * 8192), 16, 0, 0); } while (0)
; #define PG8_LDA(dst, b, h) do { _Pragma("unroll") for (int m = 0; m < 4; ++m) _Pragma("unroll") for (int k = 0; k < 2; ++k) dst[m][k] = *(const PG8_LAS bf16x8*)(lds + PG8_SA(b, h) + aoff + m * 2048 + k * 1024); } while (0)
; #define PG8_LDB(dst, b, h) do { _Pragma("unroll") for (int n = 0; n < 2; ++n) _Pragma("unroll") for (int k = 0; k < 2; ++k) dst[n][k] = *(const PG8_LAS bf16x8*)(lds + PG8_SB(b, h) + boff + n * 2048 + k * 1024); } while (0)
; #define PG8_MMA(ai, bj, At, Bt) do { __builtin_amdgcn_s_setprio(1); _Pragma("unroll") for (int m = 0; m < 4; ++m) _Pragma("unroll") for (int n = 0; n < 2; ++n) _Pragma("unroll") for (int k = 0; k < 2; ++k) \
;         acc[ai][bj][m][n] = __builtin_amdgcn_mfma_f32_16x16x32_bf16(Bt[n][k], At[m][k], acc[ai][bj][m][n], 0, 0, 0); __builtin_amdgcn_s_setprio(0); } while (0)
; #define PG8_WAIT_V(n) asm volatile("s_waitcnt vmcnt(" #n ")" ::: "memory")
; #define PG8_WAIT_L(n) asm volatile("s_waitcnt lgkmcnt(" #n ")" ::: "memory")
; #define PG8_BAR __builtin_amdgcn_s_barrier()
; #define PG8_SCHED __builtin_amdgcn_sched_barrier(0)
; template <class Epi, class Sched, bool ALIGN_EPI = false, bool SP2 = false>
; __device__ __forceinline__ void gemm_phase(PG8_LAS unsigned char* lds, const Gemm g, const Sched& S, const Epi& E, const bool skip_epi = false) {
;     ...
;             PG8_WAIT_V(8); PG8_WAIT_L(0); PG8_BAR; PG8_MMA(1, 0, At, B0); PG8_MMA(1, 1, At, B1); PG8_BAR; PG8_SCHED;
;             PG8_LDB(B0, 1, 0); PG8_LDB(B1, 1, 1); PG8_SCHED; PG8_LDA(At, 1, 0); PG8_STAGE_A(0, 1, a2, true);
;             PG8_WAIT_V(8); PG8_WAIT_L(0); PG8_BAR; PG8_MMA(0, 0, At, B0); PG8_MMA(0, 1, At, B1); PG8_BAR; PG8_SCHED;
;             PG8_LDA(At, 1, 1); PG8_STAGE(PG8_SB(1, 0), b3, voffB); PG8_STAGE(PG8_SB(1, 1), b3 + hstep, voffB); PG8_STAGE_A(1, 0, a3, true);
	s_setprio 3
	s_waitcnt lgkmcnt(0)
	v_mfma_f32_16x16x32_bf16 v[62:65], v[160:163], v[192:195], 0
	v_mfma_f32_16x16x32_bf16 v[58:61], v[168:171], v[192:195], 0
	v_mfma_f32_16x16x32_bf16 v[50:53], v[160:163], v[200:203], 0
	v_mfma_f32_16x16x32_bf16 v[42:45], v[168:171], v[200:203], 0
	v_mfma_f32_16x16x32_bf16 v[34:37], v[160:163], v[208:211], 0
	v_mfma_f32_16x16x32_bf16 v[26:29], v[168:171], v[208:211], 0
	v_mfma_f32_16x16x32_bf16 v[18:21], v[160:163], v[216:219], 0
	v_mfma_f32_16x16x32_bf16 v[10:13], v[168:171], v[216:219], 0
	v_mfma_f32_16x16x32_bf16 v[62:65], v[164:167], v[196:199], v[62:65]
	v_mfma_f32_16x16x32_bf16 v[58:61], v[172:175], v[196:199], v[58:61]
	v_mfma_f32_16x16x32_bf16 v[50:53], v[164:167], v[204:207], v[50:53]
	v_mfma_f32_16x16x32_bf16 v[42:45], v[172:175], v[204:207], v[42:45]
	v_mfma_f32_16x16x32_bf16 v[34:37], v[164:167], v[212:215], v[34:37]
	v_mfma_f32_16x16x32_bf16 v[26:29], v[172:175], v[212:215], v[26:29]
	v_mfma_f32_16x16x32_bf16 v[18:21], v[164:167], v[220:223], v[18:21]
	v_mfma_f32_16x16x32_bf16 v[10:13], v[172:175], v[220:223], v[10:13]
	s_setprio 0
	s_setprio 3
	v_mfma_f32_16x16x32_bf16 v[54:57], v[176:179], v[192:195], 0
	v_mfma_f32_16x16x32_bf16 v[46:49], v[184:187], v[192:195], 0
	v_mfma_f32_16x16x32_bf16 v[38:41], v[176:179], v[200:203], 0
	v_mfma_f32_16x16x32_bf16 v[30:33], v[184:187], v[200:203], 0
	v_mfma_f32_16x16x32_bf16 v[22:25], v[176:179], v[208:211], 0
	v_mfma_f32_16x16x32_bf16 v[14:17], v[184:187], v[208:211], 0
	v_mfma_f32_16x16x32_bf16 v[6:9], v[176:179], v[216:219], 0
	v_mfma_f32_16x16x32_bf16 v[2:5], v[184:187], v[216:219], 0
	v_mfma_f32_16x16x32_bf16 v[54:57], v[180:183], v[196:199], v[54:57]
	v_mfma_f32_16x16x32_bf16 v[46:49], v[188:191], v[196:199], v[46:49]
	v_mfma_f32_16x16x32_bf16 v[38:41], v[180:183], v[204:207], v[38:41]
	v_mfma_f32_16x16x32_bf16 v[30:33], v[188:191], v[204:207], v[30:33]
	v_mfma_f32_16x16x32_bf16 v[22:25], v[180:183], v[212:215], v[22:25]
	v_mfma_f32_16x16x32_bf16 v[14:17], v[188:191], v[212:215], v[14:17]
	v_mfma_f32_16x16x32_bf16 v[6:9], v[180:183], v[220:223], v[6:9]
	v_mfma_f32_16x16x32_bf16 v[2:5], v[188:191], v[220:223], v[2:5]
	s_setprio 0
	s_barrier
	s_add_i32 s70, 0, 0x18000
	v_add_u32_e32 v130, s70, v147
	s_add_i32 s71, 0, 0x1c000
	ds_read_b128 v[160:163], v130
	ds_read_b128 v[164:167], v130 offset:1024
	ds_read_b128 v[168:171], v130 offset:2048
	ds_read_b128 v[172:175], v130 offset:3072
	v_add_u32_e32 v130, s71, v147
	ds_read_b128 v[176:179], v130
	ds_read_b128 v[180:183], v130 offset:1024
	ds_read_b128 v[184:187], v130 offset:2048
	ds_read_b128 v[188:191], v130 offset:3072
	s_add_u32 s38, s44, 0xe0000
	s_addc_u32 s39, s45, 0
	s_mov_b32 m0, s53
	v_lshl_add_u64 v[232:233], s[38:39], 0, v[132:133]
	ds_read_b128 v[192:195], v159 offset:32768
	ds_read_b128 v[196:199], v159 offset:33792
	ds_read_b128 v[200:203], v159 offset:34816
	ds_read_b128 v[204:207], v159 offset:35840
	ds_read_b128 v[208:211], v159 offset:36864
	ds_read_b128 v[212:215], v159 offset:37888
	ds_read_b128 v[216:219], v159 offset:38912
	ds_read_b128 v[220:223], v159 offset:39936
	global_load_lds_dwordx4 v[232:233], off
	v_lshl_add_u64 v[232:233], s[38:39], 0, v[136:137]
	s_mov_b32 m0, s54
	s_nop 0
	global_load_lds_dwordx4 v[232:233], off
	s_waitcnt vmcnt(8)
	s_waitcnt lgkmcnt(0)
	s_barrier
	s_setprio 3
	s_waitcnt lgkmcnt(0)
	v_mfma_f32_16x16x32_bf16 v[126:129], v[160:163], v[192:195], v[126:129]
	v_mfma_f32_16x16x32_bf16 v[122:125], v[168:171], v[192:195], v[122:125]
	v_mfma_f32_16x16x32_bf16 v[118:121], v[160:163], v[200:203], v[118:121]
	v_mfma_f32_16x16x32_bf16 v[114:117], v[168:171], v[200:203], v[114:117]
	v_mfma_f32_16x16x32_bf16 v[106:109], v[160:163], v[208:211], v[106:109]
	v_mfma_f32_16x16x32_bf16 v[98:101], v[168:171], v[208:211], v[98:101]
	v_mfma_f32_16x16x32_bf16 v[78:81], v[160:163], v[216:219], v[78:81]
	v_mfma_f32_16x16x32_bf16 v[74:77], v[168:171], v[216:219], v[74:77]
	v_mfma_f32_16x16x32_bf16 v[126:129], v[164:167], v[196:199], v[126:129]
	v_mfma_f32_16x16x32_bf16 v[122:125], v[172:175], v[196:199], v[122:125]
	v_mfma_f32_16x16x32_bf16 v[118:121], v[164:167], v[204:207], v[118:121]
	v_mfma_f32_16x16x32_bf16 v[114:117], v[172:175], v[204:207], v[114:117]
	v_mfma_f32_16x16x32_bf16 v[106:109], v[164:167], v[212:215], v[106:109]
	v_mfma_f32_16x16x32_bf16 v[98:101], v[172:175], v[212:215], v[98:101]
	v_mfma_f32_16x16x32_bf16 v[78:81], v[164:167], v[220:223], v[78:81]
	v_mfma_f32_16x16x32_bf16 v[74:77], v[172:175], v[220:223], v[74:77]
	s_setprio 0
	s_setprio 3
	v_mfma_f32_16x16x32_bf16 v[110:113], v[176:179], v[192:195], v[110:113]
	v_mfma_f32_16x16x32_bf16 v[102:105], v[184:187], v[192:195], v[102:105]
	v_mfma_f32_16x16x32_bf16 v[94:97], v[176:179], v[200:203], v[94:97]
	v_mfma_f32_16x16x32_bf16 v[90:93], v[184:187], v[200:203], v[90:93]
	v_mfma_f32_16x16x32_bf16 v[86:89], v[176:179], v[208:211], v[86:89]
	v_mfma_f32_16x16x32_bf16 v[82:85], v[184:187], v[208:211], v[82:85]
	v_mfma_f32_16x16x32_bf16 v[70:73], v[176:179], v[216:219], v[70:73]
	v_mfma_f32_16x16x32_bf16 v[66:69], v[184:187], v[216:219], v[66:69]
	v_mfma_f32_16x16x32_bf16 v[110:113], v[180:183], v[196:199], v[110:113]
	v_mfma_f32_16x16x32_bf16 v[102:105], v[188:191], v[196:199], v[102:105]
	v_mfma_f32_16x16x32_bf16 v[94:97], v[180:183], v[204:207], v[94:97]
	v_mfma_f32_16x16x32_bf16 v[90:93], v[188:191], v[204:207], v[90:93]
	v_mfma_f32_16x16x32_bf16 v[86:89], v[180:183], v[212:215], v[86:89]
	v_mfma_f32_16x16x32_bf16 v[82:85], v[188:191], v[212:215], v[82:85]
	v_mfma_f32_16x16x32_bf16 v[70:73], v[180:183], v[220:223], v[70:73]
	v_mfma_f32_16x16x32_bf16 v[66:69], v[188:191], v[220:223], v[66:69]
	s_setprio 0
	s_barrier
; #define PG8_STAGE_A(b, h, ptr, NX) do { if constexpr (Sched::GATHER) { unsigned gs_[2]; gs_[0] = ((NX) && last_) ? gN[h][0] : gA[h][0]; gs_[1] = ((NX) && last_) ? gN[h][1] : gA[h][1]; PG8_STAGE(PG8_SA(b, h), ptr, gs_); } \
;         else PG8_STAGE(PG8_SA(b, h), (ptr) + ((h) ? hstep : (size_t)0), voffA); } while (0)
; #define PG8_STAGE(bufoff, gbase, voff) do { _Pragma("unroll") for (int _i = 0; _i < 2; ++_i) \
;         __builtin_amdgcn_global_load_lds((const unsigned*)((const char*)(gbase) + (voff)[_i]), (PG8_LAS unsigned*)(lds + (bufoff) + ldsw + _i * 8192), 16, 0, 0); } while (0)
; #define PG8_LDA(dst, b, h) do { _Pragma("unroll") for (int m = 0; m < 4; ++m) _Pragma("unroll") for (int k = 0; k < 2; ++k) dst[m][k] = *(const PG8_LAS bf16x8*)(lds + PG8_SA(b, h) + aoff + m * 2048 + k * 1024); } while (0)
; #define PG8_MMA(ai, bj, At, Bt) do { __builtin_amdgcn_s_setprio(1); _Pragma("unroll") for (int m = 0; m < 4; ++m) _Pragma("unroll") for (int n = 0; n < 2; ++n) _Pragma("unroll") for (int k = 0; k < 2; ++k) \
;         acc[ai][bj][m][n] = __builtin_amdgcn_mfma_f32_16x16x32_bf16(Bt[n][k], At[m][k], acc[ai][bj][m][n], 0, 0, 0); __builtin_amdgcn_s_setprio(0); } while (0)
; #define PG8_WAIT_V(n) asm volatile("s_waitcnt vmcnt(" #n ")" ::: "memory")
; #define PG8_WAIT_L(n) asm volatile("s_waitcnt lgkmcnt(" #n ")" ::: "memory")
; #define PG8_BAR __builtin_amdgcn_s_barrier()
; #define PG8_SCHED __builtin_amdgcn_sched_barrier(0)
; template <class Epi, class Sched, bool ALIGN_EPI = false, bool SP2 = false>
; __device__ __forceinline__ void gemm_phase(PG8_LAS unsigned char* lds, const Gemm g, const Sched& S, const Epi& E, const bool skip_epi = false) {
;     ...
;             PG8_LDA(At, 1, 1); PG8_STAGE(PG8_SB(1, 0), b3, voffB); PG8_STAGE(PG8_SB(1, 1), b3 + hstep, voffB); PG8_STAGE_A(1, 0, a3, true);
;             PG8_WAIT_V(8); PG8_WAIT_L(0); PG8_BAR; PG8_MMA(1, 0, At, B0); PG8_MMA(1, 1, At, B1); PG8_BAR; PG8_SCHED;
	s_add_i32 s38, s70, s51
	v_lshl_add_u64 v[152:153], v[152:153], 0, s[18:19]
	s_mov_b32 m0, s38
	ds_read_b128 v[192:195], v159 offset:49152
	ds_read_b128 v[196:199], v159 offset:50176
	ds_read_b128 v[200:203], v159 offset:51200
	ds_read_b128 v[204:207], v159 offset:52224
	ds_read_b128 v[208:211], v159 offset:53248
	ds_read_b128 v[212:215], v159 offset:54272
	ds_read_b128 v[216:219], v159 offset:55296
	ds_read_b128 v[220:223], v159 offset:56320
	global_load_lds_dwordx4 v[152:153], off
	s_add_i32 m0, s38, 0x2000
	s_add_u32 s38, s42, 0xe0080
	v_lshl_add_u64 v[152:153], v[224:225], 0, s[18:19]
	s_addc_u32 s39, s43, 0
	s_add_i32 s42, s71, s51
	global_load_lds_dwordx4 v[152:153], off
	v_lshl_add_u64 v[152:153], s[38:39], 0, v[134:135]
	s_mov_b32 m0, s42
	s_nop 0
	global_load_lds_dwordx4 v[152:153], off
	v_lshl_add_u64 v[152:153], s[38:39], 0, v[138:139]
	s_add_i32 m0, s42, 0x2000
	s_nop 0
	global_load_lds_dwordx4 v[152:153], off
	v_lshl_add_u64 v[152:153], v[226:227], 0, s[18:19]
	s_mov_b32 m0, s57
	s_nop 0
	global_load_lds_dwordx4 v[152:153], off
	v_lshl_add_u64 v[152:153], v[230:231], 0, s[18:19]
	s_mov_b32 m0, s58
	s_nop 0
	global_load_lds_dwordx4 v[152:153], off
	s_waitcnt vmcnt(8)
	s_waitcnt lgkmcnt(0)
	s_barrier
	s_setprio 3
	s_waitcnt lgkmcnt(0)
	v_mfma_f32_16x16x32_bf16 v[62:65], v[160:163], v[192:195], v[62:65]
	v_mfma_f32_16x16x32_bf16 v[58:61], v[168:171], v[192:195], v[58:61]
	v_mfma_f32_16x16x32_bf16 v[50:53], v[160:163], v[200:203], v[50:53]
	v_mfma_f32_16x16x32_bf16 v[42:45], v[168:171], v[200:203], v[42:45]
	v_mfma_f32_16x16x32_bf16 v[34:37], v[160:163], v[208:211], v[34:37]
	v_mfma_f32_16x16x32_bf16 v[26:29], v[168:171], v[208:211], v[26:29]
	v_mfma_f32_16x16x32_bf16 v[18:21], v[160:163], v[216:219], v[18:21]
	v_mfma_f32_16x16x32_bf16 v[10:13], v[168:171], v[216:219], v[10:13]
	v_mfma_f32_16x16x32_bf16 v[62:65], v[164:167], v[196:199], v[62:65]
	v_mfma_f32_16x16x32_bf16 v[58:61], v[172:175], v[196:199], v[58:61]
	v_mfma_f32_16x16x32_bf16 v[50:53], v[164:167], v[204:207], v[50:53]
	v_mfma_f32_16x16x32_bf16 v[42:45], v[172:175], v[204:207], v[42:45]
	v_mfma_f32_16x16x32_bf16 v[34:37], v[164:167], v[212:215], v[34:37]
	v_mfma_f32_16x16x32_bf16 v[26:29], v[172:175], v[212:215], v[26:29]
	v_mfma_f32_16x16x32_bf16 v[18:21], v[164:167], v[220:223], v[18:21]
	v_mfma_f32_16x16x32_bf16 v[10:13], v[172:175], v[220:223], v[10:13]
	s_setprio 0
	s_setprio 3
	v_mfma_f32_16x16x32_bf16 v[54:57], v[176:179], v[192:195], v[54:57]
	v_mfma_f32_16x16x32_bf16 v[46:49], v[184:187], v[192:195], v[46:49]
	v_mfma_f32_16x16x32_bf16 v[38:41], v[176:179], v[200:203], v[38:41]
	v_mfma_f32_16x16x32_bf16 v[30:33], v[184:187], v[200:203], v[30:33]
	v_mfma_f32_16x16x32_bf16 v[22:25], v[176:179], v[208:211], v[22:25]
	v_mfma_f32_16x16x32_bf16 v[14:17], v[184:187], v[208:211], v[14:17]
	v_mfma_f32_16x16x32_bf16 v[6:9], v[176:179], v[216:219], v[6:9]
	v_mfma_f32_16x16x32_bf16 v[2:5], v[184:187], v[216:219], v[2:5]
	v_mfma_f32_16x16x32_bf16 v[54:57], v[180:183], v[196:199], v[54:57]
	v_mfma_f32_16x16x32_bf16 v[46:49], v[188:191], v[196:199], v[46:49]
	v_mfma_f32_16x16x32_bf16 v[38:41], v[180:183], v[204:207], v[38:41]
	v_mfma_f32_16x16x32_bf16 v[30:33], v[188:191], v[204:207], v[30:33]
	v_mfma_f32_16x16x32_bf16 v[22:25], v[180:183], v[212:215], v[22:25]
	v_mfma_f32_16x16x32_bf16 v[14:17], v[188:191], v[212:215], v[14:17]
	v_mfma_f32_16x16x32_bf16 v[6:9], v[180:183], v[220:223], v[6:9]
	v_mfma_f32_16x16x32_bf16 v[2:5], v[188:191], v[220:223], v[2:5]
	s_setprio 0
	s_barrier
	s_add_i32 s69, s69, 2
	s_add_u32 s67, s67, 0x100
	s_addc_u32 s68, s68, 0
	s_cmp_gt_u32 s69, 53
	s_mov_b64 s[38:39], s[40:41]
	.p2align	3

; #define PG8_STAGE_A(b, h, ptr, NX) do { if constexpr (Sched::GATHER) { unsigned gs_[2]; gs_[0] = ((NX) && last_) ? gN[h][0] : gA[h][0]; gs_[1] = ((NX) && last_) ? gN[h][1] : gA[h][1]; PG8_STAGE(PG8_SA(b, h), ptr, gs_); } \
;         else PG8_STAGE(PG8_SA(b, h), (ptr) + ((h) ? hstep : (size_t)0), voffA); } while (0)
; #define PG8_STAGE(bufoff, gbase, voff) do { _Pragma("unroll") for (int _i = 0; _i < 2; ++_i) \
;         __builtin_amdgcn_global_load_lds((const unsigned*)((const char*)(gbase) + (voff)[_i]), (PG8_LAS unsigned*)(lds + (bufoff) + ldsw + _i * 8192), 16, 0, 0); } while (0)
; #define PG8_LDA(dst, b, h) do { _Pragma("unroll") for (int m = 0; m < 4; ++m) _Pragma("unroll") for (int k = 0; k < 2; ++k) dst[m][k] = *(const PG8_LAS bf16x8*)(lds + PG8_SA(b, h) + aoff + m * 2048 + k * 1024); } while (0)
; #define PG8_LDB(dst, b, h) do { _Pragma("unroll") for (int n = 0; n < 2; ++n) _Pragma("unroll") for (int k = 0; k < 2; ++k) dst[n][k] = *(const PG8_LAS bf16x8*)(lds + PG8_SB(b, h) + boff + n * 2048 + k * 1024); } while (0)
; #define PG8_WAIT_V(n) asm volatile("s_waitcnt vmcnt(" #n ")" ::: "memory")
; #define PG8_WAIT_L(n) asm volatile("s_waitcnt lgkmcnt(" #n ")" ::: "memory")
; template <class Epi, class Sched, bool ALIGN_EPI = false, bool SP2 = false>
; __device__ __forceinline__ void gemm_phase(PG8_LAS unsigned char* lds, const Gemm g, const Sched& S, const Epi& E, const bool skip_epi = false) {
;     ...
;         for (int t = 0; t < nt; t += 2) {
;             const bool last = (t == nt - 2); last_ = last && has_next;
;             const char* a1 = cA + (size_t)(t + 1) * kstep;
;             const char* a2 = last ? nA : cA + (size_t)(t + 2) * kstep; const char* b2 = last ? nB : cB + (size_t)(t + 2) * kstep;
;             const char* a3 = a2 + kstep; const char* b3 = b2 + kstep;
;             if (last && has_next) S.a_ready(nxt);
;             if constexpr (SP2) {
;             PG8_LDB(B0, 0, 0); PG8_LDB(B1, 0, 1); PG8_SCHED; PG8_LDA(At, 0, 0); PG8_STAGE_A(1, 1, a1, false);
;             PG8_WAIT_V(8); PG8_WAIT_L(0); PG8_BAR; PG8_MMA(0, 0, At, B0); PG8_MMA(0, 1, At, B1); PG8_BAR; PG8_SCHED;
;             PG8_LDA(At, 0, 1); PG8_STAGE(PG8_SB(0, 0), b2, voffB); PG8_STAGE(PG8_SB(0, 1), b2 + hstep, voffB); PG8_STAGE_A(0, 0, a2, true);
;             PG8_WAIT_V(8); PG8_WAIT_L(0); PG8_BAR; PG8_MMA(1, 0, At, B0); PG8_MMA(1, 1, At, B1); PG8_BAR; PG8_SCHED;
.LBB0_1843:
	s_add_u32 s54, s30, 0x100
	s_addc_u32 s55, s31, 0
	s_mov_b32 s56, -2
	ds_read_b128 v[142:145], v150
	ds_read_b128 v[154:157], v150 offset:1024
	ds_read_b128 v[158:161], v150 offset:2048
	ds_read_b128 v[162:165], v150 offset:3072
	ds_read_b128 v[166:169], v151
	ds_read_b128 v[170:173], v151 offset:1024
	ds_read_b128 v[174:177], v151 offset:2048
	ds_read_b128 v[178:181], v151 offset:3072
	s_add_u32 s30, s28, 0x100
	s_addc_u32 s31, s29, 0
	s_cmp_eq_u32 s56, 10
	s_cselect_b32 s37, s7, s31
	s_cselect_b32 s36, s6, s30
	s_cselect_b32 s35, s25, s55
	s_cselect_b32 s34, s24, s54
	v_lshl_add_u64 v[214:215], s[28:29], 0, v[136:137]
	s_add_i32 m0, s38, 0xc000
	ds_read_b128 v[182:185], v152
	ds_read_b128 v[186:189], v152 offset:1024
	ds_read_b128 v[190:193], v152 offset:2048
	ds_read_b128 v[194:197], v152 offset:3072
	ds_read_b128 v[198:201], v152 offset:4096
	ds_read_b128 v[202:205], v152 offset:5120
	ds_read_b128 v[206:209], v152 offset:6144
	ds_read_b128 v[210:213], v152 offset:7168
	global_load_lds_dwordx4 v[214:215], off
	v_lshl_add_u64 v[214:215], s[28:29], 0, v[138:139]
	s_add_i32 m0, s38, 0xe000
	s_nop 0
	global_load_lds_dwordx4 v[214:215], off
	s_waitcnt vmcnt(8)
	s_waitcnt lgkmcnt(0)
	s_barrier
	s_setprio 3
	s_waitcnt lgkmcnt(0)
	v_mfma_f32_16x16x32_bf16 v[126:129], v[142:145], v[182:185], 0
	v_mfma_f32_16x16x32_bf16 v[122:125], v[158:161], v[182:185], 0
	v_mfma_f32_16x16x32_bf16 v[110:113], v[142:145], v[190:193], 0
	v_mfma_f32_16x16x32_bf16 v[106:109], v[158:161], v[190:193], 0
	v_mfma_f32_16x16x32_bf16 v[94:97], v[142:145], v[198:201], 0
	v_mfma_f32_16x16x32_bf16 v[90:93], v[158:161], v[198:201], 0
	v_mfma_f32_16x16x32_bf16 v[78:81], v[142:145], v[206:209], 0
	v_mfma_f32_16x16x32_bf16 v[74:77], v[158:161], v[206:209], 0
	v_mfma_f32_16x16x32_bf16 v[126:129], v[154:157], v[186:189], v[126:129]
	v_mfma_f32_16x16x32_bf16 v[122:125], v[162:165], v[186:189], v[122:125]
	v_mfma_f32_16x16x32_bf16 v[110:113], v[154:157], v[194:197], v[110:113]
	v_mfma_f32_16x16x32_bf16 v[106:109], v[162:165], v[194:197], v[106:109]
	v_mfma_f32_16x16x32_bf16 v[94:97], v[154:157], v[202:205], v[94:97]
	v_mfma_f32_16x16x32_bf16 v[90:93], v[162:165], v[202:205], v[90:93]
	v_mfma_f32_16x16x32_bf16 v[78:81], v[154:157], v[210:213], v[78:81]
	v_mfma_f32_16x16x32_bf16 v[74:77], v[162:165], v[210:213], v[74:77]
	s_setprio 0
	s_setprio 3
	v_mfma_f32_16x16x32_bf16 v[118:121], v[166:169], v[182:185], 0
	v_mfma_f32_16x16x32_bf16 v[114:117], v[174:177], v[182:185], 0
	v_mfma_f32_16x16x32_bf16 v[102:105], v[166:169], v[190:193], 0
	v_mfma_f32_16x16x32_bf16 v[98:101], v[174:177], v[190:193], 0
	v_mfma_f32_16x16x32_bf16 v[86:89], v[166:169], v[198:201], 0
	v_mfma_f32_16x16x32_bf16 v[82:85], v[174:177], v[198:201], 0
	v_mfma_f32_16x16x32_bf16 v[70:73], v[166:169], v[206:209], 0
	v_mfma_f32_16x16x32_bf16 v[66:69], v[174:177], v[206:209], 0
	v_mfma_f32_16x16x32_bf16 v[118:121], v[170:173], v[186:189], v[118:121]
	v_mfma_f32_16x16x32_bf16 v[114:117], v[178:181], v[186:189], v[114:117]
	v_mfma_f32_16x16x32_bf16 v[102:105], v[170:173], v[194:197], v[102:105]
	v_mfma_f32_16x16x32_bf16 v[98:101], v[178:181], v[194:197], v[98:101]
	v_mfma_f32_16x16x32_bf16 v[86:89], v[170:173], v[202:205], v[86:89]
	v_mfma_f32_16x16x32_bf16 v[82:85], v[178:181], v[202:205], v[82:85]
	v_mfma_f32_16x16x32_bf16 v[70:73], v[170:173], v[210:213], v[70:73]
	v_mfma_f32_16x16x32_bf16 v[66:69], v[178:181], v[210:213], v[66:69]
	s_setprio 0
	s_barrier
	s_add_i32 s28, s50, s3
	v_lshl_add_u64 v[214:215], s[34:35], 0, v[132:133]
	s_mov_b32 m0, s28
	ds_read_b128 v[182:185], v152 offset:16384
	ds_read_b128 v[186:189], v152 offset:17408
	ds_read_b128 v[190:193], v152 offset:18432
	ds_read_b128 v[194:197], v152 offset:19456
	ds_read_b128 v[198:201], v152 offset:20480
	ds_read_b128 v[202:205], v152 offset:21504
	ds_read_b128 v[206:209], v152 offset:22528
	ds_read_b128 v[210:213], v152 offset:23552
	global_load_lds_dwordx4 v[214:215], off
	s_add_i32 m0, s28, 0x2000
	s_add_u32 s28, s34, 0xe0000
	v_lshl_add_u64 v[216:217], s[34:35], 0, v[134:135]
	s_addc_u32 s29, s35, 0
	s_add_i32 s57, s51, s3
	global_load_lds_dwordx4 v[216:217], off
	v_lshl_add_u64 v[218:219], s[28:29], 0, v[132:133]
	s_mov_b32 m0, s57
	v_lshl_add_u64 v[220:221], s[36:37], 0, v[134:135]
	global_load_lds_dwordx4 v[218:219], off
	v_lshl_add_u64 v[218:219], s[28:29], 0, v[134:135]
	s_add_i32 m0, s57, 0x2000
	s_nop 0
	global_load_lds_dwordx4 v[218:219], off
	v_lshl_add_u64 v[218:219], s[36:37], 0, v[132:133]
	s_mov_b32 m0, s38
	s_nop 0
	global_load_lds_dwordx4 v[218:219], off
	s_mov_b32 m0, s39
	s_nop 0
	global_load_lds_dwordx4 v[220:221], off
	s_waitcnt vmcnt(8)
	s_waitcnt lgkmcnt(0)
	s_barrier
; #define PG8_STAGE_A(b, h, ptr, NX) do { if constexpr (Sched::GATHER) { unsigned gs_[2]; gs_[0] = ((NX) && last_) ? gN[h][0] : gA[h][0]; gs_[1] = ((NX) && last_) ? gN[h][1] : gA[h][1]; PG8_STAGE(PG8_SA(b, h), ptr, gs_); } \
;         else PG8_STAGE(PG8_SA(b, h), (ptr) + ((h) ? hstep : (size_t)0), voffA); } while (0)
; #define PG8_LDA(dst, b, h) do { _Pragma("unroll") for (int m = 0; m < 4; ++m) _Pragma("unroll") for (int k = 0; k < 2; ++k) dst[m][k] = *(const PG8_LAS bf16x8*)(lds + PG8_SA(b, h) + aoff + m * 2048 + k * 1024); } while (0)
; #define PG8_LDB(dst, b, h) do { _Pragma("unroll") for (int n = 0; n < 2; ++n) _Pragma("unroll") for (int k = 0; k < 2; ++k) dst[n][k] = *(const PG8_LAS bf16x8*)(lds + PG8_SB(b, h) + boff + n * 2048 + k * 1024); } while (0)
; #define PG8_MMA(ai, bj, At, Bt) do { __builtin_amdgcn_s_setprio(1); _Pragma("unroll") for (int m = 0; m < 4; ++m) _Pragma("unroll") for (int n = 0; n < 2; ++n) _Pragma("unroll") for (int k = 0; k < 2; ++k) \
;         acc[ai][bj][m][n] = __builtin_amdgcn_mfma_f32_16x16x32_bf16(Bt[n][k], At[m][k], acc[ai][bj][m][n], 0, 0, 0); __builtin_amdgcn_s_setprio(0); } while (0)
; #define PG8_WAIT_V(n) asm volatile("s_waitcnt vmcnt(" #n ")" ::: "memory")
; #define PG8_WAIT_L(n) asm volatile("s_waitcnt lgkmcnt(" #n ")" ::: "memory")
; #define PG8_BAR __builtin_amdgcn_s_barrier()
; #define PG8_SCHED __builtin_amdgcn_sched_barrier(0)
; template <class Epi, class Sched, bool ALIGN_EPI = false, bool SP2 = false>
; __device__ __forceinline__ void gemm_phase(PG8_LAS unsigned char* lds, const Gemm g, const Sched& S, const Epi& E, const bool skip_epi = false) {
;     ...
;             PG8_WAIT_V(8); PG8_WAIT_L(0); PG8_BAR; PG8_MMA(1, 0, At, B0); PG8_MMA(1, 1, At, B1); PG8_BAR; PG8_SCHED;
;             PG8_LDB(B0, 1, 0); PG8_LDB(B1, 1, 1); PG8_SCHED; PG8_LDA(At, 1, 0); PG8_STAGE_A(0, 1, a2, true);
;             PG8_WAIT_V(8); PG8_WAIT_L(0); PG8_BAR; PG8_MMA(0, 0, At, B0); PG8_MMA(0, 1, At, B1); PG8_BAR; PG8_SCHED;
	s_setprio 3
	s_waitcnt lgkmcnt(0)
	v_mfma_f32_16x16x32_bf16 v[62:65], v[142:145], v[182:185], 0
	v_mfma_f32_16x16x32_bf16 v[58:61], v[158:161], v[182:185], 0
	v_mfma_f32_16x16x32_bf16 v[46:49], v[142:145], v[190:193], 0
	v_mfma_f32_16x16x32_bf16 v[42:45], v[158:161], v[190:193], 0
	v_mfma_f32_16x16x32_bf16 v[30:33], v[142:145], v[198:201], 0
	v_mfma_f32_16x16x32_bf16 v[26:29], v[158:161], v[198:201], 0
	v_mfma_f32_16x16x32_bf16 v[14:17], v[142:145], v[206:209], 0
	v_mfma_f32_16x16x32_bf16 v[10:13], v[158:161], v[206:209], 0
	v_mfma_f32_16x16x32_bf16 v[62:65], v[154:157], v[186:189], v[62:65]
	v_mfma_f32_16x16x32_bf16 v[58:61], v[162:165], v[186:189], v[58:61]
	v_mfma_f32_16x16x32_bf16 v[46:49], v[154:157], v[194:197], v[46:49]
	v_mfma_f32_16x16x32_bf16 v[42:45], v[162:165], v[194:197], v[42:45]
	v_mfma_f32_16x16x32_bf16 v[30:33], v[154:157], v[202:205], v[30:33]
	v_mfma_f32_16x16x32_bf16 v[26:29], v[162:165], v[202:205], v[26:29]
	v_mfma_f32_16x16x32_bf16 v[14:17], v[154:157], v[210:213], v[14:17]
	v_mfma_f32_16x16x32_bf16 v[10:13], v[162:165], v[210:213], v[10:13]
	s_setprio 0
	s_setprio 3
	v_mfma_f32_16x16x32_bf16 v[54:57], v[166:169], v[182:185], 0
	v_mfma_f32_16x16x32_bf16 v[50:53], v[174:177], v[182:185], 0
	v_mfma_f32_16x16x32_bf16 v[38:41], v[166:169], v[190:193], 0
	v_mfma_f32_16x16x32_bf16 v[34:37], v[174:177], v[190:193], 0
	v_mfma_f32_16x16x32_bf16 v[22:25], v[166:169], v[198:201], 0
	v_mfma_f32_16x16x32_bf16 v[18:21], v[174:177], v[198:201], 0
	v_mfma_f32_16x16x32_bf16 v[6:9], v[166:169], v[206:209], 0
	v_mfma_f32_16x16x32_bf16 v[2:5], v[174:177], v[206:209], 0
	v_mfma_f32_16x16x32_bf16 v[54:57], v[170:173], v[186:189], v[54:57]
	v_mfma_f32_16x16x32_bf16 v[50:53], v[178:181], v[186:189], v[50:53]
	v_mfma_f32_16x16x32_bf16 v[38:41], v[170:173], v[194:197], v[38:41]
	v_mfma_f32_16x16x32_bf16 v[34:37], v[178:181], v[194:197], v[34:37]
	v_mfma_f32_16x16x32_bf16 v[22:25], v[170:173], v[202:205], v[22:25]
	v_mfma_f32_16x16x32_bf16 v[18:21], v[178:181], v[202:205], v[18:21]
	v_mfma_f32_16x16x32_bf16 v[6:9], v[170:173], v[210:213], v[6:9]
	v_mfma_f32_16x16x32_bf16 v[2:5], v[178:181], v[210:213], v[2:5]
	s_setprio 0
	s_barrier
	s_add_i32 s57, 0, 0x18000
	v_add_u32_e32 v130, s57, v146
	s_add_i32 s58, 0, 0x1c000
	ds_read_b128 v[142:145], v130
	ds_read_b128 v[154:157], v130 offset:1024
	ds_read_b128 v[158:161], v130 offset:2048
	ds_read_b128 v[162:165], v130 offset:3072
	v_add_u32_e32 v130, s58, v146
	ds_read_b128 v[166:169], v130
	ds_read_b128 v[170:173], v130 offset:1024
	ds_read_b128 v[174:177], v130 offset:2048
	ds_read_b128 v[178:181], v130 offset:3072
	s_add_u32 s28, s36, 0xe0000
	s_addc_u32 s29, s37, 0
	s_mov_b32 m0, s40
	v_lshl_add_u64 v[222:223], s[28:29], 0, v[132:133]
	ds_read_b128 v[182:185], v152 offset:32768
	ds_read_b128 v[186:189], v152 offset:33792
	ds_read_b128 v[190:193], v152 offset:34816
	ds_read_b128 v[194:197], v152 offset:35840
	ds_read_b128 v[198:201], v152 offset:36864
	ds_read_b128 v[202:205], v152 offset:37888
	ds_read_b128 v[206:209], v152 offset:38912
	ds_read_b128 v[210:213], v152 offset:39936
	global_load_lds_dwordx4 v[222:223], off
	v_lshl_add_u64 v[222:223], s[28:29], 0, v[134:135]
	s_mov_b32 m0, s41
	s_nop 0
	global_load_lds_dwordx4 v[222:223], off
	s_waitcnt vmcnt(8)
	s_waitcnt lgkmcnt(0)
	s_barrier
	s_setprio 3
	s_waitcnt lgkmcnt(0)
	v_mfma_f32_16x16x32_bf16 v[126:129], v[142:145], v[182:185], v[126:129]
	v_mfma_f32_16x16x32_bf16 v[122:125], v[158:161], v[182:185], v[122:125]
	v_mfma_f32_16x16x32_bf16 v[110:113], v[142:145], v[190:193], v[110:113]
	v_mfma_f32_16x16x32_bf16 v[106:109], v[158:161], v[190:193], v[106:109]
	v_mfma_f32_16x16x32_bf16 v[94:97], v[142:145], v[198:201], v[94:97]
	v_mfma_f32_16x16x32_bf16 v[90:93], v[158:161], v[198:201], v[90:93]
	v_mfma_f32_16x16x32_bf16 v[78:81], v[142:145], v[206:209], v[78:81]
	v_mfma_f32_16x16x32_bf16 v[74:77], v[158:161], v[206:209], v[74:77]
	v_mfma_f32_16x16x32_bf16 v[126:129], v[154:157], v[186:189], v[126:129]
	v_mfma_f32_16x16x32_bf16 v[122:125], v[162:165], v[186:189], v[122:125]
	v_mfma_f32_16x16x32_bf16 v[110:113], v[154:157], v[194:197], v[110:113]
	v_mfma_f32_16x16x32_bf16 v[106:109], v[162:165], v[194:197], v[106:109]
	v_mfma_f32_16x16x32_bf16 v[94:97], v[154:157], v[202:205], v[94:97]
	v_mfma_f32_16x16x32_bf16 v[90:93], v[162:165], v[202:205], v[90:93]
	v_mfma_f32_16x16x32_bf16 v[78:81], v[154:157], v[210:213], v[78:81]
	v_mfma_f32_16x16x32_bf16 v[74:77], v[162:165], v[210:213], v[74:77]
	s_setprio 0
	s_setprio 3
	v_mfma_f32_16x16x32_bf16 v[118:121], v[166:169], v[182:185], v[118:121]
	v_mfma_f32_16x16x32_bf16 v[114:117], v[174:177], v[182:185], v[114:117]
	v_mfma_f32_16x16x32_bf16 v[102:105], v[166:169], v[190:193], v[102:105]
	v_mfma_f32_16x16x32_bf16 v[98:101], v[174:177], v[190:193], v[98:101]
	v_mfma_f32_16x16x32_bf16 v[86:89], v[166:169], v[198:201], v[86:89]
	v_mfma_f32_16x16x32_bf16 v[82:85], v[174:177], v[198:201], v[82:85]
	v_mfma_f32_16x16x32_bf16 v[70:73], v[166:169], v[206:209], v[70:73]
	v_mfma_f32_16x16x32_bf16 v[66:69], v[174:177], v[206:209], v[66:69]
	v_mfma_f32_16x16x32_bf16 v[118:121], v[170:173], v[186:189], v[118:121]
	v_mfma_f32_16x16x32_bf16 v[114:117], v[178:181], v[186:189], v[114:117]
	v_mfma_f32_16x16x32_bf16 v[102:105], v[170:173], v[194:197], v[102:105]
	v_mfma_f32_16x16x32_bf16 v[98:101], v[178:181], v[194:197], v[98:101]
	v_mfma_f32_16x16x32_bf16 v[86:89], v[170:173], v[202:205], v[86:89]
	v_mfma_f32_16x16x32_bf16 v[82:85], v[178:181], v[202:205], v[82:85]
	v_mfma_f32_16x16x32_bf16 v[70:73], v[170:173], v[210:213], v[70:73]
	v_mfma_f32_16x16x32_bf16 v[66:69], v[178:181], v[210:213], v[66:69]
	s_setprio 0
	s_barrier
; #define PG8_STAGE_A(b, h, ptr, NX) do { if constexpr (Sched::GATHER) { unsigned gs_[2]; gs_[0] = ((NX) && last_) ? gN[h][0] : gA[h][0]; gs_[1] = ((NX) && last_) ? gN[h][1] : gA[h][1]; PG8_STAGE(PG8_SA(b, h), ptr, gs_); } \
;         else PG8_STAGE(PG8_SA(b, h), (ptr) + ((h) ? hstep : (size_t)0), voffA); } while (0)
; #define PG8_STAGE(bufoff, gbase, voff) do { _Pragma("unroll") for (int _i = 0; _i < 2; ++_i) \
;         __builtin_amdgcn_global_load_lds((const unsigned*)((const char*)(gbase) + (voff)[_i]), (PG8_LAS unsigned*)(lds + (bufoff) + ldsw + _i * 8192), 16, 0, 0); } while (0)
; #define PG8_WAIT_V(n) asm volatile("s_waitcnt vmcnt(" #n ")" ::: "memory")
; #define PG8_BAR __builtin_amdgcn_s_barrier()
; template <class Epi, class Sched, bool ALIGN_EPI = false, bool SP2 = false>
; __device__ __forceinline__ void gemm_phase(PG8_LAS unsigned char* lds, const Gemm g, const Sched& S, const Epi& E, const bool skip_epi = false) {
;     ...
;         for (int t = 0; t < nt; t += 2) {
;             const bool last = (t == nt - 2); last_ = last && has_next;
;             const char* a1 = cA + (size_t)(t + 1) * kstep;
;             const char* a2 = last ? nA : cA + (size_t)(t + 2) * kstep; const char* b2 = last ? nB : cB + (size_t)(t + 2) * kstep;
;             const char* a3 = a2 + kstep; const char* b3 = b2 + kstep;
;             if (last && has_next) S.a_ready(nxt);
;             if constexpr (SP2) {
;             PG8_LDB(B0, 0, 0); PG8_LDB(B1, 0, 1); PG8_SCHED; PG8_LDA(At, 0, 0); PG8_STAGE_A(1, 1, a1, false);
;             PG8_WAIT_V(8); PG8_WAIT_L(0); PG8_BAR; PG8_MMA(0, 0, At, B0); PG8_MMA(0, 1, At, B1); PG8_BAR; PG8_SCHED;
;             PG8_LDA(At, 0, 1); PG8_STAGE(PG8_SB(0, 0), b2, voffB); PG8_STAGE(PG8_SB(0, 1), b2 + hstep, voffB); PG8_STAGE_A(0, 0, a2, true);
;             PG8_WAIT_V(8); PG8_WAIT_L(0); PG8_BAR; PG8_MMA(1, 0, At, B0); PG8_MMA(1, 1, At, B1); PG8_BAR; PG8_SCHED;
;             PG8_LDB(B0, 1, 0); PG8_LDB(B1, 1, 1); PG8_SCHED; PG8_LDA(At, 1, 0); PG8_STAGE_A(0, 1, a2, true);
;             PG8_WAIT_V(8); PG8_WAIT_L(0); PG8_BAR; PG8_MMA(0, 0, At, B0); PG8_MMA(0, 1, At, B1); PG8_BAR; PG8_SCHED;
;             PG8_LDA(At, 1, 1); PG8_STAGE(PG8_SB(1, 0), b3, voffB); PG8_STAGE(PG8_SB(1, 1), b3 + hstep, voffB); PG8_STAGE_A(1, 0, a3, true);
;             PG8_WAIT_V(8); PG8_WAIT_L(0); PG8_BAR; PG8_MMA(1, 0, At, B0); PG8_MMA(1, 1, At, B1); PG8_BAR; PG8_SCHED;
	s_add_i32 s28, s57, s3
	v_lshl_add_u64 v[214:215], v[214:215], 0, s[18:19]
	s_mov_b32 m0, s28
	ds_read_b128 v[182:185], v152 offset:49152
	ds_read_b128 v[186:189], v152 offset:50176
	ds_read_b128 v[190:193], v152 offset:51200
	ds_read_b128 v[194:197], v152 offset:52224
	ds_read_b128 v[198:201], v152 offset:53248
	ds_read_b128 v[202:205], v152 offset:54272
	ds_read_b128 v[206:209], v152 offset:55296
	ds_read_b128 v[210:213], v152 offset:56320
	global_load_lds_dwordx4 v[214:215], off
	s_add_i32 m0, s28, 0x2000
	s_add_u32 s28, s34, 0xe0080
	v_lshl_add_u64 v[214:215], v[216:217], 0, s[18:19]
	s_addc_u32 s29, s35, 0
	s_add_i32 s34, s58, s3
	global_load_lds_dwordx4 v[214:215], off
	v_lshl_add_u64 v[214:215], s[28:29], 0, v[132:133]
	s_mov_b32 m0, s34
	s_nop 0
	global_load_lds_dwordx4 v[214:215], off
	v_lshl_add_u64 v[214:215], s[28:29], 0, v[134:135]
	s_add_i32 m0, s34, 0x2000
	s_nop 0
	global_load_lds_dwordx4 v[214:215], off
	v_lshl_add_u64 v[214:215], v[218:219], 0, s[18:19]
	s_mov_b32 m0, s46
	s_nop 0
	global_load_lds_dwordx4 v[214:215], off
	v_lshl_add_u64 v[214:215], v[220:221], 0, s[18:19]
	s_mov_b32 m0, s47
	s_nop 0
	global_load_lds_dwordx4 v[214:215], off
	s_waitcnt vmcnt(8)
	s_waitcnt lgkmcnt(0)
	s_barrier
	s_setprio 3
	s_waitcnt lgkmcnt(0)
	v_mfma_f32_16x16x32_bf16 v[62:65], v[142:145], v[182:185], v[62:65]
	v_mfma_f32_16x16x32_bf16 v[58:61], v[158:161], v[182:185], v[58:61]
	v_mfma_f32_16x16x32_bf16 v[46:49], v[142:145], v[190:193], v[46:49]
	v_mfma_f32_16x16x32_bf16 v[42:45], v[158:161], v[190:193], v[42:45]
	v_mfma_f32_16x16x32_bf16 v[30:33], v[142:145], v[198:201], v[30:33]
	v_mfma_f32_16x16x32_bf16 v[26:29], v[158:161], v[198:201], v[26:29]
	v_mfma_f32_16x16x32_bf16 v[14:17], v[142:145], v[206:209], v[14:17]
	v_mfma_f32_16x16x32_bf16 v[10:13], v[158:161], v[206:209], v[10:13]
	v_mfma_f32_16x16x32_bf16 v[62:65], v[154:157], v[186:189], v[62:65]
	v_mfma_f32_16x16x32_bf16 v[58:61], v[162:165], v[186:189], v[58:61]
	v_mfma_f32_16x16x32_bf16 v[46:49], v[154:157], v[194:197], v[46:49]
	v_mfma_f32_16x16x32_bf16 v[42:45], v[162:165], v[194:197], v[42:45]
	v_mfma_f32_16x16x32_bf16 v[30:33], v[154:157], v[202:205], v[30:33]
	v_mfma_f32_16x16x32_bf16 v[26:29], v[162:165], v[202:205], v[26:29]
	v_mfma_f32_16x16x32_bf16 v[14:17], v[154:157], v[210:213], v[14:17]
	v_mfma_f32_16x16x32_bf16 v[10:13], v[162:165], v[210:213], v[10:13]
	s_setprio 0
	s_setprio 3
	v_mfma_f32_16x16x32_bf16 v[54:57], v[166:169], v[182:185], v[54:57]
	v_mfma_f32_16x16x32_bf16 v[50:53], v[174:177], v[182:185], v[50:53]
	v_mfma_f32_16x16x32_bf16 v[38:41], v[166:169], v[190:193], v[38:41]
	v_mfma_f32_16x16x32_bf16 v[34:37], v[174:177], v[190:193], v[34:37]
	v_mfma_f32_16x16x32_bf16 v[22:25], v[166:169], v[198:201], v[22:25]
	v_mfma_f32_16x16x32_bf16 v[18:21], v[174:177], v[198:201], v[18:21]
	v_mfma_f32_16x16x32_bf16 v[6:9], v[166:169], v[206:209], v[6:9]
	v_mfma_f32_16x16x32_bf16 v[2:5], v[174:177], v[206:209], v[2:5]
	v_mfma_f32_16x16x32_bf16 v[54:57], v[170:173], v[186:189], v[54:57]
	v_mfma_f32_16x16x32_bf16 v[50:53], v[178:181], v[186:189], v[50:53]
	v_mfma_f32_16x16x32_bf16 v[38:41], v[170:173], v[194:197], v[38:41]
	v_mfma_f32_16x16x32_bf16 v[34:37], v[178:181], v[194:197], v[34:37]
	v_mfma_f32_16x16x32_bf16 v[22:25], v[170:173], v[202:205], v[22:25]
	v_mfma_f32_16x16x32_bf16 v[18:21], v[178:181], v[202:205], v[18:21]
	v_mfma_f32_16x16x32_bf16 v[6:9], v[170:173], v[210:213], v[6:9]
	v_mfma_f32_16x16x32_bf16 v[2:5], v[178:181], v[210:213], v[2:5]
	s_setprio 0
	s_barrier
	s_add_i32 s56, s56, 2
	s_add_u32 s54, s54, 0x100
	s_addc_u32 s55, s55, 0
	s_cmp_gt_u32 s56, 11
	s_mov_b64 s[28:29], s[30:31]
	.p2align	3
